# combo3: scan counted vmcnt waits; window attn 2-deep tile prefetch (round loop unrolled x2, 2nd reg set); SWA all 3 tiles prefetched up front; barrier skip; XGEN before acquire; FFN act nt sc1
# speedup vs baseline: 1.0020x; 1.0020x over previous
; __device__ __forceinline__ unsigned pk2(float lo, float hi) { const f32x2 f = {lo, hi}; const bf16n2 v = __builtin_convertvector(f, bf16n2); return __builtin_bit_cast(unsigned, v); }
; #define RW_LOAD_SET(SET, UNIT) do { const bf16_t* ug_ = rwu + (size_t)(UNIT) * 16384; \
;     _Pragma("unroll") for (int ta = 0; ta < 4; ++ta) { An[SET][ta][0] = *(const bf16x8*)(ug_ + ((ta * 2) * 64 + lane) * 8); An[SET][ta][1] = *(const bf16x8*)(ug_ + ((ta * 2 + 1) * 64 + lane) * 8); \
;         Zn[SET][ta] = *(const u32x2*)(ug_ + 4096 + ((cq * 4 + ta) * 64 + lane) * 4); } } while (0)
; template <int SM>
; __device__ __forceinline__ void phase_rwkv_scan(const Ctx& c, const bf16_t* rwu, bf16_t* rws) {
;     ...
;     for (int ch = 0; ch < T / 64; ch += 32) {
; #pragma unroll
;         for (int uu = 0; uu < 32; ++uu) {
;             const int u = uu % RW_SETS;
;             const int unit = (ch + uu) * 8 + h;
;             bf16_t* sg = rws + (size_t)unit * 4096 + cq * 1024 + lane * 8;
;             *(bf16x8*)(sg) = Bhi[0]; *(bf16x8*)(sg + 512) = Bhi[1];
;             f32x4 acc[4];
; #pragma unroll
;             for (int ta = 0; ta < 4; ++ta) { const u32x2 z = Zn[u][ta];
;                 acc[ta] = (f32x4){__uint_as_float(z.x << 16), __uint_as_float(z.x & 0xffff0000u), __uint_as_float(z.y << 16), __uint_as_float(z.y & 0xffff0000u)};
; #pragma unroll
;                 for (int s = 0; s < 2; ++s) acc[ta] = __builtin_amdgcn_mfma_f32_16x16x32_bf16(An[u][ta][s], Bhi[s], acc[ta], 0, 0, 0); }
;             if (SM == 0) RW_LOAD_SET(u, (ch + uu + RW_SETS < T / 64) ? unit + 8 * RW_SETS : unit);
; #pragma unroll
;             for (int s = 0; s < 2; ++s) { u32x4 hi;
;                 hi.x = pk2(acc[2 * s][0], acc[2 * s][1]); hi.y = pk2(acc[2 * s][2], acc[2 * s][3]); hi.z = pk2(acc[2 * s + 1][0], acc[2 * s + 1][1]); hi.w = pk2(acc[2 * s + 1][2], acc[2 * s + 1][3]);
;                 Bhi[s] = __builtin_bit_cast(bf16x8, hi); }
;         }
.LBB0_981:
	s_ashr_i32 s3, s2, 31
	s_lshl_b64 s[2:3], s[2:3], 15
	s_add_u32 s4, s40, s2
	s_addc_u32 s5, s41, s3
	s_add_u32 s6, s4, 0x2000
	s_addc_u32 s7, s5, 0
	v_lshl_add_u64 v[74:75], v[182:183], 0, s[2:3]
	global_load_dwordx2 v[224:225], v0, s[6:7]
	global_load_dwordx2 v[222:223], v179, s[6:7]
	global_load_dwordx2 v[220:221], v191, s[6:7]
	global_load_dwordx2 v[218:219], v195, s[6:7]
	global_load_dwordx4 v[154:157], v[74:75], off
	global_load_dwordx4 v[158:161], v245, s[4:5]
	global_load_dwordx4 v[146:149], v246, s[4:5]
	global_load_dwordx4 v[150:153], v247, s[4:5]
	v_lshl_add_u64 v[74:75], v[184:185], 0, s[2:3]
	global_load_dwordx4 v[106:109], v[74:75], off
	v_lshl_add_u64 v[74:75], v[196:197], 0, s[2:3]
	global_load_dwordx4 v[110:113], v[74:75], off
	v_lshl_add_u64 v[74:75], v[198:199], 0, s[2:3]
	global_load_dwordx4 v[98:101], v[74:75], off
	v_lshl_add_u64 v[74:75], v[200:201], 0, s[2:3]
	global_load_dwordx4 v[102:105], v[74:75], off
	s_lshl_b32 s2, s1, 3
	s_add_i32 s2, s2, s0
	s_ashr_i32 s3, s2, 31
	s_lshl_b64 s[4:5], s[2:3], 13
	v_lshl_add_u64 v[74:75], v[180:181], 0, s[4:5]
	global_store_dwordx4 v[74:75], v[70:73], off
	global_store_dwordx4 v[74:75], v[66:69], off offset:1024
	s_waitcnt vmcnt(36)
	v_lshlrev_b32_e32 v74, 16, v202
	v_and_b32_e32 v75, 0xffff0000, v202
	v_lshlrev_b32_e32 v76, 16, v203
	v_and_b32_e32 v77, 0xffff0000, v203
	s_add_i32 s6, s2, 32
	s_ashr_i32 s7, s6, 31
	v_mfma_f32_16x16x32_bf16 v[2:5], v[2:5], v[70:73], v[74:77]
	s_lshl_b64 s[4:5], s[6:7], 15
	s_add_u32 s4, s40, s4
	s_addc_u32 s5, s41, s5
	v_mfma_f32_16x16x32_bf16 v[2:5], v[6:9], v[66:69], v[2:5]
	v_lshlrev_b32_e32 v6, 16, v204
	v_and_b32_e32 v7, 0xffff0000, v204
	v_lshlrev_b32_e32 v8, 16, v205
	v_and_b32_e32 v9, 0xffff0000, v205
	s_add_u32 s8, s4, 0x2000
	s_addc_u32 s9, s5, 0
	v_mfma_f32_16x16x32_bf16 v[6:9], v[10:13], v[70:73], v[6:9]
	v_lshlrev_b32_e32 v10, 16, v206
	v_and_b32_e32 v11, 0xffff0000, v206
	v_lshlrev_b32_e32 v12, 16, v207
	v_and_b32_e32 v13, 0xffff0000, v207
	v_mfma_f32_16x16x32_bf16 v[6:9], v[18:21], v[66:69], v[6:9]
	v_cvt_pk_bf16_f32 v2, v2, v3
	v_cvt_pk_bf16_f32 v3, v4, v5
	v_mfma_f32_16x16x32_bf16 v[10:13], v[14:17], v[70:73], v[10:13]
	v_lshlrev_b32_e32 v14, 16, v208
	v_and_b32_e32 v15, 0xffff0000, v208
	v_lshlrev_b32_e32 v16, 16, v209
	v_and_b32_e32 v17, 0xffff0000, v209
	v_mfma_f32_16x16x32_bf16 v[10:13], v[22:25], v[66:69], v[10:13]
	v_cvt_pk_bf16_f32 v4, v6, v7
	v_cvt_pk_bf16_f32 v5, v8, v9
	v_mfma_f32_16x16x32_bf16 v[14:17], v[26:29], v[70:73], v[14:17]
	v_mfma_f32_16x16x32_bf16 v[14:17], v[30:33], v[66:69], v[14:17]
	global_load_dwordx4 v[90:93], v248, s[4:5]
	global_load_dwordx4 v[94:97], v248, s[4:5] offset:1024
	global_load_dwordx2 v[176:177], v0, s[8:9]
	global_load_dwordx4 v[82:85], v248, s[4:5] offset:2048
	global_load_dwordx4 v[86:89], v248, s[4:5] offset:3072
	global_load_dwordx2 v[174:175], v179, s[8:9]
	global_load_dwordx4 v[74:77], v249, s[4:5]
	global_load_dwordx4 v[78:81], v250, s[4:5]
	global_load_dwordx2 v[172:173], v191, s[8:9]
	global_load_dwordx4 v[66:69], v189, s[4:5]
	global_load_dwordx4 v[70:73], v187, s[4:5]
	global_load_dwordx2 v[170:171], v195, s[8:9]
	s_add_i32 s8, s2, 8
	s_ashr_i32 s9, s8, 31
	s_lshl_b64 s[10:11], s[8:9], 13
	v_cvt_pk_bf16_f32 v6, v10, v11
	v_lshl_add_u64 v[10:11], v[180:181], 0, s[10:11]
	v_cvt_pk_bf16_f32 v7, v12, v13
	v_cvt_pk_bf16_f32 v8, v14, v15
	v_cvt_pk_bf16_f32 v9, v16, v17
	global_store_dwordx4 v[10:11], v[2:5], off
	global_store_dwordx4 v[10:11], v[6:9], off offset:1024
	s_waitcnt vmcnt(36)
	v_lshlrev_b32_e32 v10, 16, v216
	v_and_b32_e32 v11, 0xffff0000, v216
	v_lshlrev_b32_e32 v12, 16, v217
	v_and_b32_e32 v13, 0xffff0000, v217
	s_lshl_b64 s[8:9], s[8:9], 15
	s_add_u32 s3, s40, s8
	v_mfma_f32_16x16x32_bf16 v[10:13], v[58:61], v[2:5], v[10:13]
	s_addc_u32 s11, s41, s9
	s_add_u32 s8, s3, 0x100000
	s_addc_u32 s9, s11, 0
	v_mfma_f32_16x16x32_bf16 v[58:61], v[62:65], v[6:9], v[10:13]
	s_add_u32 s10, s3, 0x102000
	s_addc_u32 s11, s11, 0
	s_nop 1
	v_lshlrev_b32_e32 v10, 16, v214
	v_and_b32_e32 v11, 0xffff0000, v214
	v_lshlrev_b32_e32 v12, 16, v215
	v_and_b32_e32 v13, 0xffff0000, v215
	s_nop 1
	v_mfma_f32_16x16x32_bf16 v[10:13], v[50:53], v[2:5], v[10:13]
	v_mfma_f32_16x16x32_bf16 v[50:53], v[54:57], v[6:9], v[10:13]
	s_nop 6
	v_lshlrev_b32_e32 v10, 16, v212
	v_and_b32_e32 v11, 0xffff0000, v212
	v_lshlrev_b32_e32 v12, 16, v213
	v_and_b32_e32 v13, 0xffff0000, v213
	s_nop 1
	v_mfma_f32_16x16x32_bf16 v[10:13], v[38:41], v[2:5], v[10:13]
	v_cvt_pk_bf16_f32 v38, v58, v59
	v_cvt_pk_bf16_f32 v39, v60, v61
	v_cvt_pk_bf16_f32 v40, v50, v51
	v_mfma_f32_16x16x32_bf16 v[46:49], v[46:49], v[6:9], v[10:13]
	v_cvt_pk_bf16_f32 v41, v52, v53
	s_nop 2
	v_lshlrev_b32_e32 v10, 16, v210
	v_and_b32_e32 v11, 0xffff0000, v210
	v_lshlrev_b32_e32 v12, 16, v211
	v_and_b32_e32 v13, 0xffff0000, v211
	s_nop 1
	v_mfma_f32_16x16x32_bf16 v[2:5], v[34:37], v[2:5], v[10:13]
	v_cvt_pk_bf16_f32 v34, v46, v47
	v_cvt_pk_bf16_f32 v35, v48, v49
	v_mfma_f32_16x16x32_bf16 v[42:45], v[42:45], v[6:9], v[2:5]
	global_load_dwordx4 v[26:29], v248, s[8:9]
	global_load_dwordx4 v[30:33], v248, s[8:9] offset:1024
	global_load_dwordx2 v[168:169], v0, s[10:11]
	global_load_dwordx4 v[18:21], v248, s[8:9] offset:2048
	global_load_dwordx4 v[22:25], v248, s[8:9] offset:3072
	global_load_dwordx2 v[166:167], v179, s[10:11]
	global_load_dwordx4 v[10:13], v249, s[8:9]
	global_load_dwordx4 v[14:17], v250, s[8:9]
	global_load_dwordx2 v[164:165], v191, s[10:11]
	global_load_dwordx4 v[2:5], v189, s[8:9]
	global_load_dwordx4 v[6:9], v187, s[8:9]
	global_load_dwordx2 v[162:163], v195, s[10:11]
	s_add_i32 s8, s2, 16
	s_ashr_i32 s9, s8, 31
	s_lshl_b64 s[10:11], s[8:9], 13
	v_cvt_pk_bf16_f32 v36, v42, v43
	v_lshl_add_u64 v[42:43], v[180:181], 0, s[10:11]
	v_cvt_pk_bf16_f32 v37, v44, v45
	global_store_dwordx4 v[42:43], v[38:41], off
	global_store_dwordx4 v[42:43], v[34:37], off offset:1024
	s_waitcnt vmcnt(36)
; __device__ __forceinline__ unsigned pk2(float lo, float hi) { const f32x2 f = {lo, hi}; const bf16n2 v = __builtin_convertvector(f, bf16n2); return __builtin_bit_cast(unsigned, v); }
; #define RW_LOAD_SET(SET, UNIT) do { const bf16_t* ug_ = rwu + (size_t)(UNIT) * 16384; \
;     _Pragma("unroll") for (int ta = 0; ta < 4; ++ta) { An[SET][ta][0] = *(const bf16x8*)(ug_ + ((ta * 2) * 64 + lane) * 8); An[SET][ta][1] = *(const bf16x8*)(ug_ + ((ta * 2 + 1) * 64 + lane) * 8); \
;         Zn[SET][ta] = *(const u32x2*)(ug_ + 4096 + ((cq * 4 + ta) * 64 + lane) * 4); } } while (0)
; template <int SM>
; __device__ __forceinline__ void phase_rwkv_scan(const Ctx& c, const bf16_t* rwu, bf16_t* rws) {
;     ...
;     for (int ch = 0; ch < T / 64; ch += 32) {
; #pragma unroll
;         for (int uu = 0; uu < 32; ++uu) {
;             const int u = uu % RW_SETS;
;             const int unit = (ch + uu) * 8 + h;
;             bf16_t* sg = rws + (size_t)unit * 4096 + cq * 1024 + lane * 8;
;             *(bf16x8*)(sg) = Bhi[0]; *(bf16x8*)(sg + 512) = Bhi[1];
;             f32x4 acc[4];
; #pragma unroll
;             for (int ta = 0; ta < 4; ++ta) { const u32x2 z = Zn[u][ta];
;                 acc[ta] = (f32x4){__uint_as_float(z.x << 16), __uint_as_float(z.x & 0xffff0000u), __uint_as_float(z.y << 16), __uint_as_float(z.y & 0xffff0000u)};
; #pragma unroll
;                 for (int s = 0; s < 2; ++s) acc[ta] = __builtin_amdgcn_mfma_f32_16x16x32_bf16(An[u][ta][s], Bhi[s], acc[ta], 0, 0, 0); }
;             if (SM == 0) RW_LOAD_SET(u, (ch + uu + RW_SETS < T / 64) ? unit + 8 * RW_SETS : unit);
; #pragma unroll
;             for (int s = 0; s < 2; ++s) { u32x4 hi;
;                 hi.x = pk2(acc[2 * s][0], acc[2 * s][1]); hi.y = pk2(acc[2 * s][2], acc[2 * s][3]); hi.z = pk2(acc[2 * s + 1][0], acc[2 * s + 1][1]); hi.w = pk2(acc[2 * s + 1][2], acc[2 * s + 1][3]);
;                 Bhi[s] = __builtin_bit_cast(bf16x8, hi); }
;         }
	v_lshlrev_b32_e32 v42, 16, v230
	v_and_b32_e32 v43, 0xffff0000, v230
	v_lshlrev_b32_e32 v44, 16, v231
	v_and_b32_e32 v45, 0xffff0000, v231
	s_lshl_b64 s[8:9], s[8:9], 15
	s_add_u32 s3, s40, s8
	v_mfma_f32_16x16x32_bf16 v[42:45], v[134:137], v[38:41], v[42:45]
	s_addc_u32 s11, s41, s9
	s_add_u32 s8, s3, 0x100000
	s_addc_u32 s9, s11, 0
	v_mfma_f32_16x16x32_bf16 v[134:137], v[142:145], v[34:37], v[42:45]
	s_add_u32 s10, s3, 0x102000
	s_addc_u32 s11, s11, 0
	s_nop 1
	v_lshlrev_b32_e32 v42, 16, v232
	v_and_b32_e32 v43, 0xffff0000, v232
	v_lshlrev_b32_e32 v44, 16, v233
	v_and_b32_e32 v45, 0xffff0000, v233
	s_nop 1
	v_mfma_f32_16x16x32_bf16 v[42:45], v[130:133], v[38:41], v[42:45]
	v_mfma_f32_16x16x32_bf16 v[130:133], v[138:141], v[34:37], v[42:45]
	s_nop 6
	v_lshlrev_b32_e32 v42, 16, v226
	v_and_b32_e32 v43, 0xffff0000, v226
	v_lshlrev_b32_e32 v44, 16, v227
	v_and_b32_e32 v45, 0xffff0000, v227
	s_nop 1
	v_mfma_f32_16x16x32_bf16 v[42:45], v[122:125], v[38:41], v[42:45]
	v_mfma_f32_16x16x32_bf16 v[122:125], v[126:129], v[34:37], v[42:45]
	s_waitcnt vmcnt(34)
	v_lshlrev_b32_e32 v126, 16, v222
	v_and_b32_e32 v127, 0xffff0000, v222
	v_lshlrev_b32_e32 v128, 16, v223
	s_nop 3
	v_lshlrev_b32_e32 v42, 16, v228
	v_and_b32_e32 v43, 0xffff0000, v228
	v_lshlrev_b32_e32 v44, 16, v229
	v_and_b32_e32 v45, 0xffff0000, v229
	v_cvt_pk_bf16_f32 v122, v122, v123
	v_cvt_pk_bf16_f32 v123, v124, v125
	v_mfma_f32_16x16x32_bf16 v[38:41], v[118:121], v[38:41], v[42:45]
	v_cvt_pk_bf16_f32 v118, v134, v135
	v_cvt_pk_bf16_f32 v119, v136, v137
	v_cvt_pk_bf16_f32 v120, v130, v131
	v_mfma_f32_16x16x32_bf16 v[114:117], v[114:117], v[34:37], v[38:41]
	global_load_dwordx4 v[58:61], v248, s[8:9]
	global_load_dwordx4 v[62:65], v248, s[8:9] offset:1024
	global_load_dwordx2 v[208:209], v0, s[10:11]
	global_load_dwordx4 v[50:53], v248, s[8:9] offset:2048
	global_load_dwordx4 v[54:57], v248, s[8:9] offset:3072
	global_load_dwordx2 v[206:207], v179, s[10:11]
	global_load_dwordx4 v[42:45], v249, s[8:9]
	global_load_dwordx4 v[46:49], v250, s[8:9]
	global_load_dwordx2 v[204:205], v191, s[10:11]
	global_load_dwordx4 v[34:37], v189, s[8:9]
	global_load_dwordx4 v[38:41], v187, s[8:9]
	global_load_dwordx2 v[202:203], v195, s[10:11]
	v_cvt_pk_bf16_f32 v121, v132, v133
	s_waitcnt vmcnt(36)
	v_lshlrev_b32_e32 v130, 16, v220
	v_and_b32_e32 v131, 0xffff0000, v220
	v_lshlrev_b32_e32 v132, 16, v221
	v_and_b32_e32 v133, 0xffff0000, v221
	s_add_i32 s8, s2, 24
	s_ashr_i32 s9, s8, 31
	v_mfma_f32_16x16x32_bf16 v[106:109], v[106:109], v[118:121], v[130:133]
	s_lshl_b64 s[10:11], s[8:9], 13
	v_cvt_pk_bf16_f32 v124, v114, v115
	v_cvt_pk_bf16_f32 v125, v116, v117
	v_lshl_add_u64 v[114:115], v[180:181], 0, s[10:11]
	global_store_dwordx4 v[114:115], v[118:121], off
	global_store_dwordx4 v[114:115], v[122:125], off offset:1024
	v_lshlrev_b32_e32 v114, 16, v224
	v_and_b32_e32 v115, 0xffff0000, v224
	v_lshlrev_b32_e32 v116, 16, v225
	v_and_b32_e32 v117, 0xffff0000, v225
	v_and_b32_e32 v129, 0xffff0000, v223
	v_mfma_f32_16x16x32_bf16 v[106:109], v[110:113], v[122:125], v[106:109]
	v_lshlrev_b32_e32 v110, 16, v218
	v_and_b32_e32 v111, 0xffff0000, v218
	v_lshlrev_b32_e32 v112, 16, v219
	v_and_b32_e32 v113, 0xffff0000, v219
	v_mfma_f32_16x16x32_bf16 v[114:117], v[154:157], v[118:121], v[114:117]
	s_lshl_b64 s[8:9], s[8:9], 15
	s_add_u32 s3, s40, s8
	s_addc_u32 s11, s41, s9
	v_mfma_f32_16x16x32_bf16 v[126:129], v[146:149], v[118:121], v[126:129]
	s_add_u32 s8, s3, 0x100000
	s_addc_u32 s9, s11, 0
	s_add_u32 s10, s3, 0x102000
	v_mfma_f32_16x16x32_bf16 v[98:101], v[98:101], v[118:121], v[110:113]
	s_addc_u32 s11, s11, 0
	s_lshl_b64 s[6:7], s[6:7], 13
	v_cvt_pk_bf16_f32 v106, v106, v107
	v_mfma_f32_16x16x32_bf16 v[114:117], v[158:161], v[122:125], v[114:117]
	v_cvt_pk_bf16_f32 v107, v108, v109
	v_mfma_f32_16x16x32_bf16 v[126:129], v[150:153], v[122:125], v[126:129]
	global_load_dwordx4 v[130:133], v248, s[8:9]
	global_load_dwordx4 v[134:137], v248, s[8:9] offset:1024
	global_load_dwordx2 v[214:215], v0, s[10:11]
	global_load_dwordx4 v[138:141], v248, s[8:9] offset:2048
	global_load_dwordx4 v[142:145], v248, s[8:9] offset:3072
	global_load_dwordx2 v[216:217], v179, s[10:11]
	global_load_dwordx4 v[146:149], v249, s[8:9]
	global_load_dwordx4 v[150:153], v250, s[8:9]
	global_load_dwordx2 v[218:219], v191, s[10:11]
	global_load_dwordx4 v[154:157], v189, s[8:9]
	global_load_dwordx4 v[158:161], v187, s[8:9]
	global_load_dwordx2 v[220:221], v195, s[10:11]
	v_mfma_f32_16x16x32_bf16 v[98:101], v[102:105], v[122:125], v[98:101]
	v_cvt_pk_bf16_f32 v102, v114, v115
	v_cvt_pk_bf16_f32 v103, v116, v117
	v_cvt_pk_bf16_f32 v104, v126, v127
	v_cvt_pk_bf16_f32 v105, v128, v129
	s_nop 3
	v_cvt_pk_bf16_f32 v108, v98, v99
	v_lshl_add_u64 v[98:99], v[180:181], 0, s[6:7]
	v_cvt_pk_bf16_f32 v109, v100, v101
	global_store_dwordx4 v[98:99], v[102:105], off
	global_store_dwordx4 v[98:99], v[106:109], off offset:1024
	s_waitcnt vmcnt(36)
; __device__ __forceinline__ unsigned pk2(float lo, float hi) { const f32x2 f = {lo, hi}; const bf16n2 v = __builtin_convertvector(f, bf16n2); return __builtin_bit_cast(unsigned, v); }
; #define RW_LOAD_SET(SET, UNIT) do { const bf16_t* ug_ = rwu + (size_t)(UNIT) * 16384; \
;     _Pragma("unroll") for (int ta = 0; ta < 4; ++ta) { An[SET][ta][0] = *(const bf16x8*)(ug_ + ((ta * 2) * 64 + lane) * 8); An[SET][ta][1] = *(const bf16x8*)(ug_ + ((ta * 2 + 1) * 64 + lane) * 8); \
;         Zn[SET][ta] = *(const u32x2*)(ug_ + 4096 + ((cq * 4 + ta) * 64 + lane) * 4); } } while (0)
; template <int SM>
; __device__ __forceinline__ void phase_rwkv_scan(const Ctx& c, const bf16_t* rwu, bf16_t* rws) {
;     ...
;     for (int ch = 0; ch < T / 64; ch += 32) {
; #pragma unroll
;         for (int uu = 0; uu < 32; ++uu) {
;             const int u = uu % RW_SETS;
;             const int unit = (ch + uu) * 8 + h;
;             bf16_t* sg = rws + (size_t)unit * 4096 + cq * 1024 + lane * 8;
;             *(bf16x8*)(sg) = Bhi[0]; *(bf16x8*)(sg + 512) = Bhi[1];
;             f32x4 acc[4];
; #pragma unroll
;             for (int ta = 0; ta < 4; ++ta) { const u32x2 z = Zn[u][ta];
;                 acc[ta] = (f32x4){__uint_as_float(z.x << 16), __uint_as_float(z.x & 0xffff0000u), __uint_as_float(z.y << 16), __uint_as_float(z.y & 0xffff0000u)};
; #pragma unroll
;                 for (int s = 0; s < 2; ++s) acc[ta] = __builtin_amdgcn_mfma_f32_16x16x32_bf16(An[u][ta][s], Bhi[s], acc[ta], 0, 0, 0); }
;             if (SM == 0) RW_LOAD_SET(u, (ch + uu + RW_SETS < T / 64) ? unit + 8 * RW_SETS : unit);
; #pragma unroll
;             for (int s = 0; s < 2; ++s) { u32x4 hi;
;                 hi.x = pk2(acc[2 * s][0], acc[2 * s][1]); hi.y = pk2(acc[2 * s][2], acc[2 * s][3]); hi.z = pk2(acc[2 * s + 1][0], acc[2 * s + 1][1]); hi.w = pk2(acc[2 * s + 1][2], acc[2 * s + 1][3]);
;                 Bhi[s] = __builtin_bit_cast(bf16x8, hi); }
;         }
	v_lshlrev_b32_e32 v98, 16, v176
	v_and_b32_e32 v99, 0xffff0000, v176
	v_lshlrev_b32_e32 v100, 16, v177
	v_and_b32_e32 v101, 0xffff0000, v177
	s_add_u32 s6, s4, 0x100000
	s_addc_u32 s7, s5, 0
	v_mfma_f32_16x16x32_bf16 v[90:93], v[90:93], v[102:105], v[98:101]
	s_add_u32 s4, s4, 0x102000
	s_addc_u32 s5, s5, 0
	v_mfma_f32_16x16x32_bf16 v[90:93], v[94:97], v[106:109], v[90:93]
	v_lshlrev_b32_e32 v94, 16, v174
	v_and_b32_e32 v95, 0xffff0000, v174
	v_lshlrev_b32_e32 v96, 16, v175
	v_and_b32_e32 v97, 0xffff0000, v175
	s_nop 1
	v_mfma_f32_16x16x32_bf16 v[82:85], v[82:85], v[102:105], v[94:97]
	s_nop 0
	v_cvt_pk_bf16_f32 v90, v90, v91
	v_cvt_pk_bf16_f32 v91, v92, v93
	v_mfma_f32_16x16x32_bf16 v[94:97], v[86:89], v[106:109], v[82:85]
	s_nop 3
	v_lshlrev_b32_e32 v82, 16, v172
	v_and_b32_e32 v83, 0xffff0000, v172
	v_lshlrev_b32_e32 v84, 16, v173
	v_and_b32_e32 v85, 0xffff0000, v173
	v_cvt_pk_bf16_f32 v92, v94, v95
	v_cvt_pk_bf16_f32 v93, v96, v97
	v_mfma_f32_16x16x32_bf16 v[74:77], v[74:77], v[102:105], v[82:85]
	v_mfma_f32_16x16x32_bf16 v[74:77], v[78:81], v[106:109], v[74:77]
	v_lshlrev_b32_e32 v78, 16, v170
	v_and_b32_e32 v79, 0xffff0000, v170
	v_lshlrev_b32_e32 v80, 16, v171
	v_and_b32_e32 v81, 0xffff0000, v171
	s_nop 1
	v_mfma_f32_16x16x32_bf16 v[66:69], v[66:69], v[102:105], v[78:81]
	s_nop 0
	v_cvt_pk_bf16_f32 v74, v74, v75
	v_cvt_pk_bf16_f32 v75, v76, v77
	v_mfma_f32_16x16x32_bf16 v[78:81], v[70:73], v[106:109], v[66:69]
	global_load_dwordx4 v[114:117], v248, s[6:7]
	global_load_dwordx4 v[118:121], v248, s[6:7] offset:1024
	global_load_dwordx2 v[212:213], v0, s[4:5]
	global_load_dwordx4 v[98:101], v248, s[6:7] offset:2048
	global_load_dwordx4 v[102:105], v248, s[6:7] offset:3072
	global_load_dwordx2 v[210:211], v179, s[4:5]
	global_load_dwordx4 v[82:85], v249, s[6:7]
	global_load_dwordx4 v[86:89], v250, s[6:7]
	global_load_dwordx2 v[174:175], v191, s[4:5]
	global_load_dwordx4 v[66:69], v189, s[6:7]
	global_load_dwordx4 v[70:73], v187, s[6:7]
	global_load_dwordx2 v[170:171], v195, s[4:5]
	s_add_i32 s4, s2, 40
	s_ashr_i32 s5, s4, 31
	s_lshl_b64 s[6:7], s[4:5], 13
	v_cvt_pk_bf16_f32 v76, v78, v79
	v_lshl_add_u64 v[78:79], v[180:181], 0, s[6:7]
	v_cvt_pk_bf16_f32 v77, v80, v81
	global_store_dwordx4 v[78:79], v[90:93], off
	global_store_dwordx4 v[78:79], v[74:77], off offset:1024
	s_waitcnt vmcnt(36)
	v_lshlrev_b32_e32 v78, 16, v168
	v_and_b32_e32 v79, 0xffff0000, v168
	v_lshlrev_b32_e32 v80, 16, v169
	v_and_b32_e32 v81, 0xffff0000, v169
	s_lshl_b64 s[4:5], s[4:5], 15
	s_add_u32 s3, s40, s4
	v_mfma_f32_16x16x32_bf16 v[26:29], v[26:29], v[90:93], v[78:81]
	s_addc_u32 s7, s41, s5
	s_add_u32 s4, s3, 0x100000
	s_addc_u32 s5, s7, 0
	v_mfma_f32_16x16x32_bf16 v[26:29], v[30:33], v[74:77], v[26:29]
	v_lshlrev_b32_e32 v30, 16, v166
	v_and_b32_e32 v31, 0xffff0000, v166
	v_lshlrev_b32_e32 v32, 16, v167
	v_and_b32_e32 v33, 0xffff0000, v167
	s_add_u32 s6, s3, 0x102000
	s_addc_u32 s7, s7, 0
	v_mfma_f32_16x16x32_bf16 v[18:21], v[18:21], v[90:93], v[30:33]
	v_mfma_f32_16x16x32_bf16 v[18:21], v[22:25], v[74:77], v[18:21]
	v_lshlrev_b32_e32 v22, 16, v164
	v_and_b32_e32 v23, 0xffff0000, v164
	v_lshlrev_b32_e32 v24, 16, v165
	v_and_b32_e32 v25, 0xffff0000, v165
	s_nop 1
	v_mfma_f32_16x16x32_bf16 v[10:13], v[10:13], v[90:93], v[22:25]
	v_mfma_f32_16x16x32_bf16 v[10:13], v[14:17], v[74:77], v[10:13]
	v_lshlrev_b32_e32 v14, 16, v162
	v_and_b32_e32 v15, 0xffff0000, v162
	v_lshlrev_b32_e32 v16, 16, v163
	v_and_b32_e32 v17, 0xffff0000, v163
	s_waitcnt vmcnt(24)
	v_lshlrev_b32_e32 v22, 16, v202
	s_nop 2
	v_cvt_pk_bf16_f32 v10, v10, v11
	v_mfma_f32_16x16x32_bf16 v[2:5], v[2:5], v[90:93], v[14:17]
	v_cvt_pk_bf16_f32 v11, v12, v13
	v_and_b32_e32 v23, 0xffff0000, v202
	v_lshlrev_b32_e32 v24, 16, v203
	v_mfma_f32_16x16x32_bf16 v[2:5], v[6:9], v[74:77], v[2:5]
	global_load_dwordx4 v[122:125], v248, s[4:5]
	global_load_dwordx4 v[126:129], v248, s[4:5] offset:1024
	global_load_dwordx2 v[176:177], v0, s[6:7]
	global_load_dwordx4 v[106:109], v248, s[4:5] offset:2048
	global_load_dwordx4 v[110:113], v248, s[4:5] offset:3072
	global_load_dwordx2 v[172:173], v179, s[6:7]
	global_load_dwordx4 v[90:93], v249, s[4:5]
	global_load_dwordx4 v[94:97], v250, s[4:5]
	global_load_dwordx2 v[168:169], v191, s[6:7]
	global_load_dwordx4 v[74:77], v189, s[4:5]
	global_load_dwordx4 v[78:81], v187, s[4:5]
	global_load_dwordx2 v[164:165], v195, s[6:7]
	s_add_i32 s4, s2, 48
	s_ashr_i32 s5, s4, 31
	s_lshl_b64 s[6:7], s[4:5], 13
	v_cvt_pk_bf16_f32 v6, v26, v27
	v_cvt_pk_bf16_f32 v7, v28, v29
	v_cvt_pk_bf16_f32 v8, v18, v19
	v_cvt_pk_bf16_f32 v9, v20, v21
	v_cvt_pk_bf16_f32 v12, v2, v3
	v_lshl_add_u64 v[2:3], v[180:181], 0, s[6:7]
	v_cvt_pk_bf16_f32 v13, v4, v5
	global_store_dwordx4 v[2:3], v[6:9], off
	global_store_dwordx4 v[2:3], v[10:13], off offset:1024
	v_lshlrev_b32_e32 v2, 16, v208
	v_and_b32_e32 v3, 0xffff0000, v208
	v_lshlrev_b32_e32 v4, 16, v209
	v_and_b32_e32 v5, 0xffff0000, v209
	v_lshlrev_b32_e32 v14, 16, v206
	v_and_b32_e32 v15, 0xffff0000, v206
	v_lshlrev_b32_e32 v16, 16, v207
	v_and_b32_e32 v17, 0xffff0000, v207
	v_lshlrev_b32_e32 v18, 16, v204
	v_and_b32_e32 v19, 0xffff0000, v204
	v_lshlrev_b32_e32 v20, 16, v205
	v_and_b32_e32 v21, 0xffff0000, v205
	v_and_b32_e32 v25, 0xffff0000, v203
	s_lshl_b64 s[4:5], s[4:5], 15
	v_mfma_f32_16x16x32_bf16 v[2:5], v[58:61], v[6:9], v[2:5]
	s_add_u32 s3, s40, s4
	s_addc_u32 s7, s41, s5
	s_add_u32 s4, s3, 0x100000
	v_mfma_f32_16x16x32_bf16 v[14:17], v[50:53], v[6:9], v[14:17]
	s_addc_u32 s5, s7, 0
	s_add_u32 s6, s3, 0x102000
	s_addc_u32 s7, s7, 0
	v_mfma_f32_16x16x32_bf16 v[18:21], v[42:45], v[6:9], v[18:21]
	v_mfma_f32_16x16x32_bf16 v[6:9], v[34:37], v[6:9], v[22:25]
	v_mfma_f32_16x16x32_bf16 v[2:5], v[62:65], v[10:13], v[2:5]
	v_mfma_f32_16x16x32_bf16 v[14:17], v[54:57], v[10:13], v[14:17]
	v_mfma_f32_16x16x32_bf16 v[6:9], v[38:41], v[10:13], v[6:9]
	s_nop 5
	v_cvt_pk_bf16_f32 v2, v2, v3
	v_cvt_pk_bf16_f32 v3, v4, v5
	v_cvt_pk_bf16_f32 v4, v14, v15
	v_mfma_f32_16x16x32_bf16 v[18:21], v[46:49], v[10:13], v[18:21]
	global_load_dwordx4 v[58:61], v248, s[4:5]
	global_load_dwordx4 v[62:65], v248, s[4:5] offset:1024
	global_load_dwordx2 v[208:209], v0, s[6:7]
	global_load_dwordx4 v[50:53], v248, s[4:5] offset:2048
	global_load_dwordx4 v[54:57], v248, s[4:5] offset:3072
	global_load_dwordx2 v[206:207], v179, s[6:7]
	global_load_dwordx4 v[42:45], v249, s[4:5]
	global_load_dwordx4 v[46:49], v250, s[4:5]
	global_load_dwordx2 v[204:205], v191, s[6:7]
	global_load_dwordx4 v[34:37], v189, s[4:5]
	global_load_dwordx4 v[38:41], v187, s[4:5]
	global_load_dwordx2 v[202:203], v195, s[6:7]
	s_add_i32 s4, s2, 56
	s_ashr_i32 s5, s4, 31
	s_lshl_b64 s[6:7], s[4:5], 13
	v_cvt_pk_bf16_f32 v5, v16, v17
	v_cvt_pk_bf16_f32 v12, v6, v7
	v_lshl_add_u64 v[6:7], v[180:181], 0, s[6:7]
	v_cvt_pk_bf16_f32 v10, v18, v19
	v_cvt_pk_bf16_f32 v11, v20, v21
	v_cvt_pk_bf16_f32 v13, v8, v9
	global_store_dwordx4 v[6:7], v[2:5], off
	global_store_dwordx4 v[6:7], v[10:13], off offset:1024
	s_waitcnt vmcnt(36)
; __device__ __forceinline__ unsigned pk2(float lo, float hi) { const f32x2 f = {lo, hi}; const bf16n2 v = __builtin_convertvector(f, bf16n2); return __builtin_bit_cast(unsigned, v); }
; #define RW_LOAD_SET(SET, UNIT) do { const bf16_t* ug_ = rwu + (size_t)(UNIT) * 16384; \
;     _Pragma("unroll") for (int ta = 0; ta < 4; ++ta) { An[SET][ta][0] = *(const bf16x8*)(ug_ + ((ta * 2) * 64 + lane) * 8); An[SET][ta][1] = *(const bf16x8*)(ug_ + ((ta * 2 + 1) * 64 + lane) * 8); \
;         Zn[SET][ta] = *(const u32x2*)(ug_ + 4096 + ((cq * 4 + ta) * 64 + lane) * 4); } } while (0)
; template <int SM>
; __device__ __forceinline__ void phase_rwkv_scan(const Ctx& c, const bf16_t* rwu, bf16_t* rws) {
;     ...
;     for (int ch = 0; ch < T / 64; ch += 32) {
; #pragma unroll
;         for (int uu = 0; uu < 32; ++uu) {
;             const int u = uu % RW_SETS;
;             const int unit = (ch + uu) * 8 + h;
;             bf16_t* sg = rws + (size_t)unit * 4096 + cq * 1024 + lane * 8;
;             *(bf16x8*)(sg) = Bhi[0]; *(bf16x8*)(sg + 512) = Bhi[1];
;             f32x4 acc[4];
; #pragma unroll
;             for (int ta = 0; ta < 4; ++ta) { const u32x2 z = Zn[u][ta];
;                 acc[ta] = (f32x4){__uint_as_float(z.x << 16), __uint_as_float(z.x & 0xffff0000u), __uint_as_float(z.y << 16), __uint_as_float(z.y & 0xffff0000u)};
; #pragma unroll
;                 for (int s = 0; s < 2; ++s) acc[ta] = __builtin_amdgcn_mfma_f32_16x16x32_bf16(An[u][ta][s], Bhi[s], acc[ta], 0, 0, 0); }
;             if (SM == 0) RW_LOAD_SET(u, (ch + uu + RW_SETS < T / 64) ? unit + 8 * RW_SETS : unit);
; #pragma unroll
;             for (int s = 0; s < 2; ++s) { u32x4 hi;
;                 hi.x = pk2(acc[2 * s][0], acc[2 * s][1]); hi.y = pk2(acc[2 * s][2], acc[2 * s][3]); hi.z = pk2(acc[2 * s + 1][0], acc[2 * s + 1][1]); hi.w = pk2(acc[2 * s + 1][2], acc[2 * s + 1][3]);
;                 Bhi[s] = __builtin_bit_cast(bf16x8, hi); }
;         }
	v_lshlrev_b32_e32 v6, 16, v214
	v_and_b32_e32 v7, 0xffff0000, v214
	v_lshlrev_b32_e32 v8, 16, v215
	v_and_b32_e32 v9, 0xffff0000, v215
	s_lshl_b64 s[4:5], s[4:5], 15
	s_add_u32 s3, s40, s4
	v_mfma_f32_16x16x32_bf16 v[6:9], v[130:133], v[2:5], v[6:9]
	s_addc_u32 s7, s41, s5
	s_add_u32 s4, s3, 0x100000
	s_addc_u32 s5, s7, 0
	v_mfma_f32_16x16x32_bf16 v[222:225], v[134:137], v[10:13], v[6:9]
	s_add_u32 s6, s3, 0x102000
	s_addc_u32 s7, s7, 0
	s_nop 1
	v_lshlrev_b32_e32 v6, 16, v216
	v_and_b32_e32 v7, 0xffff0000, v216
	v_lshlrev_b32_e32 v8, 16, v217
	v_and_b32_e32 v9, 0xffff0000, v217
	s_nop 1
	v_mfma_f32_16x16x32_bf16 v[6:9], v[138:141], v[2:5], v[6:9]
	v_mfma_f32_16x16x32_bf16 v[214:217], v[142:145], v[10:13], v[6:9]
	s_nop 6
	v_lshlrev_b32_e32 v6, 16, v218
	v_and_b32_e32 v7, 0xffff0000, v218
	v_lshlrev_b32_e32 v8, 16, v219
	v_and_b32_e32 v9, 0xffff0000, v219
	s_nop 1
	v_mfma_f32_16x16x32_bf16 v[6:9], v[146:149], v[2:5], v[6:9]
	v_mfma_f32_16x16x32_bf16 v[144:147], v[150:153], v[10:13], v[6:9]
	v_cvt_pk_bf16_f32 v152, v222, v223
	v_cvt_pk_bf16_f32 v153, v224, v225
	s_nop 4
	v_lshlrev_b32_e32 v6, 16, v220
	v_and_b32_e32 v7, 0xffff0000, v220
	v_lshlrev_b32_e32 v8, 16, v221
	v_and_b32_e32 v9, 0xffff0000, v221
	v_cvt_pk_bf16_f32 v144, v144, v145
	v_cvt_pk_bf16_f32 v145, v146, v147
	v_mfma_f32_16x16x32_bf16 v[2:5], v[154:157], v[2:5], v[6:9]
	v_cvt_pk_bf16_f32 v154, v214, v215
	v_cvt_pk_bf16_f32 v155, v216, v217
	v_mfma_f32_16x16x32_bf16 v[148:151], v[158:161], v[10:13], v[2:5]
	global_load_dwordx4 v[26:29], v248, s[4:5]
	global_load_dwordx4 v[30:33], v248, s[4:5] offset:1024
	global_load_dwordx2 v[130:131], v0, s[6:7]
	global_load_dwordx4 v[18:21], v248, s[4:5] offset:2048
	global_load_dwordx4 v[22:25], v248, s[4:5] offset:3072
	global_load_dwordx2 v[134:135], v179, s[6:7]
	global_load_dwordx4 v[10:13], v249, s[4:5]
	global_load_dwordx4 v[14:17], v250, s[4:5]
	global_load_dwordx2 v[138:139], v191, s[6:7]
	global_load_dwordx4 v[2:5], v189, s[4:5]
	global_load_dwordx4 v[6:9], v187, s[4:5]
	global_load_dwordx2 v[142:143], v195, s[6:7]
	s_add_i32 s4, s2, 64
	s_ashr_i32 s5, s4, 31
	v_cvt_pk_bf16_f32 v146, v148, v149
	v_cvt_pk_bf16_f32 v147, v150, v151
	s_waitcnt vmcnt(36)
	v_lshlrev_b32_e32 v148, 16, v212
	v_and_b32_e32 v149, 0xffff0000, v212
	v_lshlrev_b32_e32 v150, 16, v213
	v_and_b32_e32 v151, 0xffff0000, v213
	s_lshl_b64 s[6:7], s[4:5], 13
	v_lshl_add_u64 v[132:133], v[180:181], 0, s[6:7]
	v_mfma_f32_16x16x32_bf16 v[114:117], v[114:117], v[152:155], v[148:151]
	s_lshl_b64 s[4:5], s[4:5], 15
	global_store_dwordx4 v[132:133], v[152:155], off
	global_store_dwordx4 v[132:133], v[144:147], off offset:1024
	s_add_u32 s3, s40, s4
	v_mfma_f32_16x16x32_bf16 v[148:151], v[118:121], v[144:147], v[114:117]
	s_addc_u32 s7, s41, s5
	s_add_u32 s4, s3, 0x100000
	s_addc_u32 s5, s7, 0
	v_lshlrev_b32_e32 v114, 16, v210
	v_and_b32_e32 v115, 0xffff0000, v210
	v_lshlrev_b32_e32 v116, 16, v211
	v_and_b32_e32 v117, 0xffff0000, v211
	s_add_u32 s6, s3, 0x102000
	v_cvt_pk_bf16_f32 v148, v148, v149
	v_mfma_f32_16x16x32_bf16 v[98:101], v[98:101], v[152:155], v[114:117]
	v_cvt_pk_bf16_f32 v149, v150, v151
	s_addc_u32 s7, s7, 0
	v_mfma_f32_16x16x32_bf16 v[156:159], v[102:105], v[144:147], v[98:101]
	s_nop 4
	v_lshlrev_b32_e32 v98, 16, v174
	v_and_b32_e32 v99, 0xffff0000, v174
	v_lshlrev_b32_e32 v100, 16, v175
	v_and_b32_e32 v101, 0xffff0000, v175
	v_cvt_pk_bf16_f32 v150, v156, v157
	v_cvt_pk_bf16_f32 v151, v158, v159
	v_mfma_f32_16x16x32_bf16 v[82:85], v[82:85], v[152:155], v[98:101]
	v_mfma_f32_16x16x32_bf16 v[210:213], v[86:89], v[144:147], v[82:85]
	s_nop 6
	v_lshlrev_b32_e32 v82, 16, v170
	v_and_b32_e32 v83, 0xffff0000, v170
	v_lshlrev_b32_e32 v84, 16, v171
	v_and_b32_e32 v85, 0xffff0000, v171
	s_nop 1
	v_mfma_f32_16x16x32_bf16 v[66:69], v[66:69], v[152:155], v[82:85]
	v_cvt_pk_bf16_f32 v152, v210, v211
	v_cvt_pk_bf16_f32 v153, v212, v213
	v_mfma_f32_16x16x32_bf16 v[144:147], v[70:73], v[144:147], v[66:69]
	global_load_dwordx4 v[114:117], v248, s[4:5]
	global_load_dwordx4 v[118:121], v248, s[4:5] offset:1024
	global_load_dwordx2 v[174:175], v0, s[6:7]
	global_load_dwordx4 v[98:101], v248, s[4:5] offset:2048
	global_load_dwordx4 v[102:105], v248, s[4:5] offset:3072
	global_load_dwordx2 v[170:171], v179, s[6:7]
	global_load_dwordx4 v[82:85], v249, s[4:5]
	global_load_dwordx4 v[86:89], v250, s[4:5]
	global_load_dwordx2 v[166:167], v191, s[6:7]
	global_load_dwordx4 v[66:69], v189, s[4:5]
	global_load_dwordx4 v[70:73], v187, s[4:5]
	global_load_dwordx2 v[162:163], v195, s[6:7]
	s_add_i32 s4, s2, 0x48
	s_ashr_i32 s5, s4, 31
	v_cvt_pk_bf16_f32 v154, v144, v145
	v_cvt_pk_bf16_f32 v155, v146, v147
	s_waitcnt vmcnt(36)
; __device__ __forceinline__ unsigned pk2(float lo, float hi) { const f32x2 f = {lo, hi}; const bf16n2 v = __builtin_convertvector(f, bf16n2); return __builtin_bit_cast(unsigned, v); }
; #define RW_LOAD_SET(SET, UNIT) do { const bf16_t* ug_ = rwu + (size_t)(UNIT) * 16384; \
;     _Pragma("unroll") for (int ta = 0; ta < 4; ++ta) { An[SET][ta][0] = *(const bf16x8*)(ug_ + ((ta * 2) * 64 + lane) * 8); An[SET][ta][1] = *(const bf16x8*)(ug_ + ((ta * 2 + 1) * 64 + lane) * 8); \
;         Zn[SET][ta] = *(const u32x2*)(ug_ + 4096 + ((cq * 4 + ta) * 64 + lane) * 4); } } while (0)
; template <int SM>
; __device__ __forceinline__ void phase_rwkv_scan(const Ctx& c, const bf16_t* rwu, bf16_t* rws) {
;     ...
;     for (int ch = 0; ch < T / 64; ch += 32) {
; #pragma unroll
;         for (int uu = 0; uu < 32; ++uu) {
;             const int u = uu % RW_SETS;
;             const int unit = (ch + uu) * 8 + h;
;             bf16_t* sg = rws + (size_t)unit * 4096 + cq * 1024 + lane * 8;
;             *(bf16x8*)(sg) = Bhi[0]; *(bf16x8*)(sg + 512) = Bhi[1];
;             f32x4 acc[4];
; #pragma unroll
;             for (int ta = 0; ta < 4; ++ta) { const u32x2 z = Zn[u][ta];
;                 acc[ta] = (f32x4){__uint_as_float(z.x << 16), __uint_as_float(z.x & 0xffff0000u), __uint_as_float(z.y << 16), __uint_as_float(z.y & 0xffff0000u)};
; #pragma unroll
;                 for (int s = 0; s < 2; ++s) acc[ta] = __builtin_amdgcn_mfma_f32_16x16x32_bf16(An[u][ta][s], Bhi[s], acc[ta], 0, 0, 0); }
;             if (SM == 0) RW_LOAD_SET(u, (ch + uu + RW_SETS < T / 64) ? unit + 8 * RW_SETS : unit);
; #pragma unroll
;             for (int s = 0; s < 2; ++s) { u32x4 hi;
;                 hi.x = pk2(acc[2 * s][0], acc[2 * s][1]); hi.y = pk2(acc[2 * s][2], acc[2 * s][3]); hi.z = pk2(acc[2 * s + 1][0], acc[2 * s + 1][1]); hi.w = pk2(acc[2 * s + 1][2], acc[2 * s + 1][3]);
;                 Bhi[s] = __builtin_bit_cast(bf16x8, hi); }
;         }
	v_lshlrev_b32_e32 v144, 16, v176
	v_and_b32_e32 v145, 0xffff0000, v176
	v_lshlrev_b32_e32 v146, 16, v177
	v_and_b32_e32 v147, 0xffff0000, v177
	s_lshl_b64 s[6:7], s[4:5], 13
	v_lshl_add_u64 v[132:133], v[180:181], 0, s[6:7]
	v_mfma_f32_16x16x32_bf16 v[122:125], v[122:125], v[148:151], v[144:147]
	s_lshl_b64 s[4:5], s[4:5], 15
	global_store_dwordx4 v[132:133], v[148:151], off
	global_store_dwordx4 v[132:133], v[152:155], off offset:1024
	s_add_u32 s3, s40, s4
	v_mfma_f32_16x16x32_bf16 v[144:147], v[126:129], v[152:155], v[122:125]
	s_addc_u32 s7, s41, s5
	s_add_u32 s4, s3, 0x100000
	s_addc_u32 s5, s7, 0
	v_lshlrev_b32_e32 v122, 16, v172
	v_and_b32_e32 v123, 0xffff0000, v172
	v_lshlrev_b32_e32 v124, 16, v173
	v_and_b32_e32 v125, 0xffff0000, v173
	s_add_u32 s6, s3, 0x102000
	v_cvt_pk_bf16_f32 v144, v144, v145
	v_mfma_f32_16x16x32_bf16 v[106:109], v[106:109], v[148:151], v[122:125]
	v_cvt_pk_bf16_f32 v145, v146, v147
	s_addc_u32 s7, s7, 0
	v_mfma_f32_16x16x32_bf16 v[156:159], v[110:113], v[152:155], v[106:109]
	s_nop 4
	v_lshlrev_b32_e32 v106, 16, v168
	v_and_b32_e32 v107, 0xffff0000, v168
	v_lshlrev_b32_e32 v108, 16, v169
	v_and_b32_e32 v109, 0xffff0000, v169
	v_cvt_pk_bf16_f32 v146, v156, v157
	v_cvt_pk_bf16_f32 v147, v158, v159
	v_mfma_f32_16x16x32_bf16 v[90:93], v[90:93], v[148:151], v[106:109]
	v_mfma_f32_16x16x32_bf16 v[210:213], v[94:97], v[152:155], v[90:93]
	s_nop 6
	v_lshlrev_b32_e32 v90, 16, v164
	v_and_b32_e32 v91, 0xffff0000, v164
	v_lshlrev_b32_e32 v92, 16, v165
	v_and_b32_e32 v93, 0xffff0000, v165
	s_nop 1
	v_mfma_f32_16x16x32_bf16 v[74:77], v[74:77], v[148:151], v[90:93]
	v_mfma_f32_16x16x32_bf16 v[148:151], v[78:81], v[152:155], v[74:77]
	global_load_dwordx4 v[122:125], v248, s[4:5]
	global_load_dwordx4 v[126:129], v248, s[4:5] offset:1024
	global_load_dwordx2 v[176:177], v0, s[6:7]
	global_load_dwordx4 v[106:109], v248, s[4:5] offset:2048
	global_load_dwordx4 v[110:113], v248, s[4:5] offset:3072
	global_load_dwordx2 v[172:173], v179, s[6:7]
	global_load_dwordx4 v[90:93], v249, s[4:5]
	global_load_dwordx4 v[94:97], v250, s[4:5]
	global_load_dwordx2 v[168:169], v191, s[6:7]
	global_load_dwordx4 v[74:77], v189, s[4:5]
	global_load_dwordx4 v[78:81], v187, s[4:5]
	global_load_dwordx2 v[164:165], v195, s[6:7]
	v_cvt_pk_bf16_f32 v152, v210, v211
	v_cvt_pk_bf16_f32 v153, v212, v213
	v_cvt_pk_bf16_f32 v154, v148, v149
	v_cvt_pk_bf16_f32 v155, v150, v151
	s_waitcnt vmcnt(36)
	v_lshlrev_b32_e32 v148, 16, v208
	v_and_b32_e32 v149, 0xffff0000, v208
	v_lshlrev_b32_e32 v150, 16, v209
	v_and_b32_e32 v151, 0xffff0000, v209
	s_add_i32 s4, s2, 0x50
	s_ashr_i32 s5, s4, 31
	v_mfma_f32_16x16x32_bf16 v[58:61], v[58:61], v[144:147], v[148:151]
	s_lshl_b64 s[6:7], s[4:5], 13
	v_lshl_add_u64 v[132:133], v[180:181], 0, s[6:7]
	s_lshl_b64 s[4:5], s[4:5], 15
	v_mfma_f32_16x16x32_bf16 v[148:151], v[62:65], v[152:155], v[58:61]
	global_store_dwordx4 v[132:133], v[144:147], off
	global_store_dwordx4 v[132:133], v[152:155], off offset:1024
	s_add_u32 s3, s40, s4
	s_nop 0
	v_lshlrev_b32_e32 v58, 16, v206
	v_and_b32_e32 v59, 0xffff0000, v206
	v_lshlrev_b32_e32 v60, 16, v207
	v_and_b32_e32 v61, 0xffff0000, v207
	s_addc_u32 s7, s41, s5
	s_add_u32 s4, s3, 0x100000
	v_mfma_f32_16x16x32_bf16 v[50:53], v[50:53], v[144:147], v[58:61]
	s_addc_u32 s5, s7, 0
	s_add_u32 s6, s3, 0x102000
	v_cvt_pk_bf16_f32 v148, v148, v149
	v_mfma_f32_16x16x32_bf16 v[206:209], v[54:57], v[152:155], v[50:53]
	v_cvt_pk_bf16_f32 v149, v150, v151
	s_addc_u32 s7, s7, 0
	s_nop 1
	v_lshlrev_b32_e32 v50, 16, v204
	v_and_b32_e32 v51, 0xffff0000, v204
	v_lshlrev_b32_e32 v52, 16, v205
	v_and_b32_e32 v53, 0xffff0000, v205
	v_cvt_pk_bf16_f32 v150, v206, v207
	v_cvt_pk_bf16_f32 v151, v208, v209
	v_mfma_f32_16x16x32_bf16 v[42:45], v[42:45], v[144:147], v[50:53]
	v_mfma_f32_16x16x32_bf16 v[210:213], v[46:49], v[152:155], v[42:45]
	s_nop 6
	v_lshlrev_b32_e32 v42, 16, v202
	v_and_b32_e32 v43, 0xffff0000, v202
	v_lshlrev_b32_e32 v44, 16, v203
	v_and_b32_e32 v45, 0xffff0000, v203
	v_cvt_pk_bf16_f32 v202, v210, v211
	v_cvt_pk_bf16_f32 v203, v212, v213
	v_mfma_f32_16x16x32_bf16 v[34:37], v[34:37], v[144:147], v[42:45]
	v_mfma_f32_16x16x32_bf16 v[144:147], v[38:41], v[152:155], v[34:37]
	global_load_dwordx4 v[58:61], v248, s[4:5]
	global_load_dwordx4 v[62:65], v248, s[4:5] offset:1024
	global_load_dwordx2 v[160:161], v0, s[6:7]
	global_load_dwordx4 v[50:53], v248, s[4:5] offset:2048
	global_load_dwordx4 v[54:57], v248, s[4:5] offset:3072
	global_load_dwordx2 v[158:159], v179, s[6:7]
	global_load_dwordx4 v[42:45], v249, s[4:5]
	global_load_dwordx4 v[46:49], v250, s[4:5]
	global_load_dwordx2 v[156:157], v191, s[6:7]
	global_load_dwordx4 v[34:37], v189, s[4:5]
	global_load_dwordx4 v[38:41], v187, s[4:5]
	global_load_dwordx2 v[154:155], v195, s[6:7]
	s_add_i32 s4, s2, 0x58
	s_ashr_i32 s5, s4, 31
	v_cvt_pk_bf16_f32 v204, v144, v145
	v_cvt_pk_bf16_f32 v205, v146, v147
	s_waitcnt vmcnt(36)
; __device__ __forceinline__ unsigned pk2(float lo, float hi) { const f32x2 f = {lo, hi}; const bf16n2 v = __builtin_convertvector(f, bf16n2); return __builtin_bit_cast(unsigned, v); }
; #define RW_LOAD_SET(SET, UNIT) do { const bf16_t* ug_ = rwu + (size_t)(UNIT) * 16384; \
;     _Pragma("unroll") for (int ta = 0; ta < 4; ++ta) { An[SET][ta][0] = *(const bf16x8*)(ug_ + ((ta * 2) * 64 + lane) * 8); An[SET][ta][1] = *(const bf16x8*)(ug_ + ((ta * 2 + 1) * 64 + lane) * 8); \
;         Zn[SET][ta] = *(const u32x2*)(ug_ + 4096 + ((cq * 4 + ta) * 64 + lane) * 4); } } while (0)
; template <int SM>
; __device__ __forceinline__ void phase_rwkv_scan(const Ctx& c, const bf16_t* rwu, bf16_t* rws) {
;     ...
;     for (int ch = 0; ch < T / 64; ch += 32) {
; #pragma unroll
;         for (int uu = 0; uu < 32; ++uu) {
;             const int u = uu % RW_SETS;
;             const int unit = (ch + uu) * 8 + h;
;             bf16_t* sg = rws + (size_t)unit * 4096 + cq * 1024 + lane * 8;
;             *(bf16x8*)(sg) = Bhi[0]; *(bf16x8*)(sg + 512) = Bhi[1];
;             f32x4 acc[4];
; #pragma unroll
;             for (int ta = 0; ta < 4; ++ta) { const u32x2 z = Zn[u][ta];
;                 acc[ta] = (f32x4){__uint_as_float(z.x << 16), __uint_as_float(z.x & 0xffff0000u), __uint_as_float(z.y << 16), __uint_as_float(z.y & 0xffff0000u)};
; #pragma unroll
;                 for (int s = 0; s < 2; ++s) acc[ta] = __builtin_amdgcn_mfma_f32_16x16x32_bf16(An[u][ta][s], Bhi[s], acc[ta], 0, 0, 0); }
;             if (SM == 0) RW_LOAD_SET(u, (ch + uu + RW_SETS < T / 64) ? unit + 8 * RW_SETS : unit);
; #pragma unroll
;             for (int s = 0; s < 2; ++s) { u32x4 hi;
;                 hi.x = pk2(acc[2 * s][0], acc[2 * s][1]); hi.y = pk2(acc[2 * s][2], acc[2 * s][3]); hi.z = pk2(acc[2 * s + 1][0], acc[2 * s + 1][1]); hi.w = pk2(acc[2 * s + 1][2], acc[2 * s + 1][3]);
;                 Bhi[s] = __builtin_bit_cast(bf16x8, hi); }
;         }
	v_lshlrev_b32_e32 v144, 16, v130
	v_and_b32_e32 v145, 0xffff0000, v130
	v_lshlrev_b32_e32 v146, 16, v131
	v_and_b32_e32 v147, 0xffff0000, v131
	s_lshl_b64 s[6:7], s[4:5], 13
	v_lshl_add_u64 v[132:133], v[180:181], 0, s[6:7]
	v_mfma_f32_16x16x32_bf16 v[26:29], v[26:29], v[148:151], v[144:147]
	global_store_dwordx4 v[132:133], v[148:151], off
	global_store_dwordx4 v[132:133], v[202:205], off offset:1024
	s_lshl_b64 s[4:5], s[4:5], 15
	s_add_u32 s3, s40, s4
	v_mfma_f32_16x16x32_bf16 v[130:133], v[30:33], v[202:205], v[26:29]
	s_addc_u32 s7, s41, s5
	s_add_u32 s4, s3, 0x100000
	s_addc_u32 s5, s7, 0
	v_lshlrev_b32_e32 v26, 16, v134
	v_and_b32_e32 v27, 0xffff0000, v134
	v_lshlrev_b32_e32 v28, 16, v135
	v_and_b32_e32 v29, 0xffff0000, v135
	s_add_u32 s6, s3, 0x102000
	s_addc_u32 s7, s7, 0
	v_mfma_f32_16x16x32_bf16 v[18:21], v[18:21], v[148:151], v[26:29]
	v_mfma_f32_16x16x32_bf16 v[134:137], v[22:25], v[202:205], v[18:21]
	s_nop 6
	v_lshlrev_b32_e32 v18, 16, v138
	v_and_b32_e32 v19, 0xffff0000, v138
	v_lshlrev_b32_e32 v20, 16, v139
	v_and_b32_e32 v21, 0xffff0000, v139
	s_nop 1
	v_mfma_f32_16x16x32_bf16 v[10:13], v[10:13], v[148:151], v[18:21]
	v_mfma_f32_16x16x32_bf16 v[138:141], v[14:17], v[202:205], v[10:13]
	s_nop 6
	v_lshlrev_b32_e32 v10, 16, v142
	v_and_b32_e32 v11, 0xffff0000, v142
	v_lshlrev_b32_e32 v12, 16, v143
	v_and_b32_e32 v13, 0xffff0000, v143
	v_cvt_pk_bf16_f32 v206, v138, v139
	v_cvt_pk_bf16_f32 v207, v140, v141
	v_mfma_f32_16x16x32_bf16 v[2:5], v[2:5], v[148:151], v[10:13]
	v_mfma_f32_16x16x32_bf16 v[142:145], v[6:9], v[202:205], v[2:5]
	global_load_dwordx4 v[26:29], v248, s[4:5]
	global_load_dwordx4 v[30:33], v248, s[4:5] offset:1024
	global_load_dwordx2 v[152:153], v0, s[6:7]
	global_load_dwordx4 v[18:21], v248, s[4:5] offset:2048
	global_load_dwordx4 v[22:25], v248, s[4:5] offset:3072
	global_load_dwordx2 v[150:151], v179, s[6:7]
	global_load_dwordx4 v[10:13], v249, s[4:5]
	global_load_dwordx4 v[14:17], v250, s[4:5]
	global_load_dwordx2 v[148:149], v191, s[6:7]
	global_load_dwordx4 v[2:5], v189, s[4:5]
	global_load_dwordx4 v[6:9], v187, s[4:5]
	global_load_dwordx2 v[146:147], v195, s[6:7]
	s_add_i32 s4, s2, 0x60
	s_ashr_i32 s5, s4, 31
	s_lshl_b64 s[6:7], s[4:5], 13
	v_cvt_pk_bf16_f32 v202, v130, v131
	v_cvt_pk_bf16_f32 v203, v132, v133
	v_cvt_pk_bf16_f32 v204, v134, v135
	v_cvt_pk_bf16_f32 v205, v136, v137
	v_lshl_add_u64 v[130:131], v[180:181], 0, s[6:7]
	v_cvt_pk_bf16_f32 v208, v142, v143
	v_cvt_pk_bf16_f32 v209, v144, v145
	global_store_dwordx4 v[130:131], v[202:205], off
	global_store_dwordx4 v[130:131], v[206:209], off offset:1024
	s_waitcnt vmcnt(36)
	v_lshlrev_b32_e32 v130, 16, v174
	v_and_b32_e32 v131, 0xffff0000, v174
	v_lshlrev_b32_e32 v132, 16, v175
	v_and_b32_e32 v133, 0xffff0000, v175
	s_lshl_b64 s[4:5], s[4:5], 15
	s_add_u32 s3, s40, s4
	v_mfma_f32_16x16x32_bf16 v[114:117], v[114:117], v[202:205], v[130:133]
	s_addc_u32 s7, s41, s5
	s_add_u32 s4, s3, 0x100000
	s_addc_u32 s5, s7, 0
	v_mfma_f32_16x16x32_bf16 v[130:133], v[118:121], v[206:209], v[114:117]
	s_add_u32 s6, s3, 0x102000
	s_addc_u32 s7, s7, 0
	s_nop 1
	v_lshlrev_b32_e32 v114, 16, v170
	v_and_b32_e32 v115, 0xffff0000, v170
	v_lshlrev_b32_e32 v116, 16, v171
	v_and_b32_e32 v117, 0xffff0000, v171
	s_nop 1
	v_mfma_f32_16x16x32_bf16 v[98:101], v[98:101], v[202:205], v[114:117]
	v_mfma_f32_16x16x32_bf16 v[134:137], v[102:105], v[206:209], v[98:101]
	s_nop 6
	v_lshlrev_b32_e32 v98, 16, v166
	v_and_b32_e32 v99, 0xffff0000, v166
	v_lshlrev_b32_e32 v100, 16, v167
	v_and_b32_e32 v101, 0xffff0000, v167
	s_nop 1
	v_mfma_f32_16x16x32_bf16 v[82:85], v[82:85], v[202:205], v[98:101]
	v_mfma_f32_16x16x32_bf16 v[138:141], v[86:89], v[206:209], v[82:85]
	s_nop 6
	v_lshlrev_b32_e32 v82, 16, v162
	v_and_b32_e32 v83, 0xffff0000, v162
	v_lshlrev_b32_e32 v84, 16, v163
	v_and_b32_e32 v85, 0xffff0000, v163
	s_nop 1
	v_mfma_f32_16x16x32_bf16 v[66:69], v[66:69], v[202:205], v[82:85]
	v_cvt_pk_bf16_f32 v202, v130, v131
	v_cvt_pk_bf16_f32 v203, v132, v133
	v_cvt_pk_bf16_f32 v204, v134, v135
	v_mfma_f32_16x16x32_bf16 v[142:145], v[70:73], v[206:209], v[66:69]
	global_load_dwordx4 v[114:117], v248, s[4:5]
	global_load_dwordx4 v[118:121], v248, s[4:5] offset:1024
	global_load_dwordx2 v[174:175], v0, s[6:7]
	global_load_dwordx4 v[98:101], v248, s[4:5] offset:2048
	global_load_dwordx4 v[102:105], v248, s[4:5] offset:3072
	global_load_dwordx2 v[170:171], v179, s[6:7]
	global_load_dwordx4 v[82:85], v249, s[4:5]
	global_load_dwordx4 v[86:89], v250, s[4:5]
	global_load_dwordx2 v[166:167], v191, s[6:7]
	global_load_dwordx4 v[66:69], v189, s[4:5]
	global_load_dwordx4 v[70:73], v187, s[4:5]
	global_load_dwordx2 v[162:163], v195, s[6:7]
	s_add_i32 s4, s2, 0x68
	s_ashr_i32 s5, s4, 31
	s_lshl_b64 s[6:7], s[4:5], 13
	v_cvt_pk_bf16_f32 v205, v136, v137
	v_lshl_add_u64 v[130:131], v[180:181], 0, s[6:7]
	v_cvt_pk_bf16_f32 v206, v138, v139
	v_cvt_pk_bf16_f32 v207, v140, v141
	v_cvt_pk_bf16_f32 v208, v142, v143
	v_cvt_pk_bf16_f32 v209, v144, v145
	global_store_dwordx4 v[130:131], v[202:205], off
	global_store_dwordx4 v[130:131], v[206:209], off offset:1024
	s_waitcnt vmcnt(36)
; __device__ __forceinline__ unsigned pk2(float lo, float hi) { const f32x2 f = {lo, hi}; const bf16n2 v = __builtin_convertvector(f, bf16n2); return __builtin_bit_cast(unsigned, v); }
; #define RW_LOAD_SET(SET, UNIT) do { const bf16_t* ug_ = rwu + (size_t)(UNIT) * 16384; \
;     _Pragma("unroll") for (int ta = 0; ta < 4; ++ta) { An[SET][ta][0] = *(const bf16x8*)(ug_ + ((ta * 2) * 64 + lane) * 8); An[SET][ta][1] = *(const bf16x8*)(ug_ + ((ta * 2 + 1) * 64 + lane) * 8); \
;         Zn[SET][ta] = *(const u32x2*)(ug_ + 4096 + ((cq * 4 + ta) * 64 + lane) * 4); } } while (0)
; template <int SM>
; __device__ __forceinline__ void phase_rwkv_scan(const Ctx& c, const bf16_t* rwu, bf16_t* rws) {
;     ...
;     for (int ch = 0; ch < T / 64; ch += 32) {
; #pragma unroll
;         for (int uu = 0; uu < 32; ++uu) {
;             const int u = uu % RW_SETS;
;             const int unit = (ch + uu) * 8 + h;
;             bf16_t* sg = rws + (size_t)unit * 4096 + cq * 1024 + lane * 8;
;             *(bf16x8*)(sg) = Bhi[0]; *(bf16x8*)(sg + 512) = Bhi[1];
;             f32x4 acc[4];
; #pragma unroll
;             for (int ta = 0; ta < 4; ++ta) { const u32x2 z = Zn[u][ta];
;                 acc[ta] = (f32x4){__uint_as_float(z.x << 16), __uint_as_float(z.x & 0xffff0000u), __uint_as_float(z.y << 16), __uint_as_float(z.y & 0xffff0000u)};
; #pragma unroll
;                 for (int s = 0; s < 2; ++s) acc[ta] = __builtin_amdgcn_mfma_f32_16x16x32_bf16(An[u][ta][s], Bhi[s], acc[ta], 0, 0, 0); }
;             if (SM == 0) RW_LOAD_SET(u, (ch + uu + RW_SETS < T / 64) ? unit + 8 * RW_SETS : unit);
; #pragma unroll
;             for (int s = 0; s < 2; ++s) { u32x4 hi;
;                 hi.x = pk2(acc[2 * s][0], acc[2 * s][1]); hi.y = pk2(acc[2 * s][2], acc[2 * s][3]); hi.z = pk2(acc[2 * s + 1][0], acc[2 * s + 1][1]); hi.w = pk2(acc[2 * s + 1][2], acc[2 * s + 1][3]);
;                 Bhi[s] = __builtin_bit_cast(bf16x8, hi); }
;         }
	v_lshlrev_b32_e32 v130, 16, v176
	v_and_b32_e32 v131, 0xffff0000, v176
	v_lshlrev_b32_e32 v132, 16, v177
	v_and_b32_e32 v133, 0xffff0000, v177
	s_lshl_b64 s[4:5], s[4:5], 15
	s_add_u32 s3, s40, s4
	v_mfma_f32_16x16x32_bf16 v[122:125], v[122:125], v[202:205], v[130:133]
	s_addc_u32 s7, s41, s5
	s_add_u32 s4, s3, 0x100000
	s_addc_u32 s5, s7, 0
	v_mfma_f32_16x16x32_bf16 v[130:133], v[126:129], v[206:209], v[122:125]
	s_add_u32 s6, s3, 0x102000
	s_addc_u32 s7, s7, 0
	s_nop 1
	v_lshlrev_b32_e32 v122, 16, v172
	v_and_b32_e32 v123, 0xffff0000, v172
	v_lshlrev_b32_e32 v124, 16, v173
	v_and_b32_e32 v125, 0xffff0000, v173
	s_nop 1
	v_mfma_f32_16x16x32_bf16 v[106:109], v[106:109], v[202:205], v[122:125]
	v_mfma_f32_16x16x32_bf16 v[134:137], v[110:113], v[206:209], v[106:109]
	s_nop 6
	v_lshlrev_b32_e32 v106, 16, v168
	v_and_b32_e32 v107, 0xffff0000, v168
	v_lshlrev_b32_e32 v108, 16, v169
	v_and_b32_e32 v109, 0xffff0000, v169
	s_nop 1
	v_mfma_f32_16x16x32_bf16 v[90:93], v[90:93], v[202:205], v[106:109]
	v_mfma_f32_16x16x32_bf16 v[138:141], v[94:97], v[206:209], v[90:93]
	s_nop 6
	v_lshlrev_b32_e32 v90, 16, v164
	v_and_b32_e32 v91, 0xffff0000, v164
	v_lshlrev_b32_e32 v92, 16, v165
	v_and_b32_e32 v93, 0xffff0000, v165
	s_nop 1
	v_mfma_f32_16x16x32_bf16 v[74:77], v[74:77], v[202:205], v[90:93]
	v_cvt_pk_bf16_f32 v202, v130, v131
	v_cvt_pk_bf16_f32 v203, v132, v133
	v_cvt_pk_bf16_f32 v204, v134, v135
	v_mfma_f32_16x16x32_bf16 v[142:145], v[78:81], v[206:209], v[74:77]
	global_load_dwordx4 v[122:125], v248, s[4:5]
	global_load_dwordx4 v[126:129], v248, s[4:5] offset:1024
	global_load_dwordx2 v[176:177], v0, s[6:7]
	global_load_dwordx4 v[106:109], v248, s[4:5] offset:2048
	global_load_dwordx4 v[110:113], v248, s[4:5] offset:3072
	global_load_dwordx2 v[172:173], v179, s[6:7]
	global_load_dwordx4 v[90:93], v249, s[4:5]
	global_load_dwordx4 v[94:97], v250, s[4:5]
	global_load_dwordx2 v[168:169], v191, s[6:7]
	global_load_dwordx4 v[74:77], v189, s[4:5]
	global_load_dwordx4 v[78:81], v187, s[4:5]
	global_load_dwordx2 v[164:165], v195, s[6:7]
	s_add_i32 s4, s2, 0x70
	s_ashr_i32 s5, s4, 31
	s_lshl_b64 s[6:7], s[4:5], 13
	v_cvt_pk_bf16_f32 v205, v136, v137
	v_lshl_add_u64 v[130:131], v[180:181], 0, s[6:7]
	v_cvt_pk_bf16_f32 v206, v138, v139
	v_cvt_pk_bf16_f32 v207, v140, v141
	v_cvt_pk_bf16_f32 v208, v142, v143
	v_cvt_pk_bf16_f32 v209, v144, v145
	global_store_dwordx4 v[130:131], v[202:205], off
	global_store_dwordx4 v[130:131], v[206:209], off offset:1024
	s_waitcnt vmcnt(36)
	v_lshlrev_b32_e32 v130, 16, v160
	v_and_b32_e32 v131, 0xffff0000, v160
	v_lshlrev_b32_e32 v132, 16, v161
	v_and_b32_e32 v133, 0xffff0000, v161
	s_lshl_b64 s[4:5], s[4:5], 15
	s_add_u32 s3, s40, s4
	v_mfma_f32_16x16x32_bf16 v[58:61], v[58:61], v[202:205], v[130:133]
	s_addc_u32 s7, s41, s5
	s_add_u32 s4, s3, 0x100000
	s_addc_u32 s5, s7, 0
	v_mfma_f32_16x16x32_bf16 v[130:133], v[62:65], v[206:209], v[58:61]
	s_add_u32 s6, s3, 0x102000
	s_addc_u32 s7, s7, 0
	s_nop 1
	v_lshlrev_b32_e32 v58, 16, v158
	v_and_b32_e32 v59, 0xffff0000, v158
	v_lshlrev_b32_e32 v60, 16, v159
	v_and_b32_e32 v61, 0xffff0000, v159
	s_nop 1
	v_mfma_f32_16x16x32_bf16 v[50:53], v[50:53], v[202:205], v[58:61]
	v_mfma_f32_16x16x32_bf16 v[134:137], v[54:57], v[206:209], v[50:53]
	s_nop 6
	v_lshlrev_b32_e32 v50, 16, v156
	v_and_b32_e32 v51, 0xffff0000, v156
	v_lshlrev_b32_e32 v52, 16, v157
	v_and_b32_e32 v53, 0xffff0000, v157
	s_nop 1
	v_mfma_f32_16x16x32_bf16 v[42:45], v[42:45], v[202:205], v[50:53]
	v_mfma_f32_16x16x32_bf16 v[138:141], v[46:49], v[206:209], v[42:45]
	s_nop 6
	v_lshlrev_b32_e32 v42, 16, v154
	v_and_b32_e32 v43, 0xffff0000, v154
	v_lshlrev_b32_e32 v44, 16, v155
	v_and_b32_e32 v45, 0xffff0000, v155
	s_nop 1
	v_mfma_f32_16x16x32_bf16 v[34:37], v[34:37], v[202:205], v[42:45]
	v_cvt_pk_bf16_f32 v202, v130, v131
	v_cvt_pk_bf16_f32 v203, v132, v133
	v_cvt_pk_bf16_f32 v204, v134, v135
	v_mfma_f32_16x16x32_bf16 v[142:145], v[38:41], v[206:209], v[34:37]
	global_load_dwordx4 v[58:61], v248, s[4:5]
	global_load_dwordx4 v[62:65], v248, s[4:5] offset:1024
	global_load_dwordx2 v[160:161], v0, s[6:7]
	global_load_dwordx4 v[50:53], v248, s[4:5] offset:2048
	global_load_dwordx4 v[54:57], v248, s[4:5] offset:3072
	global_load_dwordx2 v[158:159], v179, s[6:7]
	global_load_dwordx4 v[42:45], v249, s[4:5]
	global_load_dwordx4 v[46:49], v250, s[4:5]
	global_load_dwordx2 v[156:157], v191, s[6:7]
	global_load_dwordx4 v[34:37], v189, s[4:5]
	global_load_dwordx4 v[38:41], v187, s[4:5]
	global_load_dwordx2 v[154:155], v195, s[6:7]
	s_add_i32 s4, s2, 0x78
	s_ashr_i32 s5, s4, 31
	s_lshl_b64 s[6:7], s[4:5], 13
	v_cvt_pk_bf16_f32 v205, v136, v137
	v_lshl_add_u64 v[130:131], v[180:181], 0, s[6:7]
	v_cvt_pk_bf16_f32 v134, v138, v139
	v_cvt_pk_bf16_f32 v135, v140, v141
	v_cvt_pk_bf16_f32 v136, v142, v143
	v_cvt_pk_bf16_f32 v137, v144, v145
	global_store_dwordx4 v[130:131], v[202:205], off
	global_store_dwordx4 v[130:131], v[134:137], off offset:1024
	s_waitcnt vmcnt(36)
; __device__ __forceinline__ unsigned pk2(float lo, float hi) { const f32x2 f = {lo, hi}; const bf16n2 v = __builtin_convertvector(f, bf16n2); return __builtin_bit_cast(unsigned, v); }
; #define RW_LOAD_SET(SET, UNIT) do { const bf16_t* ug_ = rwu + (size_t)(UNIT) * 16384; \
;     _Pragma("unroll") for (int ta = 0; ta < 4; ++ta) { An[SET][ta][0] = *(const bf16x8*)(ug_ + ((ta * 2) * 64 + lane) * 8); An[SET][ta][1] = *(const bf16x8*)(ug_ + ((ta * 2 + 1) * 64 + lane) * 8); \
;         Zn[SET][ta] = *(const u32x2*)(ug_ + 4096 + ((cq * 4 + ta) * 64 + lane) * 4); } } while (0)
; template <int SM>
; __device__ __forceinline__ void phase_rwkv_scan(const Ctx& c, const bf16_t* rwu, bf16_t* rws) {
;     ...
;     for (int ch = 0; ch < T / 64; ch += 32) {
; #pragma unroll
;         for (int uu = 0; uu < 32; ++uu) {
;             const int u = uu % RW_SETS;
;             const int unit = (ch + uu) * 8 + h;
;             bf16_t* sg = rws + (size_t)unit * 4096 + cq * 1024 + lane * 8;
;             *(bf16x8*)(sg) = Bhi[0]; *(bf16x8*)(sg + 512) = Bhi[1];
;             f32x4 acc[4];
; #pragma unroll
;             for (int ta = 0; ta < 4; ++ta) { const u32x2 z = Zn[u][ta];
;                 acc[ta] = (f32x4){__uint_as_float(z.x << 16), __uint_as_float(z.x & 0xffff0000u), __uint_as_float(z.y << 16), __uint_as_float(z.y & 0xffff0000u)};
; #pragma unroll
;                 for (int s = 0; s < 2; ++s) acc[ta] = __builtin_amdgcn_mfma_f32_16x16x32_bf16(An[u][ta][s], Bhi[s], acc[ta], 0, 0, 0); }
;             if (SM == 0) RW_LOAD_SET(u, (ch + uu + RW_SETS < T / 64) ? unit + 8 * RW_SETS : unit);
; #pragma unroll
;             for (int s = 0; s < 2; ++s) { u32x4 hi;
;                 hi.x = pk2(acc[2 * s][0], acc[2 * s][1]); hi.y = pk2(acc[2 * s][2], acc[2 * s][3]); hi.z = pk2(acc[2 * s + 1][0], acc[2 * s + 1][1]); hi.w = pk2(acc[2 * s + 1][2], acc[2 * s + 1][3]);
;                 Bhi[s] = __builtin_bit_cast(bf16x8, hi); }
;         }
	v_lshlrev_b32_e32 v130, 16, v152
	v_and_b32_e32 v131, 0xffff0000, v152
	v_lshlrev_b32_e32 v132, 16, v153
	v_and_b32_e32 v133, 0xffff0000, v153
	s_lshl_b64 s[4:5], s[4:5], 15
	s_add_u32 s3, s40, s4
	v_mfma_f32_16x16x32_bf16 v[26:29], v[26:29], v[202:205], v[130:133]
	s_addc_u32 s7, s41, s5
	s_add_u32 s4, s3, 0x100000
	s_addc_u32 s5, s7, 0
	v_mfma_f32_16x16x32_bf16 v[130:133], v[30:33], v[134:137], v[26:29]
	s_add_u32 s6, s3, 0x102000
	s_addc_u32 s7, s7, 0
	s_nop 1
	v_lshlrev_b32_e32 v26, 16, v150
	v_and_b32_e32 v27, 0xffff0000, v150
	v_lshlrev_b32_e32 v28, 16, v151
	v_and_b32_e32 v29, 0xffff0000, v151
	v_cvt_pk_bf16_f32 v130, v130, v131
	v_cvt_pk_bf16_f32 v131, v132, v133
	v_mfma_f32_16x16x32_bf16 v[18:21], v[18:21], v[202:205], v[26:29]
	v_mfma_f32_16x16x32_bf16 v[138:141], v[22:25], v[134:137], v[18:21]
	s_nop 6
	v_lshlrev_b32_e32 v18, 16, v148
	v_and_b32_e32 v19, 0xffff0000, v148
	v_lshlrev_b32_e32 v20, 16, v149
	v_and_b32_e32 v21, 0xffff0000, v149
	v_cvt_pk_bf16_f32 v132, v138, v139
	v_cvt_pk_bf16_f32 v133, v140, v141
	v_mfma_f32_16x16x32_bf16 v[10:13], v[10:13], v[202:205], v[18:21]
	v_mfma_f32_16x16x32_bf16 v[142:145], v[14:17], v[134:137], v[10:13]
	s_nop 6
	v_lshlrev_b32_e32 v10, 16, v146
	v_and_b32_e32 v11, 0xffff0000, v146
	v_lshlrev_b32_e32 v12, 16, v147
	v_and_b32_e32 v13, 0xffff0000, v147
	v_cvt_pk_bf16_f32 v138, v142, v143
	v_cvt_pk_bf16_f32 v139, v144, v145
	v_mfma_f32_16x16x32_bf16 v[2:5], v[2:5], v[202:205], v[10:13]
	v_mfma_f32_16x16x32_bf16 v[134:137], v[6:9], v[134:137], v[2:5]
	global_load_dwordx4 v[26:29], v248, s[4:5]
	global_load_dwordx4 v[30:33], v248, s[4:5] offset:1024
	global_load_dwordx2 v[208:209], v0, s[6:7]
	global_load_dwordx4 v[18:21], v248, s[4:5] offset:2048
	global_load_dwordx4 v[22:25], v248, s[4:5] offset:3072
	global_load_dwordx2 v[206:207], v179, s[6:7]
	global_load_dwordx4 v[10:13], v249, s[4:5]
	global_load_dwordx4 v[14:17], v250, s[4:5]
	global_load_dwordx2 v[204:205], v191, s[6:7]
	global_load_dwordx4 v[2:5], v189, s[4:5]
	global_load_dwordx4 v[6:9], v187, s[4:5]
	global_load_dwordx2 v[202:203], v195, s[6:7]
	s_add_i32 s4, s2, 0x80
	s_ashr_i32 s5, s4, 31
	s_lshl_b64 s[6:7], s[4:5], 13
	v_cvt_pk_bf16_f32 v140, v134, v135
	v_lshl_add_u64 v[134:135], v[180:181], 0, s[6:7]
	v_cvt_pk_bf16_f32 v141, v136, v137
	global_store_dwordx4 v[134:135], v[130:133], off
	global_store_dwordx4 v[134:135], v[138:141], off offset:1024
	s_waitcnt vmcnt(36)
	v_lshlrev_b32_e32 v134, 16, v174
	v_and_b32_e32 v135, 0xffff0000, v174
	v_lshlrev_b32_e32 v136, 16, v175
	v_and_b32_e32 v137, 0xffff0000, v175
	s_lshl_b64 s[4:5], s[4:5], 15
	s_add_u32 s3, s40, s4
	v_mfma_f32_16x16x32_bf16 v[114:117], v[114:117], v[130:133], v[134:137]
	s_addc_u32 s7, s41, s5
	s_add_u32 s4, s3, 0x100000
	s_addc_u32 s5, s7, 0
	v_mfma_f32_16x16x32_bf16 v[114:117], v[118:121], v[138:141], v[114:117]
	v_lshlrev_b32_e32 v118, 16, v170
	v_and_b32_e32 v119, 0xffff0000, v170
	v_lshlrev_b32_e32 v120, 16, v171
	v_and_b32_e32 v121, 0xffff0000, v171
	s_add_u32 s6, s3, 0x102000
	s_addc_u32 s7, s7, 0
	v_mfma_f32_16x16x32_bf16 v[98:101], v[98:101], v[130:133], v[118:121]
	v_mfma_f32_16x16x32_bf16 v[118:121], v[102:105], v[138:141], v[98:101]
	s_nop 6
	v_lshlrev_b32_e32 v98, 16, v166
	v_and_b32_e32 v99, 0xffff0000, v166
	v_lshlrev_b32_e32 v100, 16, v167
	v_and_b32_e32 v101, 0xffff0000, v167
	s_nop 1
	v_mfma_f32_16x16x32_bf16 v[82:85], v[82:85], v[130:133], v[98:101]
	v_mfma_f32_16x16x32_bf16 v[146:149], v[86:89], v[138:141], v[82:85]
	s_nop 6
	v_lshlrev_b32_e32 v82, 16, v162
	v_and_b32_e32 v83, 0xffff0000, v162
	v_lshlrev_b32_e32 v84, 16, v163
	v_and_b32_e32 v85, 0xffff0000, v163
	s_nop 1
	v_mfma_f32_16x16x32_bf16 v[66:69], v[66:69], v[130:133], v[82:85]
	v_mfma_f32_16x16x32_bf16 v[66:69], v[70:73], v[138:141], v[66:69]
	global_load_dwordx4 v[138:141], v248, s[4:5]
	global_load_dwordx4 v[142:145], v248, s[4:5] offset:1024
	global_load_dwordx2 v[216:217], v0, s[6:7]
	global_load_dwordx4 v[130:133], v248, s[4:5] offset:2048
	global_load_dwordx4 v[134:137], v248, s[4:5] offset:3072
	global_load_dwordx2 v[214:215], v179, s[6:7]
	global_load_dwordx4 v[98:101], v249, s[4:5]
	global_load_dwordx4 v[102:105], v250, s[4:5]
	global_load_dwordx2 v[210:211], v191, s[6:7]
	global_load_dwordx4 v[82:85], v189, s[4:5]
	global_load_dwordx4 v[86:89], v187, s[4:5]
	global_load_dwordx2 v[174:175], v195, s[6:7]
	s_add_i32 s4, s2, 0x88
	s_ashr_i32 s5, s4, 31
	s_lshl_b64 s[6:7], s[4:5], 13
	v_cvt_pk_bf16_f32 v70, v114, v115
	v_cvt_pk_bf16_f32 v71, v116, v117
	v_cvt_pk_bf16_f32 v72, v118, v119
	v_cvt_pk_bf16_f32 v73, v120, v121
	v_cvt_pk_bf16_f32 v116, v66, v67
	v_lshl_add_u64 v[66:67], v[180:181], 0, s[6:7]
	v_cvt_pk_bf16_f32 v114, v146, v147
	v_cvt_pk_bf16_f32 v115, v148, v149
	v_cvt_pk_bf16_f32 v117, v68, v69
	global_store_dwordx4 v[66:67], v[70:73], off
	global_store_dwordx4 v[66:67], v[114:117], off offset:1024
	s_waitcnt vmcnt(36)
; __device__ __forceinline__ unsigned pk2(float lo, float hi) { const f32x2 f = {lo, hi}; const bf16n2 v = __builtin_convertvector(f, bf16n2); return __builtin_bit_cast(unsigned, v); }
; #define RW_LOAD_SET(SET, UNIT) do { const bf16_t* ug_ = rwu + (size_t)(UNIT) * 16384; \
;     _Pragma("unroll") for (int ta = 0; ta < 4; ++ta) { An[SET][ta][0] = *(const bf16x8*)(ug_ + ((ta * 2) * 64 + lane) * 8); An[SET][ta][1] = *(const bf16x8*)(ug_ + ((ta * 2 + 1) * 64 + lane) * 8); \
;         Zn[SET][ta] = *(const u32x2*)(ug_ + 4096 + ((cq * 4 + ta) * 64 + lane) * 4); } } while (0)
; template <int SM>
; __device__ __forceinline__ void phase_rwkv_scan(const Ctx& c, const bf16_t* rwu, bf16_t* rws) {
;     ...
;     for (int ch = 0; ch < T / 64; ch += 32) {
; #pragma unroll
;         for (int uu = 0; uu < 32; ++uu) {
;             const int u = uu % RW_SETS;
;             const int unit = (ch + uu) * 8 + h;
;             bf16_t* sg = rws + (size_t)unit * 4096 + cq * 1024 + lane * 8;
;             *(bf16x8*)(sg) = Bhi[0]; *(bf16x8*)(sg + 512) = Bhi[1];
;             f32x4 acc[4];
; #pragma unroll
;             for (int ta = 0; ta < 4; ++ta) { const u32x2 z = Zn[u][ta];
;                 acc[ta] = (f32x4){__uint_as_float(z.x << 16), __uint_as_float(z.x & 0xffff0000u), __uint_as_float(z.y << 16), __uint_as_float(z.y & 0xffff0000u)};
; #pragma unroll
;                 for (int s = 0; s < 2; ++s) acc[ta] = __builtin_amdgcn_mfma_f32_16x16x32_bf16(An[u][ta][s], Bhi[s], acc[ta], 0, 0, 0); }
;             if (SM == 0) RW_LOAD_SET(u, (ch + uu + RW_SETS < T / 64) ? unit + 8 * RW_SETS : unit);
; #pragma unroll
;             for (int s = 0; s < 2; ++s) { u32x4 hi;
;                 hi.x = pk2(acc[2 * s][0], acc[2 * s][1]); hi.y = pk2(acc[2 * s][2], acc[2 * s][3]); hi.z = pk2(acc[2 * s + 1][0], acc[2 * s + 1][1]); hi.w = pk2(acc[2 * s + 1][2], acc[2 * s + 1][3]);
;                 Bhi[s] = __builtin_bit_cast(bf16x8, hi); }
;         }
	v_lshlrev_b32_e32 v66, 16, v176
	v_and_b32_e32 v67, 0xffff0000, v176
	v_lshlrev_b32_e32 v68, 16, v177
	v_and_b32_e32 v69, 0xffff0000, v177
	s_lshl_b64 s[4:5], s[4:5], 15
	s_add_u32 s3, s40, s4
	v_mfma_f32_16x16x32_bf16 v[66:69], v[122:125], v[70:73], v[66:69]
	s_addc_u32 s7, s41, s5
	s_add_u32 s4, s3, 0x100000
	s_addc_u32 s5, s7, 0
	v_mfma_f32_16x16x32_bf16 v[146:149], v[126:129], v[114:117], v[66:69]
	s_add_u32 s6, s3, 0x102000
	s_addc_u32 s7, s7, 0
	s_nop 1
	v_lshlrev_b32_e32 v66, 16, v172
	v_and_b32_e32 v67, 0xffff0000, v172
	v_lshlrev_b32_e32 v68, 16, v173
	v_and_b32_e32 v69, 0xffff0000, v173
	s_nop 1
	v_mfma_f32_16x16x32_bf16 v[66:69], v[106:109], v[70:73], v[66:69]
	v_mfma_f32_16x16x32_bf16 v[106:109], v[110:113], v[114:117], v[66:69]
	s_nop 6
	v_lshlrev_b32_e32 v66, 16, v168
	v_and_b32_e32 v67, 0xffff0000, v168
	v_lshlrev_b32_e32 v68, 16, v169
	v_and_b32_e32 v69, 0xffff0000, v169
	s_nop 1
	v_mfma_f32_16x16x32_bf16 v[66:69], v[90:93], v[70:73], v[66:69]
	v_mfma_f32_16x16x32_bf16 v[110:113], v[94:97], v[114:117], v[66:69]
	s_nop 6
	v_lshlrev_b32_e32 v66, 16, v164
	v_and_b32_e32 v67, 0xffff0000, v164
	v_lshlrev_b32_e32 v68, 16, v165
	v_and_b32_e32 v69, 0xffff0000, v165
	s_nop 1
	v_mfma_f32_16x16x32_bf16 v[66:69], v[74:77], v[70:73], v[66:69]
	v_mfma_f32_16x16x32_bf16 v[74:77], v[78:81], v[114:117], v[66:69]
	global_load_dwordx4 v[122:125], v248, s[4:5]
	global_load_dwordx4 v[126:129], v248, s[4:5] offset:1024
	global_load_dwordx2 v[218:219], v0, s[6:7]
	global_load_dwordx4 v[114:117], v248, s[4:5] offset:2048
	global_load_dwordx4 v[118:121], v248, s[4:5] offset:3072
	global_load_dwordx2 v[176:177], v179, s[6:7]
	global_load_dwordx4 v[90:93], v249, s[4:5]
	global_load_dwordx4 v[94:97], v250, s[4:5]
	global_load_dwordx2 v[172:173], v191, s[6:7]
	global_load_dwordx4 v[66:69], v189, s[4:5]
	global_load_dwordx4 v[70:73], v187, s[4:5]
	global_load_dwordx2 v[170:171], v195, s[6:7]
	s_add_i32 s4, s2, 0x90
	s_ashr_i32 s5, s4, 31
	s_lshl_b64 s[6:7], s[4:5], 13
	v_cvt_pk_bf16_f32 v78, v146, v147
	v_cvt_pk_bf16_f32 v79, v148, v149
	v_cvt_pk_bf16_f32 v80, v106, v107
	v_cvt_pk_bf16_f32 v81, v108, v109
	v_cvt_pk_bf16_f32 v108, v74, v75
	v_lshl_add_u64 v[74:75], v[180:181], 0, s[6:7]
	v_cvt_pk_bf16_f32 v106, v110, v111
	v_cvt_pk_bf16_f32 v107, v112, v113
	v_cvt_pk_bf16_f32 v109, v76, v77
	global_store_dwordx4 v[74:75], v[78:81], off
	global_store_dwordx4 v[74:75], v[106:109], off offset:1024
	s_waitcnt vmcnt(36)
	v_lshlrev_b32_e32 v74, 16, v160
	v_and_b32_e32 v75, 0xffff0000, v160
	v_lshlrev_b32_e32 v76, 16, v161
	v_and_b32_e32 v77, 0xffff0000, v161
	s_lshl_b64 s[4:5], s[4:5], 15
	s_add_u32 s3, s40, s4
	v_mfma_f32_16x16x32_bf16 v[58:61], v[58:61], v[78:81], v[74:77]
	s_addc_u32 s7, s41, s5
	s_add_u32 s4, s3, 0x100000
	s_addc_u32 s5, s7, 0
	v_mfma_f32_16x16x32_bf16 v[58:61], v[62:65], v[106:109], v[58:61]
	v_lshlrev_b32_e32 v62, 16, v158
	v_and_b32_e32 v63, 0xffff0000, v158
	v_lshlrev_b32_e32 v64, 16, v159
	v_and_b32_e32 v65, 0xffff0000, v159
	s_add_u32 s6, s3, 0x102000
	s_addc_u32 s7, s7, 0
	v_mfma_f32_16x16x32_bf16 v[50:53], v[50:53], v[78:81], v[62:65]
	v_mfma_f32_16x16x32_bf16 v[50:53], v[54:57], v[106:109], v[50:53]
	v_lshlrev_b32_e32 v54, 16, v156
	v_and_b32_e32 v55, 0xffff0000, v156
	v_lshlrev_b32_e32 v56, 16, v157
	v_and_b32_e32 v57, 0xffff0000, v157
	s_nop 1
	v_mfma_f32_16x16x32_bf16 v[42:45], v[42:45], v[78:81], v[54:57]
	v_mfma_f32_16x16x32_bf16 v[54:57], v[46:49], v[106:109], v[42:45]
	s_nop 6
	v_lshlrev_b32_e32 v42, 16, v154
	v_and_b32_e32 v43, 0xffff0000, v154
	v_lshlrev_b32_e32 v44, 16, v155
	v_and_b32_e32 v45, 0xffff0000, v155
	s_nop 1
	v_mfma_f32_16x16x32_bf16 v[34:37], v[34:37], v[78:81], v[42:45]
	global_load_dwordx4 v[162:165], v248, s[4:5]
	global_load_dwordx4 v[166:169], v248, s[4:5] offset:1024
	global_load_dwordx2 v[226:227], v0, s[6:7]
	global_load_dwordx4 v[154:157], v248, s[4:5] offset:2048
	global_load_dwordx4 v[158:161], v248, s[4:5] offset:3072
	global_load_dwordx2 v[224:225], v179, s[6:7]
	global_load_dwordx4 v[146:149], v249, s[4:5]
	global_load_dwordx4 v[150:153], v250, s[4:5]
	global_load_dwordx2 v[222:223], v191, s[6:7]
	global_load_dwordx4 v[42:45], v189, s[4:5]
	global_load_dwordx4 v[46:49], v187, s[4:5]
	global_load_dwordx2 v[220:221], v195, s[6:7]
	s_add_i32 s4, s2, 0x98
	s_ashr_i32 s5, s4, 31
	v_mfma_f32_16x16x32_bf16 v[34:37], v[38:41], v[106:109], v[34:37]
	s_lshl_b64 s[6:7], s[4:5], 13
	v_cvt_pk_bf16_f32 v38, v58, v59
	v_cvt_pk_bf16_f32 v39, v60, v61
	v_cvt_pk_bf16_f32 v40, v50, v51
	v_cvt_pk_bf16_f32 v41, v52, v53
	s_nop 2
	v_cvt_pk_bf16_f32 v52, v34, v35
	v_lshl_add_u64 v[34:35], v[180:181], 0, s[6:7]
	v_cvt_pk_bf16_f32 v50, v54, v55
	v_cvt_pk_bf16_f32 v51, v56, v57
	v_cvt_pk_bf16_f32 v53, v36, v37
	global_store_dwordx4 v[34:35], v[38:41], off
	global_store_dwordx4 v[34:35], v[50:53], off offset:1024
	s_waitcnt vmcnt(36)
; __device__ __forceinline__ unsigned pk2(float lo, float hi) { const f32x2 f = {lo, hi}; const bf16n2 v = __builtin_convertvector(f, bf16n2); return __builtin_bit_cast(unsigned, v); }
; #define RW_LOAD_SET(SET, UNIT) do { const bf16_t* ug_ = rwu + (size_t)(UNIT) * 16384; \
;     _Pragma("unroll") for (int ta = 0; ta < 4; ++ta) { An[SET][ta][0] = *(const bf16x8*)(ug_ + ((ta * 2) * 64 + lane) * 8); An[SET][ta][1] = *(const bf16x8*)(ug_ + ((ta * 2 + 1) * 64 + lane) * 8); \
;         Zn[SET][ta] = *(const u32x2*)(ug_ + 4096 + ((cq * 4 + ta) * 64 + lane) * 4); } } while (0)
; template <int SM>
; __device__ __forceinline__ void phase_rwkv_scan(const Ctx& c, const bf16_t* rwu, bf16_t* rws) {
;     ...
;     for (int ch = 0; ch < T / 64; ch += 32) {
; #pragma unroll
;         for (int uu = 0; uu < 32; ++uu) {
;             const int u = uu % RW_SETS;
;             const int unit = (ch + uu) * 8 + h;
;             bf16_t* sg = rws + (size_t)unit * 4096 + cq * 1024 + lane * 8;
;             *(bf16x8*)(sg) = Bhi[0]; *(bf16x8*)(sg + 512) = Bhi[1];
;             f32x4 acc[4];
; #pragma unroll
;             for (int ta = 0; ta < 4; ++ta) { const u32x2 z = Zn[u][ta];
;                 acc[ta] = (f32x4){__uint_as_float(z.x << 16), __uint_as_float(z.x & 0xffff0000u), __uint_as_float(z.y << 16), __uint_as_float(z.y & 0xffff0000u)};
; #pragma unroll
;                 for (int s = 0; s < 2; ++s) acc[ta] = __builtin_amdgcn_mfma_f32_16x16x32_bf16(An[u][ta][s], Bhi[s], acc[ta], 0, 0, 0); }
;             if (SM == 0) RW_LOAD_SET(u, (ch + uu + RW_SETS < T / 64) ? unit + 8 * RW_SETS : unit);
; #pragma unroll
;             for (int s = 0; s < 2; ++s) { u32x4 hi;
;                 hi.x = pk2(acc[2 * s][0], acc[2 * s][1]); hi.y = pk2(acc[2 * s][2], acc[2 * s][3]); hi.z = pk2(acc[2 * s + 1][0], acc[2 * s + 1][1]); hi.w = pk2(acc[2 * s + 1][2], acc[2 * s + 1][3]);
;                 Bhi[s] = __builtin_bit_cast(bf16x8, hi); }
;         }
	v_lshlrev_b32_e32 v34, 16, v208
	v_and_b32_e32 v35, 0xffff0000, v208
	v_lshlrev_b32_e32 v36, 16, v209
	v_and_b32_e32 v37, 0xffff0000, v209
	s_lshl_b64 s[4:5], s[4:5], 15
	s_add_u32 s3, s40, s4
	v_mfma_f32_16x16x32_bf16 v[26:29], v[26:29], v[38:41], v[34:37]
	s_addc_u32 s7, s41, s5
	s_add_u32 s4, s3, 0x100000
	s_addc_u32 s5, s7, 0
	v_mfma_f32_16x16x32_bf16 v[34:37], v[30:33], v[50:53], v[26:29]
	s_add_u32 s6, s3, 0x102000
	s_addc_u32 s7, s7, 0
	s_nop 1
	v_lshlrev_b32_e32 v26, 16, v206
	v_and_b32_e32 v27, 0xffff0000, v206
	v_lshlrev_b32_e32 v28, 16, v207
	v_and_b32_e32 v29, 0xffff0000, v207
	s_nop 1
	v_mfma_f32_16x16x32_bf16 v[18:21], v[18:21], v[38:41], v[26:29]
	v_mfma_f32_16x16x32_bf16 v[18:21], v[22:25], v[50:53], v[18:21]
	v_lshlrev_b32_e32 v22, 16, v204
	v_and_b32_e32 v23, 0xffff0000, v204
	v_lshlrev_b32_e32 v24, 16, v205
	v_and_b32_e32 v25, 0xffff0000, v205
	s_nop 1
	v_mfma_f32_16x16x32_bf16 v[10:13], v[10:13], v[38:41], v[22:25]
	v_mfma_f32_16x16x32_bf16 v[22:25], v[14:17], v[50:53], v[10:13]
	s_nop 6
	v_lshlrev_b32_e32 v10, 16, v202
	v_and_b32_e32 v11, 0xffff0000, v202
	v_lshlrev_b32_e32 v12, 16, v203
	v_and_b32_e32 v13, 0xffff0000, v203
	s_nop 1
	v_mfma_f32_16x16x32_bf16 v[2:5], v[2:5], v[38:41], v[10:13]
	v_mfma_f32_16x16x32_bf16 v[2:5], v[6:9], v[50:53], v[2:5]
	global_load_dwordx4 v[74:77], v248, s[4:5]
	global_load_dwordx4 v[78:81], v248, s[4:5] offset:1024
	global_load_dwordx2 v[212:213], v0, s[6:7]
	global_load_dwordx4 v[50:53], v248, s[4:5] offset:2048
	global_load_dwordx4 v[54:57], v248, s[4:5] offset:3072
	global_load_dwordx2 v[208:209], v179, s[6:7]
	global_load_dwordx4 v[26:29], v249, s[4:5]
	global_load_dwordx4 v[30:33], v250, s[4:5]
	global_load_dwordx2 v[204:205], v191, s[6:7]
	global_load_dwordx4 v[10:13], v189, s[4:5]
	global_load_dwordx4 v[14:17], v187, s[4:5]
	global_load_dwordx2 v[202:203], v195, s[6:7]
	s_add_i32 s4, s2, 0xa0
	s_ashr_i32 s5, s4, 31
	v_cvt_pk_bf16_f32 v6, v34, v35
	v_cvt_pk_bf16_f32 v7, v36, v37
	v_cvt_pk_bf16_f32 v8, v18, v19
	v_cvt_pk_bf16_f32 v9, v20, v21
	s_lshl_b64 s[6:7], s[4:5], 13
	s_waitcnt vmcnt(36)
	v_lshlrev_b32_e32 v34, 16, v210
	v_and_b32_e32 v35, 0xffff0000, v210
	v_lshlrev_b32_e32 v36, 16, v211
	v_and_b32_e32 v37, 0xffff0000, v211
	s_lshl_b64 s[4:5], s[4:5], 15
	s_add_u32 s3, s40, s4
	v_mfma_f32_16x16x32_bf16 v[34:37], v[98:101], v[6:9], v[34:37]
	v_cvt_pk_bf16_f32 v20, v2, v3
	v_lshl_add_u64 v[2:3], v[180:181], 0, s[6:7]
	s_addc_u32 s7, s41, s5
	s_add_u32 s4, s3, 0x100000
	v_cvt_pk_bf16_f32 v18, v22, v23
	v_cvt_pk_bf16_f32 v19, v24, v25
	v_cvt_pk_bf16_f32 v21, v4, v5
	v_lshlrev_b32_e32 v22, 16, v214
	v_and_b32_e32 v23, 0xffff0000, v214
	v_lshlrev_b32_e32 v24, 16, v215
	v_and_b32_e32 v25, 0xffff0000, v215
	s_addc_u32 s5, s7, 0
	global_store_dwordx4 v[2:3], v[6:9], off
	global_store_dwordx4 v[2:3], v[18:21], off offset:1024
	v_lshlrev_b32_e32 v2, 16, v216
	v_and_b32_e32 v3, 0xffff0000, v216
	v_lshlrev_b32_e32 v4, 16, v217
	v_and_b32_e32 v5, 0xffff0000, v217
	v_mfma_f32_16x16x32_bf16 v[22:25], v[130:133], v[6:9], v[22:25]
	s_add_u32 s6, s3, 0x102000
	s_addc_u32 s7, s7, 0
	v_mfma_f32_16x16x32_bf16 v[130:133], v[102:105], v[18:21], v[34:37]
	s_nop 2
	v_lshlrev_b32_e32 v34, 16, v174
	v_and_b32_e32 v35, 0xffff0000, v174
	v_lshlrev_b32_e32 v36, 16, v175
	v_and_b32_e32 v37, 0xffff0000, v175
	v_mfma_f32_16x16x32_bf16 v[2:5], v[138:141], v[6:9], v[2:5]
	s_nop 0
	v_mfma_f32_16x16x32_bf16 v[6:9], v[82:85], v[6:9], v[34:37]
	global_load_dwordx4 v[106:109], v248, s[4:5]
	global_load_dwordx4 v[110:113], v248, s[4:5] offset:1024
	global_load_dwordx2 v[216:217], v0, s[6:7]
	global_load_dwordx4 v[98:101], v248, s[4:5] offset:2048
	global_load_dwordx4 v[102:105], v248, s[4:5] offset:3072
	global_load_dwordx2 v[214:215], v179, s[6:7]
	global_load_dwordx4 v[58:61], v249, s[4:5]
	global_load_dwordx4 v[62:65], v250, s[4:5]
	global_load_dwordx2 v[210:211], v191, s[6:7]
	global_load_dwordx4 v[34:37], v189, s[4:5]
	global_load_dwordx4 v[38:41], v187, s[4:5]
	global_load_dwordx2 v[206:207], v195, s[6:7]
	s_waitcnt vmcnt(36)
	v_lshlrev_b32_e32 v82, 16, v172
	v_and_b32_e32 v83, 0xffff0000, v172
	v_mfma_f32_16x16x32_bf16 v[2:5], v[142:145], v[18:21], v[2:5]
	v_lshlrev_b32_e32 v84, 16, v173
	v_and_b32_e32 v85, 0xffff0000, v173
	s_add_i32 s4, s2, 0xa8
	v_mfma_f32_16x16x32_bf16 v[22:25], v[134:137], v[18:21], v[22:25]
	s_ashr_i32 s5, s4, 31
	s_nop 2
	v_cvt_pk_bf16_f32 v2, v2, v3
	v_cvt_pk_bf16_f32 v3, v4, v5
	v_mfma_f32_16x16x32_bf16 v[6:9], v[86:89], v[18:21], v[6:9]
	s_lshl_b64 s[6:7], s[4:5], 13
	v_cvt_pk_bf16_f32 v4, v22, v23
	v_cvt_pk_bf16_f32 v5, v24, v25
	v_cvt_pk_bf16_f32 v18, v130, v131
	v_cvt_pk_bf16_f32 v19, v132, v133
	v_mfma_f32_16x16x32_bf16 v[82:85], v[90:93], v[2:5], v[82:85]
	s_nop 1
	v_cvt_pk_bf16_f32 v20, v6, v7
	v_cvt_pk_bf16_f32 v21, v8, v9
	v_lshl_add_u64 v[6:7], v[180:181], 0, s[6:7]
	global_store_dwordx4 v[6:7], v[2:5], off
	global_store_dwordx4 v[6:7], v[18:21], off offset:1024
	v_lshlrev_b32_e32 v6, 16, v218
	v_and_b32_e32 v7, 0xffff0000, v218
	v_lshlrev_b32_e32 v8, 16, v219
	v_and_b32_e32 v9, 0xffff0000, v219
	v_lshlrev_b32_e32 v22, 16, v176
	v_and_b32_e32 v23, 0xffff0000, v176
	v_lshlrev_b32_e32 v24, 16, v177
	v_and_b32_e32 v25, 0xffff0000, v177
	v_mfma_f32_16x16x32_bf16 v[130:133], v[94:97], v[18:21], v[82:85]
	s_lshl_b64 s[4:5], s[4:5], 15
	s_add_u32 s3, s40, s4
	s_addc_u32 s7, s41, s5
	v_lshlrev_b32_e32 v82, 16, v170
	v_and_b32_e32 v83, 0xffff0000, v170
	v_lshlrev_b32_e32 v84, 16, v171
	v_and_b32_e32 v85, 0xffff0000, v171
	v_mfma_f32_16x16x32_bf16 v[6:9], v[122:125], v[2:5], v[6:9]
	s_add_u32 s4, s3, 0x100000
	s_addc_u32 s5, s7, 0
	s_add_u32 s6, s3, 0x102000
	v_mfma_f32_16x16x32_bf16 v[22:25], v[114:117], v[2:5], v[22:25]
	s_addc_u32 s7, s7, 0
	v_mfma_f32_16x16x32_bf16 v[2:5], v[66:69], v[2:5], v[82:85]
	v_mfma_f32_16x16x32_bf16 v[6:9], v[126:129], v[18:21], v[6:9]
	v_mfma_f32_16x16x32_bf16 v[22:25], v[118:121], v[18:21], v[22:25]
	global_load_dwordx4 v[122:125], v248, s[4:5]
	global_load_dwordx4 v[126:129], v248, s[4:5] offset:1024
	global_load_dwordx2 v[176:177], v0, s[6:7]
	global_load_dwordx4 v[114:117], v248, s[4:5] offset:2048
	global_load_dwordx4 v[118:121], v248, s[4:5] offset:3072
	global_load_dwordx2 v[174:175], v179, s[6:7]
	global_load_dwordx4 v[90:93], v249, s[4:5]
	global_load_dwordx4 v[94:97], v250, s[4:5]
	global_load_dwordx2 v[172:173], v191, s[6:7]
	global_load_dwordx4 v[82:85], v189, s[4:5]
	global_load_dwordx4 v[86:89], v187, s[4:5]
	global_load_dwordx2 v[170:171], v195, s[6:7]
	s_add_i32 s4, s2, 0xb0
	s_ashr_i32 s5, s4, 31
	v_mfma_f32_16x16x32_bf16 v[2:5], v[70:73], v[18:21], v[2:5]
	s_lshl_b64 s[6:7], s[4:5], 13
	v_cvt_pk_bf16_f32 v6, v6, v7
	v_cvt_pk_bf16_f32 v7, v8, v9
	v_cvt_pk_bf16_f32 v8, v22, v23
	v_cvt_pk_bf16_f32 v9, v24, v25
	s_nop 2
	v_cvt_pk_bf16_f32 v20, v2, v3
	v_lshl_add_u64 v[2:3], v[180:181], 0, s[6:7]
	v_cvt_pk_bf16_f32 v18, v130, v131
	v_cvt_pk_bf16_f32 v19, v132, v133
	v_cvt_pk_bf16_f32 v21, v4, v5
	global_store_dwordx4 v[2:3], v[6:9], off
	global_store_dwordx4 v[2:3], v[18:21], off offset:1024
	s_waitcnt vmcnt(36)
; __device__ __forceinline__ unsigned pk2(float lo, float hi) { const f32x2 f = {lo, hi}; const bf16n2 v = __builtin_convertvector(f, bf16n2); return __builtin_bit_cast(unsigned, v); }
; #define RW_LOAD_SET(SET, UNIT) do { const bf16_t* ug_ = rwu + (size_t)(UNIT) * 16384; \
;     _Pragma("unroll") for (int ta = 0; ta < 4; ++ta) { An[SET][ta][0] = *(const bf16x8*)(ug_ + ((ta * 2) * 64 + lane) * 8); An[SET][ta][1] = *(const bf16x8*)(ug_ + ((ta * 2 + 1) * 64 + lane) * 8); \
;         Zn[SET][ta] = *(const u32x2*)(ug_ + 4096 + ((cq * 4 + ta) * 64 + lane) * 4); } } while (0)
; template <int SM>
; __device__ __forceinline__ void phase_rwkv_scan(const Ctx& c, const bf16_t* rwu, bf16_t* rws) {
;     ...
;     for (int ch = 0; ch < T / 64; ch += 32) {
; #pragma unroll
;         for (int uu = 0; uu < 32; ++uu) {
;             const int u = uu % RW_SETS;
;             const int unit = (ch + uu) * 8 + h;
;             bf16_t* sg = rws + (size_t)unit * 4096 + cq * 1024 + lane * 8;
;             *(bf16x8*)(sg) = Bhi[0]; *(bf16x8*)(sg + 512) = Bhi[1];
;             f32x4 acc[4];
; #pragma unroll
;             for (int ta = 0; ta < 4; ++ta) { const u32x2 z = Zn[u][ta];
;                 acc[ta] = (f32x4){__uint_as_float(z.x << 16), __uint_as_float(z.x & 0xffff0000u), __uint_as_float(z.y << 16), __uint_as_float(z.y & 0xffff0000u)};
; #pragma unroll
;                 for (int s = 0; s < 2; ++s) acc[ta] = __builtin_amdgcn_mfma_f32_16x16x32_bf16(An[u][ta][s], Bhi[s], acc[ta], 0, 0, 0); }
;             if (SM == 0) RW_LOAD_SET(u, (ch + uu + RW_SETS < T / 64) ? unit + 8 * RW_SETS : unit);
; #pragma unroll
;             for (int s = 0; s < 2; ++s) { u32x4 hi;
;                 hi.x = pk2(acc[2 * s][0], acc[2 * s][1]); hi.y = pk2(acc[2 * s][2], acc[2 * s][3]); hi.z = pk2(acc[2 * s + 1][0], acc[2 * s + 1][1]); hi.w = pk2(acc[2 * s + 1][2], acc[2 * s + 1][3]);
;                 Bhi[s] = __builtin_bit_cast(bf16x8, hi); }
;         }
	v_lshlrev_b32_e32 v2, 16, v226
	v_and_b32_e32 v3, 0xffff0000, v226
	v_lshlrev_b32_e32 v4, 16, v227
	v_and_b32_e32 v5, 0xffff0000, v227
	s_lshl_b64 s[4:5], s[4:5], 15
	s_add_u32 s3, s40, s4
	v_mfma_f32_16x16x32_bf16 v[2:5], v[162:165], v[6:9], v[2:5]
	s_addc_u32 s7, s41, s5
	s_add_u32 s4, s3, 0x100000
	s_addc_u32 s5, s7, 0
	v_mfma_f32_16x16x32_bf16 v[130:133], v[166:169], v[18:21], v[2:5]
	s_add_u32 s6, s3, 0x102000
	s_addc_u32 s7, s7, 0
	s_nop 1
	v_lshlrev_b32_e32 v2, 16, v224
	v_and_b32_e32 v3, 0xffff0000, v224
	v_lshlrev_b32_e32 v4, 16, v225
	v_and_b32_e32 v5, 0xffff0000, v225
	s_nop 1
	v_mfma_f32_16x16x32_bf16 v[2:5], v[154:157], v[6:9], v[2:5]
	v_mfma_f32_16x16x32_bf16 v[134:137], v[158:161], v[18:21], v[2:5]
	s_nop 6
	v_lshlrev_b32_e32 v2, 16, v222
	v_and_b32_e32 v3, 0xffff0000, v222
	v_lshlrev_b32_e32 v4, 16, v223
	v_and_b32_e32 v5, 0xffff0000, v223
	s_nop 1
	v_mfma_f32_16x16x32_bf16 v[2:5], v[146:149], v[6:9], v[2:5]
	v_cvt_pk_bf16_f32 v146, v130, v131
	v_cvt_pk_bf16_f32 v147, v132, v133
	v_cvt_pk_bf16_f32 v148, v134, v135
	v_mfma_f32_16x16x32_bf16 v[138:141], v[150:153], v[18:21], v[2:5]
	v_cvt_pk_bf16_f32 v149, v136, v137
	s_waitcnt vmcnt(33)
	v_lshlrev_b32_e32 v132, 16, v213
	v_and_b32_e32 v133, 0xffff0000, v213
	s_nop 0
	v_lshlrev_b32_e32 v2, 16, v220
	v_and_b32_e32 v3, 0xffff0000, v220
	v_lshlrev_b32_e32 v4, 16, v221
	v_and_b32_e32 v5, 0xffff0000, v221
	v_cvt_pk_bf16_f32 v150, v138, v139
	v_cvt_pk_bf16_f32 v151, v140, v141
	v_mfma_f32_16x16x32_bf16 v[2:5], v[42:45], v[6:9], v[2:5]
	v_mfma_f32_16x16x32_bf16 v[142:145], v[46:49], v[18:21], v[2:5]
	global_load_dwordx4 v[66:69], v248, s[4:5]
	global_load_dwordx4 v[70:73], v248, s[4:5] offset:1024
	global_load_dwordx2 v[160:161], v0, s[6:7]
	global_load_dwordx4 v[42:45], v248, s[4:5] offset:2048
	global_load_dwordx4 v[46:49], v248, s[4:5] offset:3072
	global_load_dwordx2 v[158:159], v179, s[6:7]
	global_load_dwordx4 v[18:21], v249, s[4:5]
	global_load_dwordx4 v[22:25], v250, s[4:5]
	global_load_dwordx2 v[156:157], v191, s[6:7]
	global_load_dwordx4 v[2:5], v189, s[4:5]
	global_load_dwordx4 v[6:9], v187, s[4:5]
	global_load_dwordx2 v[154:155], v195, s[6:7]
	s_add_i32 s4, s2, 0xb8
	s_ashr_i32 s5, s4, 31
	s_lshl_b64 s[6:7], s[4:5], 13
	v_lshl_add_u64 v[130:131], v[180:181], 0, s[6:7]
	v_cvt_pk_bf16_f32 v152, v142, v143
	v_cvt_pk_bf16_f32 v153, v144, v145
	global_store_dwordx4 v[130:131], v[146:149], off
	global_store_dwordx4 v[130:131], v[150:153], off offset:1024
	v_lshlrev_b32_e32 v130, 16, v212
	v_and_b32_e32 v131, 0xffff0000, v212
	s_lshl_b64 s[4:5], s[4:5], 15
	s_add_u32 s3, s40, s4
	v_mfma_f32_16x16x32_bf16 v[74:77], v[74:77], v[146:149], v[130:133]
	s_addc_u32 s7, s41, s5
	s_add_u32 s4, s3, 0x100000
	s_addc_u32 s5, s7, 0
	v_mfma_f32_16x16x32_bf16 v[130:133], v[78:81], v[150:153], v[74:77]
	s_add_u32 s6, s3, 0x102000
	s_addc_u32 s7, s7, 0
	s_nop 1
	s_waitcnt vmcnt(36)
	v_lshlrev_b32_e32 v74, 16, v208
	v_and_b32_e32 v75, 0xffff0000, v208
	v_lshlrev_b32_e32 v76, 16, v209
	v_and_b32_e32 v77, 0xffff0000, v209
	s_nop 1
	v_mfma_f32_16x16x32_bf16 v[50:53], v[50:53], v[146:149], v[74:77]
	v_mfma_f32_16x16x32_bf16 v[134:137], v[54:57], v[150:153], v[50:53]
	s_nop 6
	v_lshlrev_b32_e32 v50, 16, v204
	v_and_b32_e32 v51, 0xffff0000, v204
	v_lshlrev_b32_e32 v52, 16, v205
	v_and_b32_e32 v53, 0xffff0000, v205
	s_nop 1
	v_mfma_f32_16x16x32_bf16 v[26:29], v[26:29], v[146:149], v[50:53]
	v_mfma_f32_16x16x32_bf16 v[138:141], v[30:33], v[150:153], v[26:29]
	s_nop 6
	v_lshlrev_b32_e32 v26, 16, v202
	v_and_b32_e32 v27, 0xffff0000, v202
	v_lshlrev_b32_e32 v28, 16, v203
	v_and_b32_e32 v29, 0xffff0000, v203
	s_nop 1
	v_mfma_f32_16x16x32_bf16 v[10:13], v[10:13], v[146:149], v[26:29]
	v_cvt_pk_bf16_f32 v146, v130, v131
	v_cvt_pk_bf16_f32 v147, v132, v133
	v_cvt_pk_bf16_f32 v148, v134, v135
	v_mfma_f32_16x16x32_bf16 v[142:145], v[14:17], v[150:153], v[10:13]
	global_load_dwordx4 v[74:77], v248, s[4:5]
	global_load_dwordx4 v[78:81], v248, s[4:5] offset:1024
	global_load_dwordx2 v[212:213], v0, s[6:7]
	global_load_dwordx4 v[50:53], v248, s[4:5] offset:2048
	global_load_dwordx4 v[54:57], v248, s[4:5] offset:3072
	global_load_dwordx2 v[208:209], v179, s[6:7]
	global_load_dwordx4 v[26:29], v249, s[4:5]
	global_load_dwordx4 v[30:33], v250, s[4:5]
	global_load_dwordx2 v[204:205], v191, s[6:7]
	global_load_dwordx4 v[10:13], v189, s[4:5]
	global_load_dwordx4 v[14:17], v187, s[4:5]
	global_load_dwordx2 v[202:203], v195, s[6:7]
	s_add_i32 s4, s2, 0xc0
	s_ashr_i32 s5, s4, 31
	s_lshl_b64 s[6:7], s[4:5], 13
	v_cvt_pk_bf16_f32 v149, v136, v137
	v_lshl_add_u64 v[130:131], v[180:181], 0, s[6:7]
	v_cvt_pk_bf16_f32 v150, v138, v139
	v_cvt_pk_bf16_f32 v151, v140, v141
	v_cvt_pk_bf16_f32 v152, v142, v143
	v_cvt_pk_bf16_f32 v153, v144, v145
	global_store_dwordx4 v[130:131], v[146:149], off
	global_store_dwordx4 v[130:131], v[150:153], off offset:1024
	s_waitcnt vmcnt(36)
	v_lshlrev_b32_e32 v130, 16, v216
	v_and_b32_e32 v131, 0xffff0000, v216
	v_lshlrev_b32_e32 v132, 16, v217
	v_and_b32_e32 v133, 0xffff0000, v217
	s_lshl_b64 s[4:5], s[4:5], 15
	s_add_u32 s3, s40, s4
	v_mfma_f32_16x16x32_bf16 v[106:109], v[106:109], v[146:149], v[130:133]
	s_addc_u32 s7, s41, s5
	s_add_u32 s4, s3, 0x100000
	s_addc_u32 s5, s7, 0
	v_mfma_f32_16x16x32_bf16 v[130:133], v[110:113], v[150:153], v[106:109]
	s_add_u32 s6, s3, 0x102000
	s_addc_u32 s7, s7, 0
	s_nop 1
	v_lshlrev_b32_e32 v106, 16, v214
	v_and_b32_e32 v107, 0xffff0000, v214
	v_lshlrev_b32_e32 v108, 16, v215
	v_and_b32_e32 v109, 0xffff0000, v215
	v_cvt_pk_bf16_f32 v130, v130, v131
	v_cvt_pk_bf16_f32 v131, v132, v133
	v_mfma_f32_16x16x32_bf16 v[98:101], v[98:101], v[146:149], v[106:109]
	v_mfma_f32_16x16x32_bf16 v[134:137], v[102:105], v[150:153], v[98:101]
	s_nop 6
	v_lshlrev_b32_e32 v98, 16, v210
	v_and_b32_e32 v99, 0xffff0000, v210
	v_lshlrev_b32_e32 v100, 16, v211
	v_and_b32_e32 v101, 0xffff0000, v211
	v_cvt_pk_bf16_f32 v132, v134, v135
	v_cvt_pk_bf16_f32 v133, v136, v137
	v_mfma_f32_16x16x32_bf16 v[58:61], v[58:61], v[146:149], v[98:101]
	v_mfma_f32_16x16x32_bf16 v[138:141], v[62:65], v[150:153], v[58:61]
	s_nop 6
	v_lshlrev_b32_e32 v58, 16, v206
	v_and_b32_e32 v59, 0xffff0000, v206
	v_lshlrev_b32_e32 v60, 16, v207
	v_and_b32_e32 v61, 0xffff0000, v207
	v_cvt_pk_bf16_f32 v134, v138, v139
	v_cvt_pk_bf16_f32 v135, v140, v141
	v_mfma_f32_16x16x32_bf16 v[34:37], v[34:37], v[146:149], v[58:61]
	s_waitcnt vmcnt(33)
; __device__ __forceinline__ unsigned pk2(float lo, float hi) { const f32x2 f = {lo, hi}; const bf16n2 v = __builtin_convertvector(f, bf16n2); return __builtin_bit_cast(unsigned, v); }
; #define RW_LOAD_SET(SET, UNIT) do { const bf16_t* ug_ = rwu + (size_t)(UNIT) * 16384; \
;     _Pragma("unroll") for (int ta = 0; ta < 4; ++ta) { An[SET][ta][0] = *(const bf16x8*)(ug_ + ((ta * 2) * 64 + lane) * 8); An[SET][ta][1] = *(const bf16x8*)(ug_ + ((ta * 2 + 1) * 64 + lane) * 8); \
;         Zn[SET][ta] = *(const u32x2*)(ug_ + 4096 + ((cq * 4 + ta) * 64 + lane) * 4); } } while (0)
; template <int SM>
; __device__ __forceinline__ void phase_rwkv_scan(const Ctx& c, const bf16_t* rwu, bf16_t* rws) {
;     ...
;     for (int ch = 0; ch < T / 64; ch += 32) {
; #pragma unroll
;         for (int uu = 0; uu < 32; ++uu) {
;             const int u = uu % RW_SETS;
;             const int unit = (ch + uu) * 8 + h;
;             bf16_t* sg = rws + (size_t)unit * 4096 + cq * 1024 + lane * 8;
;             *(bf16x8*)(sg) = Bhi[0]; *(bf16x8*)(sg + 512) = Bhi[1];
;             f32x4 acc[4];
; #pragma unroll
;             for (int ta = 0; ta < 4; ++ta) { const u32x2 z = Zn[u][ta];
;                 acc[ta] = (f32x4){__uint_as_float(z.x << 16), __uint_as_float(z.x & 0xffff0000u), __uint_as_float(z.y << 16), __uint_as_float(z.y & 0xffff0000u)};
; #pragma unroll
;                 for (int s = 0; s < 2; ++s) acc[ta] = __builtin_amdgcn_mfma_f32_16x16x32_bf16(An[u][ta][s], Bhi[s], acc[ta], 0, 0, 0); }
;             if (SM == 0) RW_LOAD_SET(u, (ch + uu + RW_SETS < T / 64) ? unit + 8 * RW_SETS : unit);
; #pragma unroll
;             for (int s = 0; s < 2; ++s) { u32x4 hi;
;                 hi.x = pk2(acc[2 * s][0], acc[2 * s][1]); hi.y = pk2(acc[2 * s][2], acc[2 * s][3]); hi.z = pk2(acc[2 * s + 1][0], acc[2 * s + 1][1]); hi.w = pk2(acc[2 * s + 1][2], acc[2 * s + 1][3]);
;                 Bhi[s] = __builtin_bit_cast(bf16x8, hi); }
;         }
	v_lshlrev_b32_e32 v140, 16, v177
	v_and_b32_e32 v141, 0xffff0000, v177
	v_mfma_f32_16x16x32_bf16 v[142:145], v[38:41], v[150:153], v[34:37]
	global_load_dwordx4 v[106:109], v248, s[4:5]
	global_load_dwordx4 v[110:113], v248, s[4:5] offset:1024
	global_load_dwordx2 v[216:217], v0, s[6:7]
	global_load_dwordx4 v[98:101], v248, s[4:5] offset:2048
	global_load_dwordx4 v[102:105], v248, s[4:5] offset:3072
	global_load_dwordx2 v[214:215], v179, s[6:7]
	global_load_dwordx4 v[58:61], v249, s[4:5]
	global_load_dwordx4 v[62:65], v250, s[4:5]
	global_load_dwordx2 v[210:211], v191, s[6:7]
	global_load_dwordx4 v[34:37], v189, s[4:5]
	global_load_dwordx4 v[38:41], v187, s[4:5]
	global_load_dwordx2 v[206:207], v195, s[6:7]
	s_add_i32 s4, s2, 0xc8
	s_ashr_i32 s5, s4, 31
	s_lshl_b64 s[6:7], s[4:5], 13
	v_lshl_add_u64 v[138:139], v[180:181], 0, s[6:7]
	v_cvt_pk_bf16_f32 v136, v142, v143
	v_cvt_pk_bf16_f32 v137, v144, v145
	global_store_dwordx4 v[138:139], v[130:133], off
	global_store_dwordx4 v[138:139], v[134:137], off offset:1024
	v_lshlrev_b32_e32 v138, 16, v176
	v_and_b32_e32 v139, 0xffff0000, v176
	s_lshl_b64 s[4:5], s[4:5], 15
	s_add_u32 s3, s40, s4
	v_mfma_f32_16x16x32_bf16 v[122:125], v[122:125], v[130:133], v[138:141]
	s_addc_u32 s7, s41, s5
	s_add_u32 s4, s3, 0x100000
	s_addc_u32 s5, s7, 0
	v_mfma_f32_16x16x32_bf16 v[146:149], v[126:129], v[134:137], v[122:125]
	s_add_u32 s6, s3, 0x102000
	s_addc_u32 s7, s7, 0
	s_nop 1
	s_waitcnt vmcnt(36)
	v_lshlrev_b32_e32 v122, 16, v174
	v_and_b32_e32 v123, 0xffff0000, v174
	v_lshlrev_b32_e32 v124, 16, v175
	v_and_b32_e32 v125, 0xffff0000, v175
	s_nop 1
	v_mfma_f32_16x16x32_bf16 v[114:117], v[114:117], v[130:133], v[122:125]
	v_mfma_f32_16x16x32_bf16 v[150:153], v[118:121], v[134:137], v[114:117]
	s_nop 6
	v_lshlrev_b32_e32 v114, 16, v172
	v_and_b32_e32 v115, 0xffff0000, v172
	v_lshlrev_b32_e32 v116, 16, v173
	v_and_b32_e32 v117, 0xffff0000, v173
	s_nop 1
	v_mfma_f32_16x16x32_bf16 v[90:93], v[90:93], v[130:133], v[114:117]
	v_mfma_f32_16x16x32_bf16 v[90:93], v[94:97], v[134:137], v[90:93]
	v_lshlrev_b32_e32 v94, 16, v170
	v_and_b32_e32 v95, 0xffff0000, v170
	v_lshlrev_b32_e32 v96, 16, v171
	v_and_b32_e32 v97, 0xffff0000, v171
	s_nop 1
	v_mfma_f32_16x16x32_bf16 v[82:85], v[82:85], v[130:133], v[94:97]
	s_nop 0
	v_cvt_pk_bf16_f32 v90, v90, v91
	v_cvt_pk_bf16_f32 v91, v92, v93
	v_mfma_f32_16x16x32_bf16 v[82:85], v[86:89], v[134:137], v[82:85]
	global_load_dwordx4 v[138:141], v248, s[4:5]
	global_load_dwordx4 v[142:145], v248, s[4:5] offset:1024
	global_load_dwordx2 v[232:233], v0, s[6:7]
	global_load_dwordx4 v[130:133], v248, s[4:5] offset:2048
	global_load_dwordx4 v[134:137], v248, s[4:5] offset:3072
	global_load_dwordx2 v[230:231], v179, s[6:7]
	global_load_dwordx4 v[122:125], v249, s[4:5]
	global_load_dwordx4 v[126:129], v250, s[4:5]
	global_load_dwordx2 v[228:229], v191, s[6:7]
	global_load_dwordx4 v[114:117], v189, s[4:5]
	global_load_dwordx4 v[118:121], v187, s[4:5]
	global_load_dwordx2 v[226:227], v195, s[6:7]
	s_add_i32 s4, s2, 0xd0
	s_ashr_i32 s5, s4, 31
	s_lshl_b64 s[6:7], s[4:5], 13
	v_cvt_pk_bf16_f32 v86, v146, v147
	v_cvt_pk_bf16_f32 v87, v148, v149
	v_cvt_pk_bf16_f32 v88, v150, v151
	v_cvt_pk_bf16_f32 v89, v152, v153
	v_cvt_pk_bf16_f32 v92, v82, v83
	v_lshl_add_u64 v[82:83], v[180:181], 0, s[6:7]
	v_cvt_pk_bf16_f32 v93, v84, v85
	global_store_dwordx4 v[82:83], v[86:89], off
	global_store_dwordx4 v[82:83], v[90:93], off offset:1024
	s_waitcnt vmcnt(36)
	v_lshlrev_b32_e32 v82, 16, v160
	v_and_b32_e32 v83, 0xffff0000, v160
	v_lshlrev_b32_e32 v84, 16, v161
	v_and_b32_e32 v85, 0xffff0000, v161
	s_lshl_b64 s[4:5], s[4:5], 15
	s_add_u32 s3, s40, s4
	v_mfma_f32_16x16x32_bf16 v[66:69], v[66:69], v[86:89], v[82:85]
	s_addc_u32 s7, s41, s5
	s_add_u32 s4, s3, 0x100000
	s_addc_u32 s5, s7, 0
	v_mfma_f32_16x16x32_bf16 v[66:69], v[70:73], v[90:93], v[66:69]
	v_lshlrev_b32_e32 v70, 16, v158
	v_and_b32_e32 v71, 0xffff0000, v158
	v_lshlrev_b32_e32 v72, 16, v159
	v_and_b32_e32 v73, 0xffff0000, v159
	s_add_u32 s6, s3, 0x102000
	s_addc_u32 s7, s7, 0
	v_mfma_f32_16x16x32_bf16 v[42:45], v[42:45], v[86:89], v[70:73]
	s_addk_i32 s2, 0xd8
	s_ashr_i32 s3, s2, 31
	v_mfma_f32_16x16x32_bf16 v[42:45], v[46:49], v[90:93], v[42:45]
	v_lshlrev_b32_e32 v46, 16, v156
	v_and_b32_e32 v47, 0xffff0000, v156
	v_lshlrev_b32_e32 v48, 16, v157
	v_and_b32_e32 v49, 0xffff0000, v157
	s_nop 1
	v_mfma_f32_16x16x32_bf16 v[18:21], v[18:21], v[86:89], v[46:49]
	v_mfma_f32_16x16x32_bf16 v[18:21], v[22:25], v[90:93], v[18:21]
	v_lshlrev_b32_e32 v22, 16, v154
	v_and_b32_e32 v23, 0xffff0000, v154
	v_lshlrev_b32_e32 v24, 16, v155
	v_and_b32_e32 v25, 0xffff0000, v155
	global_load_dwordx4 v[170:173], v248, s[4:5]
	global_load_dwordx4 v[174:177], v248, s[4:5] offset:1024
	global_load_dwordx2 v[240:241], v0, s[6:7]
	global_load_dwordx4 v[162:165], v248, s[4:5] offset:2048
	global_load_dwordx4 v[166:169], v248, s[4:5] offset:3072
	global_load_dwordx2 v[238:239], v179, s[6:7]
	global_load_dwordx4 v[154:157], v249, s[4:5]
	global_load_dwordx4 v[158:161], v250, s[4:5]
	global_load_dwordx2 v[236:237], v191, s[6:7]
	global_load_dwordx4 v[146:149], v189, s[4:5]
	global_load_dwordx4 v[150:153], v187, s[4:5]
	global_load_dwordx2 v[234:235], v195, s[6:7]
	v_mfma_f32_16x16x32_bf16 v[2:5], v[2:5], v[86:89], v[22:25]
	s_lshl_b64 s[4:5], s[2:3], 13
	v_cvt_pk_bf16_f32 v18, v18, v19
	v_cvt_pk_bf16_f32 v19, v20, v21
	v_mfma_f32_16x16x32_bf16 v[2:5], v[6:9], v[90:93], v[2:5]
	v_cvt_pk_bf16_f32 v6, v66, v67
	v_cvt_pk_bf16_f32 v7, v68, v69
	v_cvt_pk_bf16_f32 v8, v42, v43
	v_cvt_pk_bf16_f32 v9, v44, v45
	s_waitcnt vmcnt(36)
; __device__ __forceinline__ unsigned pk2(float lo, float hi) { const f32x2 f = {lo, hi}; const bf16n2 v = __builtin_convertvector(f, bf16n2); return __builtin_bit_cast(unsigned, v); }
; #define RW_LOAD_SET(SET, UNIT) do { const bf16_t* ug_ = rwu + (size_t)(UNIT) * 16384; \
;     _Pragma("unroll") for (int ta = 0; ta < 4; ++ta) { An[SET][ta][0] = *(const bf16x8*)(ug_ + ((ta * 2) * 64 + lane) * 8); An[SET][ta][1] = *(const bf16x8*)(ug_ + ((ta * 2 + 1) * 64 + lane) * 8); \
;         Zn[SET][ta] = *(const u32x2*)(ug_ + 4096 + ((cq * 4 + ta) * 64 + lane) * 4); } } while (0)
; template <int SM>
; __device__ __forceinline__ void phase_rwkv_scan(const Ctx& c, const bf16_t* rwu, bf16_t* rws) {
;     ...
;     for (int ch = 0; ch < T / 64; ch += 32) {
; #pragma unroll
;         for (int uu = 0; uu < 32; ++uu) {
;             const int u = uu % RW_SETS;
;             const int unit = (ch + uu) * 8 + h;
;             bf16_t* sg = rws + (size_t)unit * 4096 + cq * 1024 + lane * 8;
;             *(bf16x8*)(sg) = Bhi[0]; *(bf16x8*)(sg + 512) = Bhi[1];
;             f32x4 acc[4];
; #pragma unroll
;             for (int ta = 0; ta < 4; ++ta) { const u32x2 z = Zn[u][ta];
;                 acc[ta] = (f32x4){__uint_as_float(z.x << 16), __uint_as_float(z.x & 0xffff0000u), __uint_as_float(z.y << 16), __uint_as_float(z.y & 0xffff0000u)};
; #pragma unroll
;                 for (int s = 0; s < 2; ++s) acc[ta] = __builtin_amdgcn_mfma_f32_16x16x32_bf16(An[u][ta][s], Bhi[s], acc[ta], 0, 0, 0); }
;             if (SM == 0) RW_LOAD_SET(u, (ch + uu + RW_SETS < T / 64) ? unit + 8 * RW_SETS : unit);
; #pragma unroll
;             for (int s = 0; s < 2; ++s) { u32x4 hi;
;                 hi.x = pk2(acc[2 * s][0], acc[2 * s][1]); hi.y = pk2(acc[2 * s][2], acc[2 * s][3]); hi.z = pk2(acc[2 * s + 1][0], acc[2 * s + 1][1]); hi.w = pk2(acc[2 * s + 1][2], acc[2 * s + 1][3]);
;                 Bhi[s] = __builtin_bit_cast(bf16x8, hi); }
;         }
	v_lshlrev_b32_e32 v42, 16, v204
	v_and_b32_e32 v43, 0xffff0000, v204
	v_lshlrev_b32_e32 v44, 16, v205
	v_and_b32_e32 v45, 0xffff0000, v205
	v_cvt_pk_bf16_f32 v20, v2, v3
	v_lshl_add_u64 v[2:3], v[180:181], 0, s[4:5]
	v_mfma_f32_16x16x32_bf16 v[26:29], v[26:29], v[6:9], v[42:45]
	s_lshl_b64 s[2:3], s[2:3], 15
	v_cvt_pk_bf16_f32 v21, v4, v5
	global_store_dwordx4 v[2:3], v[6:9], off
	global_store_dwordx4 v[2:3], v[18:21], off offset:1024
	v_lshlrev_b32_e32 v2, 16, v212
	v_and_b32_e32 v3, 0xffff0000, v212
	v_lshlrev_b32_e32 v4, 16, v213
	v_and_b32_e32 v5, 0xffff0000, v213
	s_add_u32 s4, s40, s2
	v_lshlrev_b32_e32 v22, 16, v208
	v_mfma_f32_16x16x32_bf16 v[2:5], v[74:77], v[6:9], v[2:5]
	v_and_b32_e32 v23, 0xffff0000, v208
	v_lshlrev_b32_e32 v24, 16, v209
	v_and_b32_e32 v25, 0xffff0000, v209
	v_mfma_f32_16x16x32_bf16 v[26:29], v[30:33], v[18:21], v[26:29]
	v_lshlrev_b32_e32 v30, 16, v202
	v_and_b32_e32 v31, 0xffff0000, v202
	v_lshlrev_b32_e32 v32, 16, v203
	v_and_b32_e32 v33, 0xffff0000, v203
	s_addc_u32 s5, s41, s3
	v_mfma_f32_16x16x32_bf16 v[22:25], v[50:53], v[6:9], v[22:25]
	s_add_u32 s2, s4, 0x100000
	s_addc_u32 s3, s5, 0
	s_add_u32 s4, s4, 0x102000
	v_mfma_f32_16x16x32_bf16 v[6:9], v[10:13], v[6:9], v[30:33]
	s_addc_u32 s5, s5, 0
	s_waitcnt vmcnt(33)
	v_lshlrev_b32_e32 v12, 16, v217
	v_and_b32_e32 v13, 0xffff0000, v217
	v_mfma_f32_16x16x32_bf16 v[2:5], v[78:81], v[18:21], v[2:5]
	global_load_dwordx4 v[90:93], v248, s[2:3]
	global_load_dwordx4 v[94:97], v248, s[2:3] offset:1024
	global_load_dwordx2 v[224:225], v0, s[4:5]
	global_load_dwordx4 v[82:85], v248, s[2:3] offset:2048
	global_load_dwordx4 v[86:89], v248, s[2:3] offset:3072
	global_load_dwordx2 v[222:223], v179, s[4:5]
	global_load_dwordx4 v[74:77], v249, s[2:3]
	global_load_dwordx4 v[78:81], v250, s[2:3]
	global_load_dwordx2 v[220:221], v191, s[4:5]
	global_load_dwordx4 v[66:69], v189, s[2:3]
	global_load_dwordx4 v[70:73], v187, s[2:3]
	global_load_dwordx2 v[218:219], v195, s[4:5]
	s_or_b32 s4, s1, 28
	s_lshl_b32 s2, s4, 3
	v_mfma_f32_16x16x32_bf16 v[22:25], v[54:57], v[18:21], v[22:25]
	s_add_i32 s2, s2, s0
	s_ashr_i32 s3, s2, 31
	s_lshl_b64 s[6:7], s[2:3], 13
	v_mfma_f32_16x16x32_bf16 v[8:11], v[14:17], v[18:21], v[6:9]
	v_cvt_pk_bf16_f32 v2, v2, v3
	v_cvt_pk_bf16_f32 v3, v4, v5
	s_nop 1
	v_cvt_pk_bf16_f32 v4, v22, v23
	v_cvt_pk_bf16_f32 v5, v24, v25
	v_cvt_pk_bf16_f32 v6, v26, v27
	s_nop 0
	v_cvt_pk_bf16_f32 v8, v8, v9
	v_cvt_pk_bf16_f32 v9, v10, v11
	v_lshl_add_u64 v[10:11], v[180:181], 0, s[6:7]
	v_cvt_pk_bf16_f32 v7, v28, v29
	global_store_dwordx4 v[10:11], v[2:5], off
	global_store_dwordx4 v[10:11], v[6:9], off offset:1024
	v_lshlrev_b32_e32 v10, 16, v216
	v_and_b32_e32 v11, 0xffff0000, v216
	s_add_i32 s3, s2, 32
	s_cmpk_lt_u32 s4, 0xfc
	v_mfma_f32_16x16x32_bf16 v[10:13], v[106:109], v[2:5], v[10:13]
	s_cselect_b32 s2, s3, s2
	s_ashr_i32 s3, s2, 31
	s_lshl_b64 s[2:3], s[2:3], 15
	v_mfma_f32_16x16x32_bf16 v[42:45], v[110:113], v[6:9], v[10:13]
	s_add_u32 s2, s40, s2
	s_addc_u32 s3, s41, s3
	s_add_u32 s4, s2, 0x2000
	s_nop 0
	s_waitcnt vmcnt(36)
	v_lshlrev_b32_e32 v10, 16, v214
	v_and_b32_e32 v11, 0xffff0000, v214
	v_lshlrev_b32_e32 v12, 16, v215
	v_and_b32_e32 v13, 0xffff0000, v215
	s_addc_u32 s5, s3, 0
	s_or_b32 s6, s1, 29
	v_mfma_f32_16x16x32_bf16 v[10:13], v[98:101], v[2:5], v[10:13]
	v_mfma_f32_16x16x32_bf16 v[46:49], v[102:105], v[6:9], v[10:13]
	s_nop 6
	v_lshlrev_b32_e32 v10, 16, v210
	v_and_b32_e32 v11, 0xffff0000, v210
	v_lshlrev_b32_e32 v12, 16, v211
	v_and_b32_e32 v13, 0xffff0000, v211
	s_nop 1
	v_mfma_f32_16x16x32_bf16 v[10:13], v[58:61], v[2:5], v[10:13]
	v_mfma_f32_16x16x32_bf16 v[50:53], v[62:65], v[6:9], v[10:13]
	s_nop 6
	v_lshlrev_b32_e32 v10, 16, v206
	v_and_b32_e32 v11, 0xffff0000, v206
	v_lshlrev_b32_e32 v12, 16, v207
	v_and_b32_e32 v13, 0xffff0000, v207
	s_nop 1
	v_mfma_f32_16x16x32_bf16 v[2:5], v[34:37], v[2:5], v[10:13]
	v_mfma_f32_16x16x32_bf16 v[34:37], v[38:41], v[6:9], v[2:5]
	s_nop 6
	global_load_dwordx4 v[2:5], v248, s[2:3]
	global_load_dwordx4 v[6:9], v248, s[2:3] offset:1024
	global_load_dwordx2 v[202:203], v0, s[4:5]
	global_load_dwordx4 v[10:13], v248, s[2:3] offset:2048
	global_load_dwordx4 v[18:21], v248, s[2:3] offset:3072
	global_load_dwordx2 v[204:205], v179, s[4:5]
	global_load_dwordx4 v[14:17], v249, s[2:3]
	global_load_dwordx4 v[22:25], v250, s[2:3]
	global_load_dwordx2 v[206:207], v191, s[4:5]
	global_load_dwordx4 v[26:29], v189, s[2:3]
	global_load_dwordx4 v[30:33], v187, s[2:3]
	global_load_dwordx2 v[208:209], v195, s[4:5]
	s_lshl_b32 s2, s6, 3
	s_add_i32 s2, s2, s0
	s_ashr_i32 s3, s2, 31
	s_lshl_b64 s[4:5], s[2:3], 13
	v_cvt_pk_bf16_f32 v38, v42, v43
	v_cvt_pk_bf16_f32 v39, v44, v45
	v_cvt_pk_bf16_f32 v40, v46, v47
	v_cvt_pk_bf16_f32 v41, v48, v49
	v_cvt_pk_bf16_f32 v44, v34, v35
	v_lshl_add_u64 v[34:35], v[180:181], 0, s[4:5]
	v_cvt_pk_bf16_f32 v42, v50, v51
	v_cvt_pk_bf16_f32 v43, v52, v53
	v_cvt_pk_bf16_f32 v45, v36, v37
	global_store_dwordx4 v[34:35], v[38:41], off
	global_store_dwordx4 v[34:35], v[42:45], off offset:1024
	s_waitcnt vmcnt(36)
; __device__ __forceinline__ unsigned pk2(float lo, float hi) { const f32x2 f = {lo, hi}; const bf16n2 v = __builtin_convertvector(f, bf16n2); return __builtin_bit_cast(unsigned, v); }
; #define RW_LOAD_SET(SET, UNIT) do { const bf16_t* ug_ = rwu + (size_t)(UNIT) * 16384; \
;     _Pragma("unroll") for (int ta = 0; ta < 4; ++ta) { An[SET][ta][0] = *(const bf16x8*)(ug_ + ((ta * 2) * 64 + lane) * 8); An[SET][ta][1] = *(const bf16x8*)(ug_ + ((ta * 2 + 1) * 64 + lane) * 8); \
;         Zn[SET][ta] = *(const u32x2*)(ug_ + 4096 + ((cq * 4 + ta) * 64 + lane) * 4); } } while (0)
; template <int SM>
; __device__ __forceinline__ void phase_rwkv_scan(const Ctx& c, const bf16_t* rwu, bf16_t* rws) {
;     ...
;     for (int ch = 0; ch < T / 64; ch += 32) {
; #pragma unroll
;         for (int uu = 0; uu < 32; ++uu) {
;             const int u = uu % RW_SETS;
;             const int unit = (ch + uu) * 8 + h;
;             bf16_t* sg = rws + (size_t)unit * 4096 + cq * 1024 + lane * 8;
;             *(bf16x8*)(sg) = Bhi[0]; *(bf16x8*)(sg + 512) = Bhi[1];
;             f32x4 acc[4];
; #pragma unroll
;             for (int ta = 0; ta < 4; ++ta) { const u32x2 z = Zn[u][ta];
;                 acc[ta] = (f32x4){__uint_as_float(z.x << 16), __uint_as_float(z.x & 0xffff0000u), __uint_as_float(z.y << 16), __uint_as_float(z.y & 0xffff0000u)};
; #pragma unroll
;                 for (int s = 0; s < 2; ++s) acc[ta] = __builtin_amdgcn_mfma_f32_16x16x32_bf16(An[u][ta][s], Bhi[s], acc[ta], 0, 0, 0); }
;             if (SM == 0) RW_LOAD_SET(u, (ch + uu + RW_SETS < T / 64) ? unit + 8 * RW_SETS : unit);
; #pragma unroll
;             for (int s = 0; s < 2; ++s) { u32x4 hi;
;                 hi.x = pk2(acc[2 * s][0], acc[2 * s][1]); hi.y = pk2(acc[2 * s][2], acc[2 * s][3]); hi.z = pk2(acc[2 * s + 1][0], acc[2 * s + 1][1]); hi.w = pk2(acc[2 * s + 1][2], acc[2 * s + 1][3]);
;                 Bhi[s] = __builtin_bit_cast(bf16x8, hi); }
;         }
	v_lshlrev_b32_e32 v34, 16, v232
	v_and_b32_e32 v35, 0xffff0000, v232
	v_lshlrev_b32_e32 v36, 16, v233
	v_and_b32_e32 v37, 0xffff0000, v233
	s_add_i32 s3, s2, 32
	s_cmpk_lt_u32 s6, 0xfc
	v_mfma_f32_16x16x32_bf16 v[34:37], v[138:141], v[38:41], v[34:37]
	s_cselect_b32 s2, s3, s2
	s_ashr_i32 s3, s2, 31
	s_lshl_b64 s[2:3], s[2:3], 15
	v_mfma_f32_16x16x32_bf16 v[98:101], v[142:145], v[42:45], v[34:37]
	s_add_u32 s2, s40, s2
	s_addc_u32 s3, s41, s3
	s_add_u32 s4, s2, 0x2000
	s_nop 0
	v_lshlrev_b32_e32 v34, 16, v230
	v_and_b32_e32 v35, 0xffff0000, v230
	v_lshlrev_b32_e32 v36, 16, v231
	v_and_b32_e32 v37, 0xffff0000, v231
	s_addc_u32 s5, s3, 0
	s_or_b32 s6, s1, 30
	v_mfma_f32_16x16x32_bf16 v[34:37], v[130:133], v[38:41], v[34:37]
	v_mfma_f32_16x16x32_bf16 v[102:105], v[134:137], v[42:45], v[34:37]
	s_nop 6
	v_lshlrev_b32_e32 v34, 16, v228
	v_and_b32_e32 v35, 0xffff0000, v228
	v_lshlrev_b32_e32 v36, 16, v229
	v_and_b32_e32 v37, 0xffff0000, v229
	s_nop 1
	v_mfma_f32_16x16x32_bf16 v[34:37], v[122:125], v[38:41], v[34:37]
	v_mfma_f32_16x16x32_bf16 v[106:109], v[126:129], v[42:45], v[34:37]
	s_nop 6
	v_lshlrev_b32_e32 v34, 16, v226
	v_and_b32_e32 v35, 0xffff0000, v226
	v_lshlrev_b32_e32 v36, 16, v227
	v_and_b32_e32 v37, 0xffff0000, v227
	s_nop 1
	v_mfma_f32_16x16x32_bf16 v[34:37], v[114:117], v[38:41], v[34:37]
	v_cvt_pk_bf16_f32 v114, v98, v99
	v_cvt_pk_bf16_f32 v115, v100, v101
	v_cvt_pk_bf16_f32 v116, v102, v103
	v_mfma_f32_16x16x32_bf16 v[110:113], v[118:121], v[42:45], v[34:37]
	global_load_dwordx4 v[58:61], v248, s[2:3]
	global_load_dwordx4 v[62:65], v248, s[2:3] offset:1024
	global_load_dwordx2 v[216:217], v0, s[4:5]
	global_load_dwordx4 v[50:53], v248, s[2:3] offset:2048
	global_load_dwordx4 v[54:57], v248, s[2:3] offset:3072
	global_load_dwordx2 v[214:215], v179, s[4:5]
	global_load_dwordx4 v[38:41], v249, s[2:3]
	global_load_dwordx4 v[46:49], v250, s[2:3]
	global_load_dwordx2 v[212:213], v191, s[4:5]
	global_load_dwordx4 v[34:37], v189, s[2:3]
	global_load_dwordx4 v[42:45], v187, s[2:3]
	global_load_dwordx2 v[210:211], v195, s[4:5]
	s_lshl_b32 s2, s6, 3
	s_add_i32 s2, s2, s0
	s_ashr_i32 s3, s2, 31
	s_lshl_b64 s[4:5], s[2:3], 13
	s_add_i32 s3, s2, 32
	s_cmpk_lt_u32 s6, 0xfc
	v_cvt_pk_bf16_f32 v117, v104, v105
	v_lshl_add_u64 v[98:99], v[180:181], 0, s[4:5]
	s_cselect_b32 s2, s3, s2
	v_cvt_pk_bf16_f32 v118, v106, v107
	v_cvt_pk_bf16_f32 v119, v108, v109
	v_cvt_pk_bf16_f32 v120, v110, v111
	v_cvt_pk_bf16_f32 v121, v112, v113
	global_store_dwordx4 v[98:99], v[114:117], off
	global_store_dwordx4 v[98:99], v[118:121], off offset:1024
	s_waitcnt vmcnt(36)
	v_lshlrev_b32_e32 v98, 16, v240
	v_and_b32_e32 v99, 0xffff0000, v240
	v_lshlrev_b32_e32 v100, 16, v241
	v_and_b32_e32 v101, 0xffff0000, v241
	v_lshlrev_b32_e32 v102, 16, v238
	v_and_b32_e32 v103, 0xffff0000, v238
	v_lshlrev_b32_e32 v104, 16, v239
	v_and_b32_e32 v105, 0xffff0000, v239
	v_lshlrev_b32_e32 v106, 16, v236
	v_and_b32_e32 v107, 0xffff0000, v236
	v_lshlrev_b32_e32 v108, 16, v237
	v_and_b32_e32 v109, 0xffff0000, v237
	v_lshlrev_b32_e32 v110, 16, v234
	v_and_b32_e32 v111, 0xffff0000, v234
	v_lshlrev_b32_e32 v112, 16, v235
	v_and_b32_e32 v113, 0xffff0000, v235
	s_ashr_i32 s3, s2, 31
	v_mfma_f32_16x16x32_bf16 v[98:101], v[170:173], v[114:117], v[98:101]
	s_lshl_b64 s[2:3], s[2:3], 15
	s_add_u32 s2, s40, s2
	s_addc_u32 s3, s41, s3
	v_mfma_f32_16x16x32_bf16 v[102:105], v[162:165], v[114:117], v[102:105]
	s_add_u32 s4, s2, 0x2000
	s_addc_u32 s5, s3, 0
	v_mfma_f32_16x16x32_bf16 v[106:109], v[154:157], v[114:117], v[106:109]
	v_mfma_f32_16x16x32_bf16 v[110:113], v[146:149], v[114:117], v[110:113]
	v_mfma_f32_16x16x32_bf16 v[98:101], v[174:177], v[118:121], v[98:101]
	v_mfma_f32_16x16x32_bf16 v[102:105], v[166:169], v[118:121], v[102:105]
	v_mfma_f32_16x16x32_bf16 v[106:109], v[158:161], v[118:121], v[106:109]
	s_nop 5
	v_cvt_pk_bf16_f32 v98, v98, v99
	v_cvt_pk_bf16_f32 v99, v100, v101
	v_cvt_pk_bf16_f32 v100, v102, v103
	v_mfma_f32_16x16x32_bf16 v[110:113], v[150:153], v[118:121], v[110:113]
	global_load_dwordx4 v[134:137], v248, s[2:3]
	global_load_dwordx4 v[142:145], v248, s[2:3] offset:1024
	global_load_dwordx2 v[230:231], v0, s[4:5]
	global_load_dwordx4 v[130:133], v248, s[2:3] offset:2048
	global_load_dwordx4 v[138:141], v248, s[2:3] offset:3072
	global_load_dwordx2 v[232:233], v179, s[4:5]
	global_load_dwordx4 v[122:125], v249, s[2:3]
	global_load_dwordx4 v[126:129], v250, s[2:3]
	global_load_dwordx2 v[226:227], v191, s[4:5]
	global_load_dwordx4 v[118:121], v189, s[2:3]
	global_load_dwordx4 v[114:117], v187, s[2:3]
	global_load_dwordx2 v[228:229], v195, s[4:5]
	s_or_b32 s4, s1, 31
	s_lshl_b32 s2, s4, 3
	s_add_i32 s2, s2, s0
	s_ashr_i32 s3, s2, 31
	s_lshl_b64 s[6:7], s[2:3], 13
	v_cvt_pk_bf16_f32 v101, v104, v105
	v_cvt_pk_bf16_f32 v102, v106, v107
	v_lshl_add_u64 v[106:107], v[180:181], 0, s[6:7]
	v_cvt_pk_bf16_f32 v103, v108, v109
	v_cvt_pk_bf16_f32 v104, v110, v111
	v_cvt_pk_bf16_f32 v105, v112, v113
	global_store_dwordx4 v[106:107], v[98:101], off
	global_store_dwordx4 v[106:107], v[102:105], off offset:1024
	s_waitcnt vmcnt(36)
	v_lshlrev_b32_e32 v106, 16, v224
	v_and_b32_e32 v107, 0xffff0000, v224
	v_lshlrev_b32_e32 v108, 16, v225
	v_and_b32_e32 v109, 0xffff0000, v225
	s_add_i32 s3, s2, 32
	s_cmpk_lt_u32 s4, 0xfc
	v_mfma_f32_16x16x32_bf16 v[90:93], v[90:93], v[98:101], v[106:109]
	s_cselect_b32 s2, s3, s2
	s_add_i32 s3, s1, 32
	s_cmpk_lt_u32 s1, 0xe0
	v_mfma_f32_16x16x32_bf16 v[90:93], v[94:97], v[102:105], v[90:93]
	v_lshlrev_b32_e32 v94, 16, v222
	v_and_b32_e32 v95, 0xffff0000, v222
	v_lshlrev_b32_e32 v96, 16, v223
	v_and_b32_e32 v97, 0xffff0000, v223
	s_mov_b32 s1, s3
	s_nop 0
	v_mfma_f32_16x16x32_bf16 v[82:85], v[82:85], v[98:101], v[94:97]
	v_mfma_f32_16x16x32_bf16 v[82:85], v[86:89], v[102:105], v[82:85]
	v_lshlrev_b32_e32 v86, 16, v220
	v_and_b32_e32 v87, 0xffff0000, v220
	v_lshlrev_b32_e32 v88, 16, v221
	v_and_b32_e32 v89, 0xffff0000, v221
	s_nop 1
	v_mfma_f32_16x16x32_bf16 v[74:77], v[74:77], v[98:101], v[86:89]
	v_mfma_f32_16x16x32_bf16 v[74:77], v[78:81], v[102:105], v[74:77]
	v_lshlrev_b32_e32 v78, 16, v218
	v_and_b32_e32 v79, 0xffff0000, v218
	v_lshlrev_b32_e32 v80, 16, v219
	v_and_b32_e32 v81, 0xffff0000, v219
	s_nop 1
	v_mfma_f32_16x16x32_bf16 v[66:69], v[66:69], v[98:101], v[78:81]
	v_mfma_f32_16x16x32_bf16 v[78:81], v[70:73], v[102:105], v[66:69]
	v_cvt_pk_bf16_f32 v70, v90, v91
	v_cvt_pk_bf16_f32 v71, v92, v93
	v_cvt_pk_bf16_f32 v72, v82, v83
	v_cvt_pk_bf16_f32 v73, v84, v85
	s_nop 2
	v_cvt_pk_bf16_f32 v66, v74, v75
	v_cvt_pk_bf16_f32 v67, v76, v77
	v_cvt_pk_bf16_f32 v68, v78, v79
	v_cvt_pk_bf16_f32 v69, v80, v81
	s_cbranch_scc1 .LBB0_981
	s_waitcnt vmcnt(0)

;     ...
;         const int g = unit / NU, t0 = ((g == 0) ? (unit % NU) : (NU - 1 - unit % NU)) * TB, tw0 = t0 + wave * TW;
;         const bf16_t* Ksrc; size_t kstride; const bf16_t* Vsrc; size_t vstride; int qcol;
;         if (MODE == 0) { Ksrc = proj + PC_SK + g * 64; kstride = PLD; Vsrc = vtb + (size_t)(4 + g) * 64 * T; vstride = T; qcol = PC_SQ + g * 256; }
;         else if (MODE == 1) { Ksrc = proj + PC_KW + g * 64; kstride = PLD; Vsrc = vtb + (size_t)(2 + g) * 64 * T; vstride = T; qcol = PC_NQ + g * 256; }
;         else if (MODE == 2) { Ksrc = kcb + (size_t)g * 1024 * 64; kstride = 64; Vsrc = vctb + (size_t)g * 64 * 1024; vstride = 1024; qcol = PC_NQ + g * 256; }
;         else { Ksrc = proj + PC_KS + g * 64; kstride = PLD; Vsrc = vtb + (size_t)(0 + g) * 64 * T; vstride = T; qcol = PC_NQ + g * 256; }
;         bf16x8 Bq[NQ][2]; bf16_t graw[NQ]; float sinkv = 0.f;
; #pragma unroll
;         for (int qd = 0; qd < NQ; ++qd) { const bf16_t* qp = proj + (size_t)(tw0 + 4 * qd + (n >> 2)) * PLD + qcol + hr * 64 + 8 * q;
;             Bq[qd][0] = *(const bf16x8*)qp; Bq[qd][1] = *(const bf16x8*)(qp + 32);
;             graw[qd] = (MODE != 0) ? proj[(size_t)(tw0 + 4 * qd + (n >> 2)) * PLD + PC_GL + (MODE == 2 ? 0 : (MODE == 3 ? 8 : 16)) + g * 4 + hr] : (bf16_t)0; }
;         if (MODE == 0) sinkv = inptr(c, I_SINK)[layer * 8 + g * 4 + hr];
;     ...
;             const unsigned kthr = (unsigned)(c.tid >> 3) * (unsigned)kstride + (unsigned)(c.tid & 7) * 8u, vthr = (unsigned)(c.tid >> 3) * (unsigned)vstride + (unsigned)(c.tid & 7) * 8u;
;             int st_k, st_va;
;             { const int row = c.tid >> 3, cj = c.tid & 7, ga = 2 * cj;
;               st_k = row * 128 + (((cj ^ row) & 7) << 4);
;               st_va = row * 128 + (((((ga >> 3) * 4 + (ga & 3)) ^ row) & 7) << 4) + ((ga >> 2) & 1) * 8; }
;             u32x4 kreg[TS], vreg[TS]; int p0n[TS];
;             const int nrounds = (ntiles + TS - 1) / TS;
;             if (nrounds > 0) AT_ISSUE(0);
.LBB0_1003:
	s_lshl_b32 s36, s37, 6
	s_lshl_b32 s12, s8, 8
	s_add_i32 s38, s36, s28
	s_lshl_b32 s6, s8, 6
	s_ashr_i32 s9, s8, 31
	s_ashr_i32 s13, s12, 31
	s_ashr_i32 s7, s6, 31
	s_lshl_b64 s[10:11], s[8:9], 21
	v_or_b32_e32 v130, s38, v134
	s_lshl_b64 s[12:13], s[12:13], 1
	s_add_u32 s12, s80, s12
	v_ashrrev_i32_e32 v131, 31, v130
	s_addc_u32 s13, s81, s13
	v_lshlrev_b64 v[2:3], 13, v[130:131]
	v_lshl_add_u64 v[2:3], s[12:13], 0, v[2:3]
	v_lshl_add_u64 v[2:3], v[2:3], 0, v[0:1]
	v_mov_b32_e32 v127, v1
	v_lshl_add_u64 v[2:3], v[2:3], 0, v[126:127]
	s_mov_b64 s[14:15], 0x1a00
	v_lshl_add_u64 v[4:5], v[2:3], 0, s[14:15]
	v_add_co_u32_e32 v2, vcc, s97, v2
	v_or_b32_e32 v128, 4, v130
	s_nop 0
	v_addc_co_u32_e32 v3, vcc, 0, v3, vcc
	v_ashrrev_i32_e32 v129, 31, v128
	global_load_dwordx4 v[42:45], v[2:3], off offset:2560
	global_load_dwordx4 v[46:49], v[4:5], off offset:64
	v_lshlrev_b64 v[2:3], 13, v[128:129]
	v_lshl_add_u64 v[2:3], s[12:13], 0, v[2:3]
	v_lshl_add_u64 v[2:3], v[2:3], 0, v[0:1]
	v_lshl_add_u64 v[2:3], v[2:3], 0, v[126:127]
	v_lshl_add_u64 v[6:7], v[2:3], 0, s[14:15]
	v_add_co_u32_e32 v2, vcc, s97, v2
	v_mov_b32_e32 v10, s64
	s_nop 0
	v_addc_co_u32_e32 v3, vcc, 0, v3, vcc
	global_load_dwordx4 v[2:5], v[2:3], off offset:2560
	s_nop 0
	global_load_dwordx4 v[6:9], v[6:7], off offset:64
	ds_read_b32 v10, v10
	s_lshl_b64 s[6:7], s[6:7], 1
	s_add_u32 s6, s92, s6
	s_addc_u32 s7, s93, s7
	s_lshl_b32 s22, s8, 2
	v_mov_b32_e32 v11, s65
	s_waitcnt lgkmcnt(0)
	v_readfirstlane_b32 s9, v10
	s_add_u32 s8, s82, s10
	ds_read_b32 v11, v11
	v_mov_b32_e32 v10, s9
	s_addc_u32 s9, s83, s11
	s_add_u32 s8, s8, 0x800000
	s_addc_u32 s9, s9, 0
	s_add_i32 s39, s36, 0xffffff80
	s_max_i32 s42, s39, 0
	s_lshl_b64 s[10:11], s[42:43], 13
	s_waitcnt lgkmcnt(0)
	v_readfirstlane_b32 s12, v11
	s_add_u32 s10, s6, s10
	v_add_u32_e32 v12, s22, v135
	v_mov_b32_e32 v11, s12
	s_addc_u32 s11, s7, s11
	s_lshl_b32 s12, s42, 1
	v_ashrrev_i32_e32 v13, 31, v12
	s_add_u32 s12, s8, s12
	v_lshl_add_u64 v[10:11], v[12:13], 2, v[10:11]
	s_addc_u32 s13, s9, 0
	flat_load_dword v127, v[10:11]
	v_lshl_add_u64 v[10:11], v[122:123], 1, s[10:11]
	v_lshl_add_u64 v[12:13], v[124:125], 1, s[12:13]
	s_waitcnt lgkmcnt(0)
	s_barrier
	global_load_dwordx4 v[14:17], v[10:11], off
	s_nop 0
	global_load_dwordx4 v[10:13], v[12:13], off
	s_sub_i32 s10, s36, 64
	s_max_i32 s42, s10, 0
	s_lshl_b64 s[10:11], s[42:43], 13
	s_lshl_b32 s42, s42, 1
	v_lshl_add_u64 v[18:19], v[122:123], 1, s[6:7]
	v_lshl_add_u64 v[20:21], v[124:125], 1, s[8:9]
	v_lshl_add_u64 v[22:23], v[18:19], 0, s[10:11]
	v_lshl_add_u64 v[24:25], v[20:21], 0, s[42:43]
	global_load_dwordx4 v[200:203], v[22:23], off
	global_load_dwordx4 v[204:207], v[24:25], off
	s_max_i32 s42, s36, 0
	s_lshl_b64 s[10:11], s[42:43], 13
	s_lshl_b32 s42, s42, 1
	v_lshl_add_u64 v[22:23], v[18:19], 0, s[10:11]
	v_lshl_add_u64 v[24:25], v[20:21], 0, s[42:43]
	global_load_dwordx4 v[208:211], v[22:23], off
	global_load_dwordx4 v[212:215], v[24:25], off
	s_and_saveexec_b64 s[10:11], s[0:1]
	s_cbranch_execz .LBB0_1010
	s_lshl_b32 s12, s22, 2
	s_add_i32 s42, s12, 0
	s_add_i32 s42, s42, 0x25520
	s_mov_b64 s[12:13], 0
	v_mov_b32_e32 v18, v145
	v_mov_b32_e32 v19, v144
	v_mov_b32_e32 v20, v178
	s_branch .LBB0_1007

;     ...
;                 __syncthreads();
; #pragma unroll
;                 for (int i = 0; i < TS; ++i) {
;                     *(LAS u32x4*)(L + AT_K + i * AT_TS + st_k) = kreg[i];
;                     if (do_pv) { const u32x2 lo = {vreg[i].x, vreg[i].y}, hi = {vreg[i].z, vreg[i].w};
;                         *(LAS u32x2*)(L + AT_V + i * AT_TS + st_va) = lo; *(LAS u32x2*)(L + AT_V + i * AT_TS + (st_va ^ 16)) = hi; } }
;                 if (rd + 1 < nrounds) AT_ISSUE(rd + 1);
;                 __syncthreads();
;     ...
;                 if (MODE != 3) {
; #pragma unroll
;                     for (int kt = 0; kt < 4; ++kt)
; #pragma unroll
;                         for (int ks = 0; ks < 2; ++ks) akf[kt][ks] = *(const LAS bf16x8*)(L + LK + (16 * kt + n) * 128 + ((((4 * ks + q) ^ n) & 7) << 4));
;                     if (do_pv) {
; #pragma unroll
;                         for (int st = 0; st < 2; ++st)
; #pragma unroll
;                             for (int dt = 0; dt < 4; ++dt) avf[st][dt] = *(const LAS bf16x8*)(L + LV + (16 * dt + n) * 128 + ((((4 * st + q) ^ n) & 7) << 4)); }
;                 }
;                 unsigned tokmask = 0u;
;                 if (MODE == 3) { tokmask = (unsigned)__ballot(lane < TW && ((selm[(wave * TW + (lane & (TW - 1))) * 8 + (jblk >> 5)] >> (jblk & 31)) & 1u)); if (tokmask == 0u) continue; }
; #pragma unroll
;                 for (int qd = 0; qd < NQ; ++qd) {
;                     const int tq = tw0 + 4 * qd + (n >> 2);
;                     if (DBG == 3) continue;
;                     bool colsel = true;
;                     if (MODE == 3) { colsel = (tokmask >> (4 * qd + (n >> 2))) & 1u; if (((tokmask >> (4 * qd)) & 0xfu) == 0u) continue; }
;                     {
;                         f32x4 sc[4];
;                         float bia[4][4];
;                         bf16x8 akq[4][2], avq[2][4];
;                         if (MODE == 3) {
; #pragma unroll
;                             for (int kt = 0; kt < 4; ++kt)
; #pragma unroll
;                                 for (int ks = 0; ks < 2; ++ks) akq[kt][ks] = *(const LAS bf16x8*)(L + LK + (16 * kt + n) * 128 + ((((4 * ks + q) ^ n) & 7) << 4));
;                             if (!far) { const LAS float* tp = biasd + hr * NT + (DOFF - tq + p0) + 4 * q;
; #pragma unroll
;                                 for (int kt = 0; kt < 4; ++kt)
; #pragma unroll
.LBB0_1010:
	s_or_b64 exec, exec, s[10:11]
	v_lshl_add_u64 v[112:113], v[122:123], 1, s[6:7]
	s_sub_i32 s6, s36, 64
	s_max_i32 s42, s6, 0
	v_lshl_add_u64 v[110:111], v[124:125], 1, s[8:9]
	s_lshl_b64 s[8:9], s[42:43], 13
	s_waitcnt lgkmcnt(0)
	s_barrier
	s_waitcnt vmcnt(4)
	ds_write_b128 v146, v[14:17]
	ds_write_b64 v147, v[10:11] offset:8192
	ds_write_b64 v148, v[12:13] offset:8192
	s_or_b32 s10, s38, 7
	s_cmp_lt_i32 s37, 2
	s_cselect_b64 s[8:9], -1, 0
	s_cmp_gt_i32 s39, s10
	s_cselect_b64 s[12:13], -1, 0
	s_sub_i32 s7, s38, 62
	s_cmp_lt_i32 s36, s7
	s_cselect_b64 s[14:15], -1, 0
	s_or_b64 s[8:9], s[8:9], s[14:15]
	s_or_b64 s[8:9], s[8:9], s[12:13]
	s_andn2_b64 vcc, exec, s[8:9]
	s_waitcnt lgkmcnt(0)
	s_barrier
	s_cbranch_vccz .LBB0_1013
	v_add_u32_e32 v10, v136, v140
	ds_read_b128 v[74:77], v10
	v_add_u32_e32 v11, v136, v141
	ds_read_b128 v[78:81], v11
	ds_read_b128 v[86:89], v10 offset:2048
	ds_read_b128 v[90:93], v11 offset:2048
	ds_read_b128 v[94:97], v10 offset:4096
	ds_read_b128 v[98:101], v11 offset:4096
	ds_read_b128 v[102:105], v10 offset:6144
	ds_read_b128 v[82:85], v11 offset:6144
	ds_read_b128 v[70:73], v10 offset:8192
	ds_read_b128 v[66:69], v10 offset:10240
	ds_read_b128 v[62:65], v10 offset:12288
	ds_read_b128 v[58:61], v10 offset:14336
	ds_read_b128 v[38:41], v11 offset:8192
	ds_read_b128 v[34:37], v11 offset:10240
	ds_read_b128 v[26:29], v11 offset:12288
	ds_read_b128 v[22:25], v11 offset:14336
	s_waitcnt lgkmcnt(13)
	v_mfma_f32_16x16x32_bf16 v[16:19], v[86:89], v[42:45], 0
	v_mov_b32_e32 v149, 0xf149f2ca
	s_waitcnt lgkmcnt(12)
	v_mfma_f32_16x16x32_bf16 v[16:19], v[90:93], v[46:49], v[16:19]
	v_mfma_f32_16x16x32_bf16 v[10:13], v[74:77], v[42:45], 0
	v_mfma_f32_16x16x32_bf16 v[12:15], v[78:81], v[46:49], v[10:13]
	s_waitcnt lgkmcnt(11)
	v_mfma_f32_16x16x32_bf16 v[30:33], v[94:97], v[42:45], 0
	s_nop 4
	v_sub_u32_e32 v10, s39, v130
	v_lshl_add_u32 v114, v10, 2, v143
	v_add_u32_e32 v10, 0xffc, v114
	ds_read2_b32 v[20:21], v10 offset1:1
	s_waitcnt lgkmcnt(11)
	v_mfma_f32_16x16x32_bf16 v[30:33], v[98:101], v[46:49], v[30:33]
	s_waitcnt lgkmcnt(0)
	v_add_f32_e32 v11, v12, v20
	v_add_u32_e32 v12, 0x1004, v114
	v_add_f32_e32 v10, v13, v21
	ds_read2_b32 v[20:21], v12 offset1:1
	v_mfma_f32_16x16x32_bf16 v[106:109], v[102:105], v[42:45], 0
	s_waitcnt lgkmcnt(0)
	v_add_f32_e32 v13, v14, v20
	v_add_u32_e32 v14, 0x103c, v114
	v_add_f32_e32 v12, v15, v21
	ds_read2_b32 v[20:21], v14 offset1:1
	v_mfma_f32_16x16x32_bf16 v[106:109], v[82:85], v[46:49], v[106:109]
	s_waitcnt lgkmcnt(0)
	v_add_f32_e32 v15, v16, v20
	v_add_u32_e32 v16, 0x1044, v114
	v_add_f32_e32 v14, v17, v21
	ds_read2_b32 v[20:21], v16 offset1:1
	s_waitcnt lgkmcnt(0)
	v_add_f32_e32 v17, v18, v20
	v_add_u32_e32 v18, 0x107c, v114
	v_add_f32_e32 v16, v19, v21
	ds_read2_b32 v[20:21], v18 offset1:1
	s_waitcnt lgkmcnt(0)
	v_add_f32_e32 v19, v30, v20
	v_add_u32_e32 v20, 0x1084, v114
	v_add_f32_e32 v18, v31, v21
	ds_read2_b32 v[20:21], v20 offset1:1
	s_waitcnt lgkmcnt(0)
	v_add_f32_e32 v31, v32, v20
	v_add_u32_e32 v20, 0x10bc, v114
	v_add_f32_e32 v30, v33, v21
	ds_read2_b32 v[32:33], v20 offset1:1
	s_waitcnt lgkmcnt(0)
	v_add_f32_e32 v21, v106, v32
	v_add_u32_e32 v32, 0x10c4, v114
	v_add_f32_e32 v20, v107, v33
	ds_read2_b32 v[106:107], v32 offset1:1
	s_waitcnt lgkmcnt(0)
	v_add_f32_e32 v33, v108, v106
	v_max_f32_e32 v106, v11, v10
	v_max3_f32 v106, v106, v13, v12
	v_max3_f32 v106, v106, v15, v14
	v_max3_f32 v106, v106, v17, v16
	v_max3_f32 v106, v106, v19, v18
	v_max3_f32 v106, v106, v31, v30
	v_add_f32_e32 v32, v109, v107
	v_max3_f32 v106, v106, v21, v20
	v_max3_f32 v106, v106, v33, v32
	v_cmp_gt_f32_e32 vcc, v106, v149
	s_cbranch_vccz .LBB0_1014
	v_add_f32_e32 v106, 0, v106
	ds_bpermute_b32 v107, v137, v106
	s_waitcnt lgkmcnt(0)
	v_max_f32_e32 v107, v107, v107
	v_max_f32_e32 v106, v106, v107
	ds_bpermute_b32 v107, v138, v106
	s_waitcnt lgkmcnt(0)
	v_max3_f32 v150, v106, v107, s72
	v_sub_f32_e32 v106, 0xf149f2ca, v150
	v_mul_f32_e32 v106, 0x3fb8aa3b, v106
	v_exp_f32_e32 v106, v106
	s_nop 0
	v_mul_f32_e32 v106, 0, v106
	s_branch .LBB0_1015

;     ...
;                 __syncthreads();
; #pragma unroll
;                 for (int i = 0; i < TS; ++i) {
;                     *(LAS u32x4*)(L + AT_K + i * AT_TS + st_k) = kreg[i];
;                     if (do_pv) { const u32x2 lo = {vreg[i].x, vreg[i].y}, hi = {vreg[i].z, vreg[i].w};
;                         *(LAS u32x2*)(L + AT_V + i * AT_TS + st_va) = lo; *(LAS u32x2*)(L + AT_V + i * AT_TS + (st_va ^ 16)) = hi; } }
;                 if (rd + 1 < nrounds) AT_ISSUE(rd + 1);
;                 __syncthreads();
; #pragma unroll
;               for (int ts = 0; ts < TS; ++ts) {
;                 const int p0 = p0s[ts]; const int LK = AT_K + ts * AT_TS, LV = AT_V + ts * AT_TS;
;                 if (p0 < 0) continue;
;                 if (MODE == 0) { if (p0 > tw0 + TW - 1 || p0 + 63 < tw0 - 127) continue; }
;                 if (MODE == 1) { if (p0 > tw0 + TW - 1 || p0 + 63 < tw0 - 511) continue; }
;                 if (MODE == 2) { if (16 * p0 + 31 > tw0 + TW - 1) continue; }
;                 if (MODE == 3) { if (p0 > tw0 + TW - 1) continue; }
;                 const bool far = (MODE == 2) ? (tw0 - (16 * (p0 + 63) + 31) >= 790) : ((MODE == 3) ? (tw0 - (p0 + 63) >= 790) : false);
;                 const int jblk = p0 >> 6;
;                 bf16x8 akf[4][2]; bf16x8 avf[2][4];
;                 if (MODE != 3) {
; #pragma unroll
;                     for (int kt = 0; kt < 4; ++kt)
; #pragma unroll
;                         for (int ks = 0; ks < 2; ++ks) akf[kt][ks] = *(const LAS bf16x8*)(L + LK + (16 * kt + n) * 128 + ((((4 * ks + q) ^ n) & 7) << 4));
;     ...
;                         for (int kt = 0; kt < 4; ++kt) { sc[kt] = (f32x4){0.f, 0.f, 0.f, 0.f};
; #pragma unroll
;                             for (int ks = 0; ks < 2; ++ks) { const bf16x8 ak = (MODE != 3) ? akf[kt][ks] : akq[kt][ks];
;                                 sc[kt] = __builtin_amdgcn_mfma_f32_16x16x32_bf16(ak, Bq[qd][ks], sc[kt], 0, 0, 0); } }
;                         if (MODE == 3) {
; #pragma unroll
;                             for (int st = 0; st < 2; ++st)
; #pragma unroll
;                                 for (int dt = 0; dt < 4; ++dt) avq[st][dt] = *(const LAS bf16x8*)(L + LV + (16 * dt + n) * 128 + ((((4 * st + q) ^ n) & 7) << 4));
;                             __builtin_amdgcn_sched_barrier(0);
;                         }
;                         if (!far) {
.LBB0_1019:
	s_max_i32 s42, s36, 0
	s_lshl_b64 s[8:9], s[42:43], 13
	s_lshl_b32 s42, s42, 1
	s_barrier
	s_waitcnt vmcnt(3)
	ds_write_b128 v146, v[200:203]
	s_waitcnt vmcnt(2)
	ds_write_b64 v147, v[204:205] offset:8192
	ds_write_b64 v148, v[206:207] offset:8192
	s_add_i32 s7, s38, 0xffffff81
	s_cmp_lt_i32 s37, 1
	s_cselect_b64 s[8:9], -1, 0
	s_cmp_gt_i32 s6, s10
	s_cselect_b64 s[12:13], -1, 0
	s_or_b64 s[8:9], s[8:9], s[12:13]
	s_cmp_le_i32 s36, s7
	s_cselect_b64 s[12:13], -1, 0
	s_or_b64 s[8:9], s[8:9], s[12:13]
	s_and_b64 vcc, exec, s[8:9]
	s_waitcnt lgkmcnt(0)
	s_barrier
	s_cbranch_vccnz .LBB0_1025
	v_add_u32_e32 v58, v136, v140
	ds_read_b128 v[90:93], v58
	v_sub_u32_e32 v153, s6, v130
	v_lshl_add_u32 v172, v153, 2, v143
	v_add_u32_e32 v59, v136, v141
	v_add_u32_e32 v153, 0xffc, v172
	ds_read_b128 v[94:97], v59
	ds_read_b128 v[98:101], v58 offset:2048
	ds_read_b128 v[102:105], v59 offset:2048
	ds_read_b128 v[106:109], v58 offset:4096
	ds_read_b128 v[110:113], v59 offset:4096
	ds_read_b128 v[114:117], v58 offset:6144
	ds_read_b128 v[118:121], v59 offset:6144
	ds_read_b128 v[86:89], v58 offset:8192
	ds_read_b128 v[82:85], v58 offset:10240
	ds_read_b128 v[78:81], v58 offset:12288
	ds_read_b128 v[74:77], v58 offset:14336
	ds_read_b128 v[70:73], v59 offset:8192
	ds_read_b128 v[66:69], v59 offset:10240
	ds_read_b128 v[62:65], v59 offset:12288
	ds_read_b128 v[58:61], v59 offset:14336
	ds_read2_b32 v[170:171], v153 offset1:1
	s_waitcnt lgkmcnt(14)
	v_mfma_f32_16x16x32_bf16 v[158:161], v[98:101], v[42:45], 0
	v_mfma_f32_16x16x32_bf16 v[154:157], v[90:93], v[42:45], 0
	v_mfma_f32_16x16x32_bf16 v[154:157], v[94:97], v[46:49], v[154:157]
	s_waitcnt lgkmcnt(13)
	v_mfma_f32_16x16x32_bf16 v[158:161], v[102:105], v[46:49], v[158:161]
	s_waitcnt lgkmcnt(12)
	v_mfma_f32_16x16x32_bf16 v[162:165], v[106:109], v[42:45], 0
	s_waitcnt lgkmcnt(0)
	s_nop 2
	v_add_f32_e32 v153, v154, v170
	v_add_f32_e32 v154, v155, v171
	v_add_u32_e32 v155, 0x1004, v172
	ds_read2_b32 v[170:171], v155 offset1:1
	v_mfma_f32_16x16x32_bf16 v[162:165], v[110:113], v[46:49], v[162:165]
	s_waitcnt lgkmcnt(0)
	v_add_f32_e32 v155, v156, v170
	v_add_f32_e32 v156, v157, v171
	v_add_u32_e32 v157, 0x103c, v172
	ds_read2_b32 v[170:171], v157 offset1:1
	v_mfma_f32_16x16x32_bf16 v[166:169], v[114:117], v[42:45], 0
	s_waitcnt lgkmcnt(0)
	v_add_f32_e32 v157, v158, v170
	v_add_f32_e32 v158, v159, v171
	v_add_u32_e32 v159, 0x1044, v172
	ds_read2_b32 v[170:171], v159 offset1:1
	v_mfma_f32_16x16x32_bf16 v[166:169], v[118:121], v[46:49], v[166:169]
	s_waitcnt lgkmcnt(0)
	v_add_f32_e32 v159, v160, v170
	v_add_f32_e32 v160, v161, v171
	v_add_u32_e32 v161, 0x107c, v172
	ds_read2_b32 v[170:171], v161 offset1:1
	s_waitcnt lgkmcnt(0)
	v_add_f32_e32 v161, v162, v170
	v_add_f32_e32 v162, v163, v171
	v_add_u32_e32 v163, 0x1084, v172
	ds_read2_b32 v[170:171], v163 offset1:1
	s_waitcnt lgkmcnt(0)
	v_add_f32_e32 v163, v164, v170
	v_add_f32_e32 v164, v165, v171
	v_add_u32_e32 v165, 0x10bc, v172
	ds_read2_b32 v[170:171], v165 offset1:1
	s_waitcnt lgkmcnt(0)
	v_add_f32_e32 v165, v166, v170
	v_add_f32_e32 v166, v167, v171
	v_add_u32_e32 v167, 0x10c4, v172
	ds_read2_b32 v[170:171], v167 offset1:1
	s_waitcnt lgkmcnt(0)
	v_add_f32_e32 v167, v168, v170
	v_add_f32_e32 v168, v169, v171
	v_max_f32_e32 v169, v153, v154
	v_max3_f32 v169, v169, v155, v156
	v_max3_f32 v169, v169, v157, v158
	v_max3_f32 v169, v169, v159, v160
	v_max3_f32 v169, v169, v161, v162
	v_max3_f32 v169, v169, v163, v164
	v_max3_f32 v169, v169, v165, v166
	v_max3_f32 v169, v169, v167, v168
	v_add_f32_e32 v170, 0x40c00000, v150
	v_cmp_gt_f32_e32 vcc, v169, v170
	s_cbranch_vccz .LBB0_1022
	v_add_f32_e32 v169, 0, v169
	ds_bpermute_b32 v170, v137, v169
	s_waitcnt lgkmcnt(0)
	v_max_f32_e32 v170, v170, v170
	v_max_f32_e32 v169, v169, v170
	ds_bpermute_b32 v170, v138, v169
	s_waitcnt lgkmcnt(0)
	v_max3_f32 v169, v150, v169, v170
	v_sub_f32_e32 v150, v150, v169
	v_mul_f32_e32 v150, 0x3fb8aa3b, v150
	v_exp_f32_e32 v150, v150
	s_nop 0
	v_mul_f32_e32 v152, v152, v150
	v_pk_mul_f32 v[32:33], v[32:33], v[150:151] op_sel_hi:[1,0]
	v_pk_mul_f32 v[30:31], v[30:31], v[150:151] op_sel_hi:[1,0]
	v_pk_mul_f32 v[20:21], v[20:21], v[150:151] op_sel_hi:[1,0]
	v_pk_mul_f32 v[18:19], v[18:19], v[150:151] op_sel_hi:[1,0]
	v_pk_mul_f32 v[16:17], v[16:17], v[150:151] op_sel_hi:[1,0]
	v_pk_mul_f32 v[14:15], v[14:15], v[150:151] op_sel_hi:[1,0]
	v_pk_mul_f32 v[12:13], v[12:13], v[150:151] op_sel_hi:[1,0]
	v_pk_mul_f32 v[10:11], v[10:11], v[150:151] op_sel_hi:[1,0]
	v_mov_b32_e32 v150, v169

;     ...
;                 __syncthreads();
; #pragma unroll
;                 for (int i = 0; i < TS; ++i) {
;                     *(LAS u32x4*)(L + AT_K + i * AT_TS + st_k) = kreg[i];
;                     if (do_pv) { const u32x2 lo = {vreg[i].x, vreg[i].y}, hi = {vreg[i].z, vreg[i].w};
;                         *(LAS u32x2*)(L + AT_V + i * AT_TS + st_va) = lo; *(LAS u32x2*)(L + AT_V + i * AT_TS + (st_va ^ 16)) = hi; } }
;                 if (rd + 1 < nrounds) AT_ISSUE(rd + 1);
;                 __syncthreads();
; #pragma unroll
;               for (int ts = 0; ts < TS; ++ts) {
;                 const int p0 = p0s[ts]; const int LK = AT_K + ts * AT_TS, LV = AT_V + ts * AT_TS;
;                 if (p0 < 0) continue;
;                 if (MODE == 0) { if (p0 > tw0 + TW - 1 || p0 + 63 < tw0 - 127) continue; }
;                 if (MODE == 1) { if (p0 > tw0 + TW - 1 || p0 + 63 < tw0 - 511) continue; }
;                 if (MODE == 2) { if (16 * p0 + 31 > tw0 + TW - 1) continue; }
;                 if (MODE == 3) { if (p0 > tw0 + TW - 1) continue; }
;                 const bool far = (MODE == 2) ? (tw0 - (16 * (p0 + 63) + 31) >= 790) : ((MODE == 3) ? (tw0 - (p0 + 63) >= 790) : false);
;                 const int jblk = p0 >> 6;
;                 bf16x8 akf[4][2]; bf16x8 avf[2][4];
;                 if (MODE != 3) {
; #pragma unroll
;                     for (int kt = 0; kt < 4; ++kt)
; #pragma unroll
;                         for (int ks = 0; ks < 2; ++ks) akf[kt][ks] = *(const LAS bf16x8*)(L + LK + (16 * kt + n) * 128 + ((((4 * ks + q) ^ n) & 7) << 4));
;     ...
;                         for (int kt = 0; kt < 4; ++kt) { sc[kt] = (f32x4){0.f, 0.f, 0.f, 0.f};
; #pragma unroll
;                             for (int ks = 0; ks < 2; ++ks) { const bf16x8 ak = (MODE != 3) ? akf[kt][ks] : akq[kt][ks];
;                                 sc[kt] = __builtin_amdgcn_mfma_f32_16x16x32_bf16(ak, Bq[qd][ks], sc[kt], 0, 0, 0); } }
;                         if (MODE == 3) {
; #pragma unroll
;                             for (int st = 0; st < 2; ++st)
; #pragma unroll
;                                 for (int dt = 0; dt < 4; ++dt) avq[st][dt] = *(const LAS bf16x8*)(L + LV + (16 * dt + n) * 128 + ((((4 * st + q) ^ n) & 7) << 4));
;                             __builtin_amdgcn_sched_barrier(0);
;                         }
;                         if (!far) {
.LBB0_1025:
	s_cmp_lt_i32 s37, 0
	s_cselect_b64 s[8:9], -1, 0
	s_cmp_gt_i32 s36, s10
	s_cselect_b64 s[10:11], -1, 0
	s_or_b32 s6, s36, 63
	s_cmp_lt_i32 s6, s7
	s_cselect_b64 s[6:7], -1, 0
	s_or_b64 s[6:7], s[8:9], s[6:7]
	s_or_b64 s[6:7], s[6:7], s[10:11]
	s_and_b64 vcc, exec, s[6:7]
	s_barrier
	s_waitcnt vmcnt(1)
	ds_write_b128 v146, v[208:211]
	s_waitcnt vmcnt(0)
	ds_write_b64 v147, v[212:213] offset:8192
	ds_write_b64 v148, v[214:215] offset:8192
	s_waitcnt lgkmcnt(0)
	s_barrier
	s_cbranch_vccnz .LBB0_1000
	v_add_u32_e32 v50, v136, v140
	ds_read_b128 v[82:85], v50
	v_add_u32_e32 v51, v136, v141
	ds_read_b128 v[86:89], v51
	ds_read_b128 v[90:93], v50 offset:2048
	ds_read_b128 v[94:97], v51 offset:2048
	ds_read_b128 v[98:101], v50 offset:4096
	ds_read_b128 v[102:105], v51 offset:4096
	ds_read_b128 v[106:109], v50 offset:6144
	ds_read_b128 v[110:113], v51 offset:6144
	ds_read_b128 v[78:81], v50 offset:8192
	ds_read_b128 v[74:77], v50 offset:10240
	ds_read_b128 v[70:73], v50 offset:12288
	ds_read_b128 v[66:69], v50 offset:14336
	ds_read_b128 v[62:65], v51 offset:8192
	ds_read_b128 v[58:61], v51 offset:10240
	ds_read_b128 v[54:57], v51 offset:12288
	ds_read_b128 v[50:53], v51 offset:14336
	s_waitcnt lgkmcnt(13)
	v_mfma_f32_16x16x32_bf16 v[118:121], v[90:93], v[42:45], 0
	s_waitcnt lgkmcnt(11)
	v_mfma_f32_16x16x32_bf16 v[154:157], v[98:101], v[42:45], 0
	v_mfma_f32_16x16x32_bf16 v[114:117], v[82:85], v[42:45], 0
	s_waitcnt lgkmcnt(9)
	v_mfma_f32_16x16x32_bf16 v[42:45], v[106:109], v[42:45], 0
	s_waitcnt lgkmcnt(8)
	v_mfma_f32_16x16x32_bf16 v[158:161], v[110:113], v[46:49], v[42:45]
	v_mfma_f32_16x16x32_bf16 v[114:117], v[86:89], v[46:49], v[114:117]
	s_nop 4
	v_sub_u32_e32 v42, s36, v130
	v_lshl_add_u32 v153, v42, 2, v143
	v_add_u32_e32 v42, 0xffc, v153
	ds_read2_b32 v[42:43], v42 offset1:1
	v_add_u32_e32 v44, 0x1004, v153
	v_mfma_f32_16x16x32_bf16 v[118:121], v[94:97], v[46:49], v[118:121]
	ds_read2_b32 v[44:45], v44 offset1:1
	v_mfma_f32_16x16x32_bf16 v[154:157], v[102:105], v[46:49], v[154:157]
	v_add_u32_e32 v46, 0x103c, v153
	ds_read2_b32 v[46:47], v46 offset1:1
	v_add_u32_e32 v48, 0x1044, v153
	ds_read2_b32 v[48:49], v48 offset1:1
	s_waitcnt lgkmcnt(3)
	v_add_f32_e32 v42, v114, v42
	v_add_u32_e32 v114, 0x107c, v153
	v_add_f32_e32 v43, v115, v43
	s_waitcnt lgkmcnt(2)
	v_add_f32_e32 v44, v116, v44
	ds_read2_b32 v[114:115], v114 offset1:1
	v_add_u32_e32 v116, 0x1084, v153
	v_add_f32_e32 v45, v117, v45
	s_waitcnt lgkmcnt(2)
	v_add_f32_e32 v46, v118, v46
	ds_read2_b32 v[116:117], v116 offset1:1
	v_add_u32_e32 v118, 0x10bc, v153
	v_add_f32_e32 v47, v119, v47
	s_waitcnt lgkmcnt(2)
	v_add_f32_e32 v48, v120, v48
	ds_read2_b32 v[118:119], v118 offset1:1
	v_add_u32_e32 v120, 0x10c4, v153
	v_max_f32_e32 v153, v42, v43
	v_add_f32_e32 v49, v121, v49
	ds_read2_b32 v[120:121], v120 offset1:1
	v_max3_f32 v153, v153, v44, v45
	v_max3_f32 v153, v153, v46, v47
	s_waitcnt lgkmcnt(3)
	v_add_f32_e32 v114, v154, v114
	v_add_f32_e32 v115, v155, v115
	v_max3_f32 v153, v153, v48, v49
	s_waitcnt lgkmcnt(2)
	v_add_f32_e32 v116, v156, v116
	v_add_f32_e32 v117, v157, v117
	v_max3_f32 v153, v153, v114, v115
	s_waitcnt lgkmcnt(1)
	v_add_f32_e32 v118, v158, v118
	v_add_f32_e32 v119, v159, v119
	v_max3_f32 v153, v153, v116, v117
	s_waitcnt lgkmcnt(0)
	v_add_f32_e32 v120, v160, v120
	v_add_f32_e32 v121, v161, v121
	v_max3_f32 v153, v153, v118, v119
	v_max3_f32 v153, v153, v120, v121
	v_add_f32_e32 v154, 0x40c00000, v150
	v_cmp_gt_f32_e32 vcc, v153, v154
	s_cbranch_vccz .LBB0_1028
	v_add_f32_e32 v153, 0, v153
	ds_bpermute_b32 v154, v137, v153
	s_waitcnt lgkmcnt(0)
	v_max_f32_e32 v154, v154, v154
	v_max_f32_e32 v153, v153, v154
	ds_bpermute_b32 v154, v138, v153
	s_waitcnt lgkmcnt(0)
	v_max3_f32 v153, v150, v153, v154
	v_sub_f32_e32 v150, v150, v153
	v_mul_f32_e32 v150, 0x3fb8aa3b, v150
	v_exp_f32_e32 v150, v150
	s_nop 0
	v_mul_f32_e32 v152, v152, v150
	v_pk_mul_f32 v[32:33], v[32:33], v[150:151] op_sel_hi:[1,0]
	v_pk_mul_f32 v[30:31], v[30:31], v[150:151] op_sel_hi:[1,0]
	v_pk_mul_f32 v[20:21], v[20:21], v[150:151] op_sel_hi:[1,0]
	v_pk_mul_f32 v[18:19], v[18:19], v[150:151] op_sel_hi:[1,0]
	v_pk_mul_f32 v[16:17], v[16:17], v[150:151] op_sel_hi:[1,0]
	v_pk_mul_f32 v[14:15], v[14:15], v[150:151] op_sel_hi:[1,0]
	v_pk_mul_f32 v[12:13], v[12:13], v[150:151] op_sel_hi:[1,0]
	v_pk_mul_f32 v[10:11], v[10:11], v[150:151] op_sel_hi:[1,0]
	v_mov_b32_e32 v150, v153

;     ...
;         const int g = unit / NU, t0 = ((g == 0) ? (unit % NU) : (NU - 1 - unit % NU)) * TB, tw0 = t0 + wave * TW;
;         const bf16_t* Ksrc; size_t kstride; const bf16_t* Vsrc; size_t vstride; int qcol;
;         if (MODE == 0) { Ksrc = proj + PC_SK + g * 64; kstride = PLD; Vsrc = vtb + (size_t)(4 + g) * 64 * T; vstride = T; qcol = PC_SQ + g * 256; }
;         else if (MODE == 1) { Ksrc = proj + PC_KW + g * 64; kstride = PLD; Vsrc = vtb + (size_t)(2 + g) * 64 * T; vstride = T; qcol = PC_NQ + g * 256; }
;         else if (MODE == 2) { Ksrc = kcb + (size_t)g * 1024 * 64; kstride = 64; Vsrc = vctb + (size_t)g * 64 * 1024; vstride = 1024; qcol = PC_NQ + g * 256; }
;         else { Ksrc = proj + PC_KS + g * 64; kstride = PLD; Vsrc = vtb + (size_t)(0 + g) * 64 * T; vstride = T; qcol = PC_NQ + g * 256; }
;         bf16x8 Bq[NQ][2]; bf16_t graw[NQ]; float sinkv = 0.f;
; #pragma unroll
;         for (int qd = 0; qd < NQ; ++qd) { const bf16_t* qp = proj + (size_t)(tw0 + 4 * qd + (n >> 2)) * PLD + qcol + hr * 64 + 8 * q;
;             Bq[qd][0] = *(const bf16x8*)qp; Bq[qd][1] = *(const bf16x8*)(qp + 32);
;             graw[qd] = (MODE != 0) ? proj[(size_t)(tw0 + 4 * qd + (n >> 2)) * PLD + PC_GL + (MODE == 2 ? 0 : (MODE == 3 ? 8 : 16)) + g * 4 + hr] : (bf16_t)0; }
;         if (MODE == 0) sinkv = inptr(c, I_SINK)[layer * 8 + g * 4 + hr];
;     ...
;             const unsigned kthr = (unsigned)(c.tid >> 3) * (unsigned)kstride + (unsigned)(c.tid & 7) * 8u, vthr = (unsigned)(c.tid >> 3) * (unsigned)vstride + (unsigned)(c.tid & 7) * 8u;
;             int st_k, st_va;
;             { const int row = c.tid >> 3, cj = c.tid & 7, ga = 2 * cj;
;               st_k = row * 128 + (((cj ^ row) & 7) << 4);
;               st_va = row * 128 + (((((ga >> 3) * 4 + (ga & 3)) ^ row) & 7) << 4) + ((ga >> 2) & 1) * 8; }
;             u32x4 kreg[TS], vreg[TS]; int p0n[TS];
;             const int nrounds = (ntiles + TS - 1) / TS;
;             if (nrounds > 0) AT_ISSUE(0);
.LBB0_1037:
	s_lshl_b32 s16, s7, 6
	s_add_i32 s29, s16, s28
	v_or_b32_e32 v134, s29, v123
	s_ashr_i32 s7, s6, 31
	s_lshl_b32 s12, s6, 8
	v_ashrrev_i32_e32 v135, 31, v134
	s_lshl_b32 s8, s6, 6
	s_lshl_b64 s[10:11], s[6:7], 21
	s_ashr_i32 s13, s12, 31
	s_lshl_b32 s6, s6, 2
	v_lshlrev_b64 v[2:3], 13, v[134:135]
	s_ashr_i32 s9, s8, 31
	s_ashr_i32 s7, s6, 31
	v_lshl_add_u64 v[2:3], s[80:81], 0, v[2:3]
	s_lshl_b64 s[12:13], s[12:13], 1
	v_lshl_add_u64 v[4:5], v[2:3], 0, s[12:13]
	s_lshl_b64 s[14:15], s[6:7], 1
	s_lshl_b64 s[8:9], s[8:9], 1
	v_lshl_add_u64 v[4:5], v[4:5], 0, v[0:1]
	v_mov_b32_e32 v129, v1
	v_or_b32_e32 v132, 4, v134
	s_add_u32 s8, s94, s8
	v_lshl_add_u64 v[4:5], v[4:5], 0, v[128:129]
	v_ashrrev_i32_e32 v133, 31, v132
	s_addc_u32 s9, s95, s9
	s_add_i32 s7, s16, 0xfffffe00
	global_load_dwordx4 v[42:45], v[4:5], off offset:3584
	global_load_dwordx4 v[46:49], v[4:5], off offset:3648
	v_lshl_add_u64 v[2:3], v[2:3], 0, s[14:15]
	v_mov_b32_e32 v131, v1
	v_lshlrev_b64 v[4:5], 13, v[132:133]
	s_add_u32 s10, s82, s10
	v_lshl_add_u64 v[2:3], v[2:3], 0, v[130:131]
	v_lshl_add_u64 v[4:5], s[80:81], 0, v[4:5]
	s_addc_u32 s11, s83, s11
	v_add_co_u32_e32 v2, vcc, s97, v2
	v_lshl_add_u64 v[6:7], v[4:5], 0, s[12:13]
	s_add_u32 s10, s10, 0x400000
	v_addc_co_u32_e32 v3, vcc, 0, v3, vcc
	v_lshl_add_u64 v[6:7], v[6:7], 0, v[0:1]
	s_addc_u32 s11, s11, 0
	s_max_i32 s42, s7, 0
	v_lshl_add_u64 v[6:7], v[6:7], 0, v[128:129]
	global_load_ushort v156, v[2:3], off offset:2080
	global_load_dwordx4 v[34:37], v[6:7], off offset:3584
	v_lshl_add_u64 v[2:3], v[4:5], 0, s[14:15]
	s_lshl_b64 s[12:13], s[42:43], 13
	v_lshl_add_u64 v[2:3], v[2:3], 0, v[130:131]
	s_add_u32 s12, s8, s12
	v_add_co_u32_e32 v2, vcc, s97, v2
	s_addc_u32 s13, s9, s13
	s_lshl_b32 s14, s42, 1
	v_addc_co_u32_e32 v3, vcc, 0, v3, vcc
	s_add_u32 s14, s10, s14
	global_load_dwordx4 v[38:41], v[6:7], off offset:3648
	global_load_ushort v129, v[2:3], off offset:2080
	s_addc_u32 s15, s11, 0
	v_lshl_add_u64 v[2:3], v[124:125], 1, s[12:13]
	s_barrier
	v_lshl_add_u64 v[4:5], v[126:127], 1, s[14:15]
	global_load_dwordx4 v[54:57], v[2:3], off
	global_load_dwordx4 v[50:53], v[4:5], off
	s_add_i32 s42, s7, 64
	s_max_i32 s42, s42, 0
	s_lshl_b64 s[12:13], s[42:43], 13
	s_lshl_b32 s42, s42, 1
	v_lshl_add_u64 v[200:201], v[124:125], 1, s[8:9]
	v_lshl_add_u64 v[202:203], v[126:127], 1, s[10:11]
	v_lshl_add_u64 v[200:201], v[200:201], 0, s[12:13]
	v_lshl_add_u64 v[202:203], v[202:203], 0, s[42:43]
	global_load_dwordx4 v[204:207], v[200:201], off
	s_nop 0
	global_load_dwordx4 v[200:203], v[202:203], off
	s_and_saveexec_b64 s[12:13], s[0:1]
	s_cbranch_execz .LBB0_1044
	s_lshl_b32 s14, s6, 2
	s_add_i32 s36, s14, 0
	s_add_i32 s36, s36, 0x25500
	s_mov_b64 s[14:15], 0
	v_mov_b32_e32 v2, v151
	v_mov_b32_e32 v3, v150
	v_mov_b32_e32 v4, v178
	s_branch .LBB0_1041

;     ...
;                 __syncthreads();
; #pragma unroll
;                 for (int i = 0; i < TS; ++i) {
;                     *(LAS u32x4*)(L + AT_K + i * AT_TS + st_k) = kreg[i];
;                     if (do_pv) { const u32x2 lo = {vreg[i].x, vreg[i].y}, hi = {vreg[i].z, vreg[i].w};
;                         *(LAS u32x2*)(L + AT_V + i * AT_TS + st_va) = lo; *(LAS u32x2*)(L + AT_V + i * AT_TS + (st_va ^ 16)) = hi; } }
;                 if (rd + 1 < nrounds) AT_ISSUE(rd + 1);
;                 __syncthreads();
;     ...
;                         for (int kt = 0; kt < 4; ++kt) { sc[kt] = (f32x4){0.f, 0.f, 0.f, 0.f};
; #pragma unroll
;                             for (int ks = 0; ks < 2; ++ks) { const bf16x8 ak = (MODE != 3) ? akf[kt][ks] : akq[kt][ks];
;                                 sc[kt] = __builtin_amdgcn_mfma_f32_16x16x32_bf16(ak, Bq[qd][ks], sc[kt], 0, 0, 0); } }
;                         if (MODE == 3) {
; #pragma unroll
;                             for (int st = 0; st < 2; ++st)
; #pragma unroll
;                                 for (int dt = 0; dt < 4; ++dt) avq[st][dt] = *(const LAS bf16x8*)(L + LV + (16 * dt + n) * 128 + ((((4 * st + q) ^ n) & 7) << 4));
;                             __builtin_amdgcn_sched_barrier(0);
;                         }
;                         if (!far) {
;                             const LAS float* tp = (MODE == 2) ? biasd + hr * NT + (DOFF - tq + 31 + 16 * p0) + 64 * q : biasd + hr * NT + (DOFF - tq + p0) + 4 * q;
; #pragma unroll
;                             for (int kt = 0; kt < 4; ++kt)
; #pragma unroll
;                                 for (int r = 0; r < 4; ++r) sc[kt][r] += (MODE == 3) ? bia[kt][r] : ((MODE == 2) ? tp[256 * kt + 16 * r] : tp[16 * kt + r]);
;                         }
;                         const float bshift = far ? bfar : 0.f, boff = bshift * 1.4426950408889634f;
;                         float mx;
;                         { float m = fmaxf(fmaxf(sc[0][0], sc[0][1]), sc[0][2]);
;                           m = fmaxf(fmaxf(m, sc[0][3]), sc[1][0]); m = fmaxf(fmaxf(m, sc[1][1]), sc[1][2]); m = fmaxf(fmaxf(m, sc[1][3]), sc[2][0]);
;                           m = fmaxf(fmaxf(m, sc[2][1]), sc[2][2]); m = fmaxf(fmaxf(m, sc[2][3]), sc[3][0]); m = fmaxf(fmaxf(m, sc[3][1]), sc[3][2]); mx = fmaxf(m, sc[3][3]) + bshift; }
;                         if (MODE == 3 && !colsel) mx = -1e30f;
.LBB0_1046:
	s_addk_i32 s8, 0x100
	s_branch .Lw2_1047
.LBB0_1047:
	s_mov_b32 s9, s7
	s_add_i32 s7, s7, 64
	s_add_i32 s42, s7, 64
	s_max_i32 s42, s42, 0
	s_lshl_b64 s[10:11], s[42:43], 13
	s_lshl_b32 s42, s42, 1
	s_waitcnt lgkmcnt(0)
	s_barrier
	s_waitcnt vmcnt(3)
	ds_write_b128 v153, v[54:57]
	s_waitcnt vmcnt(2)
	ds_write_b64 v154, v[50:51] offset:8192
	ds_write_b64 v155, v[52:53] offset:8192
	v_lshl_add_u64 v[50:51], v[138:139], 0, s[10:11]
	v_lshl_add_u64 v[52:53], v[140:141], 0, s[42:43]
	global_load_dwordx4 v[54:57], v[50:51], off
	s_nop 0
	global_load_dwordx4 v[50:53], v[52:53], off
	s_cmp_lt_i32 s9, 0
	s_cselect_b64 s[10:11], -1, 0
	s_cmp_gt_i32 s9, s13
	s_cselect_b64 s[14:15], -1, 0
	s_add_i32 s9, s9, 63
	s_cmp_lt_i32 s9, s12
	s_cselect_b64 s[16:17], -1, 0
	s_or_b64 s[10:11], s[10:11], s[16:17]
	s_or_b64 s[10:11], s[10:11], s[14:15]
	s_and_b64 vcc, exec, s[10:11]
	s_waitcnt lgkmcnt(0)
	s_barrier
	s_cbranch_vccnz .LBB0_1046
	v_add_u32_e32 v58, v143, v147
	ds_read_b128 v[90:93], v58
	v_add_u32_e32 v59, v143, v148
	ds_read_b128 v[94:97], v59
	ds_read_b128 v[98:101], v58 offset:2048
	ds_read_b128 v[102:105], v59 offset:2048
	ds_read_b128 v[106:109], v58 offset:4096
	ds_read_b128 v[110:113], v59 offset:4096
	ds_read_b128 v[114:117], v58 offset:6144
	ds_read_b128 v[118:121], v59 offset:6144
	ds_read_b128 v[86:89], v58 offset:8192
	ds_read_b128 v[82:85], v58 offset:10240
	ds_read_b128 v[78:81], v58 offset:12288
	ds_read_b128 v[74:77], v58 offset:14336
	ds_read_b128 v[70:73], v59 offset:8192
	ds_read_b128 v[66:69], v59 offset:10240
	ds_read_b128 v[62:65], v59 offset:12288
	ds_read_b128 v[58:61], v59 offset:14336
	s_waitcnt lgkmcnt(13)
	v_mfma_f32_16x16x32_bf16 v[164:167], v[98:101], v[42:45], 0
	s_waitcnt lgkmcnt(12)
	v_mfma_f32_16x16x32_bf16 v[164:167], v[102:105], v[46:49], v[164:167]
	v_mfma_f32_16x16x32_bf16 v[158:161], v[90:93], v[42:45], 0
	v_mfma_f32_16x16x32_bf16 v[160:163], v[94:97], v[46:49], v[158:161]
	s_waitcnt lgkmcnt(11)
	v_mfma_f32_16x16x32_bf16 v[168:171], v[106:109], v[42:45], 0
	s_nop 4
	v_add_u32_e32 v158, s8, v152
	v_add_u32_e32 v159, 0x207fc, v158
	ds_read2_b32 v[176:177], v159 offset1:1
	s_waitcnt lgkmcnt(11)
	v_mfma_f32_16x16x32_bf16 v[168:171], v[110:113], v[46:49], v[168:171]
	s_waitcnt lgkmcnt(0)
	v_add_f32_e32 v159, v160, v176
	v_add_f32_e32 v160, v161, v177
	v_add_u32_e32 v161, 0x20804, v158
	ds_read2_b32 v[176:177], v161 offset1:1
	v_mfma_f32_16x16x32_bf16 v[172:175], v[114:117], v[42:45], 0
	s_waitcnt lgkmcnt(0)
	v_add_f32_e32 v161, v162, v176
	v_add_f32_e32 v162, v163, v177
	v_add_u32_e32 v163, 0x2083c, v158
	ds_read2_b32 v[176:177], v163 offset1:1
	v_mfma_f32_16x16x32_bf16 v[172:175], v[118:121], v[46:49], v[172:175]
	s_waitcnt lgkmcnt(0)
	v_add_f32_e32 v163, v164, v176
	v_add_f32_e32 v164, v165, v177
	v_add_u32_e32 v165, 0x20844, v158
	ds_read2_b32 v[176:177], v165 offset1:1
	s_waitcnt lgkmcnt(0)
	v_add_f32_e32 v165, v166, v176
	v_add_f32_e32 v166, v167, v177
	v_add_u32_e32 v167, 0x2087c, v158
	ds_read2_b32 v[176:177], v167 offset1:1
	s_waitcnt lgkmcnt(0)
	v_add_f32_e32 v167, v168, v176
	v_add_f32_e32 v168, v169, v177
	v_add_u32_e32 v169, 0x20884, v158
	ds_read2_b32 v[176:177], v169 offset1:1
	s_waitcnt lgkmcnt(0)
	v_add_f32_e32 v169, v170, v176
	v_add_f32_e32 v170, v171, v177
	v_add_u32_e32 v171, 0x208bc, v158
	ds_read2_b32 v[176:177], v171 offset1:1
	s_waitcnt lgkmcnt(0)
	v_add_f32_e32 v171, v172, v176
	v_add_f32_e32 v172, v173, v177
	v_add_u32_e32 v173, 0x208c4, v158
	ds_read2_b32 v[176:177], v173 offset1:1
	s_waitcnt lgkmcnt(0)
	v_add_f32_e32 v173, v174, v176
	v_add_f32_e32 v174, v175, v177
	v_max_f32_e32 v175, v159, v160
	v_max3_f32 v175, v175, v161, v162
	v_max3_f32 v175, v175, v163, v164
	v_max3_f32 v175, v175, v165, v166
	v_max3_f32 v175, v175, v167, v168
	v_max3_f32 v175, v175, v169, v170
	v_max3_f32 v175, v175, v171, v172
	v_max3_f32 v175, v175, v173, v174
	v_add_f32_e32 v176, 0x40c00000, v157
	v_cmp_gt_f32_e32 vcc, v175, v176
	s_cbranch_vccz .LBB0_1050
	v_add_f32_e32 v175, 0, v175
	ds_bpermute_b32 v176, v144, v175
	s_waitcnt lgkmcnt(0)
	v_max_f32_e32 v176, v176, v176
	v_max_f32_e32 v175, v175, v176
	ds_bpermute_b32 v176, v145, v175
	s_waitcnt lgkmcnt(0)
	v_max3_f32 v175, v157, v175, v176
	v_sub_f32_e32 v157, v157, v175
	v_mul_f32_e32 v157, 0x3fb8aa3b, v157
	v_exp_f32_e32 v176, v157
	v_mov_b32_e32 v157, v175
	v_mul_f32_e32 v137, v137, v176
	v_pk_mul_f32 v[32:33], v[32:33], v[176:177] op_sel_hi:[1,0]
	v_pk_mul_f32 v[30:31], v[30:31], v[176:177] op_sel_hi:[1,0]
	v_pk_mul_f32 v[28:29], v[28:29], v[176:177] op_sel_hi:[1,0]
	v_pk_mul_f32 v[26:27], v[26:27], v[176:177] op_sel_hi:[1,0]
	v_pk_mul_f32 v[24:25], v[24:25], v[176:177] op_sel_hi:[1,0]
	v_pk_mul_f32 v[22:23], v[22:23], v[176:177] op_sel_hi:[1,0]
	v_pk_mul_f32 v[20:21], v[20:21], v[176:177] op_sel_hi:[1,0]
	v_pk_mul_f32 v[18:19], v[18:19], v[176:177] op_sel_hi:[1,0]
;     ...
;                         for (int kt = 0; kt < 4; ++kt) { sc[kt] = (f32x4){0.f, 0.f, 0.f, 0.f};
; #pragma unroll
;                             for (int ks = 0; ks < 2; ++ks) { const bf16x8 ak = (MODE != 3) ? akf[kt][ks] : akq[kt][ks];
;                                 sc[kt] = __builtin_amdgcn_mfma_f32_16x16x32_bf16(ak, Bq[qd][ks], sc[kt], 0, 0, 0); } }
;                         if (MODE == 3) {
; #pragma unroll
;                             for (int st = 0; st < 2; ++st)
; #pragma unroll
;                                 for (int dt = 0; dt < 4; ++dt) avq[st][dt] = *(const LAS bf16x8*)(L + LV + (16 * dt + n) * 128 + ((((4 * st + q) ^ n) & 7) << 4));
;                             __builtin_amdgcn_sched_barrier(0);
;                         }
;                         if (!far) {
;                             const LAS float* tp = (MODE == 2) ? biasd + hr * NT + (DOFF - tq + 31 + 16 * p0) + 64 * q : biasd + hr * NT + (DOFF - tq + p0) + 4 * q;
; #pragma unroll
;                             for (int kt = 0; kt < 4; ++kt)
; #pragma unroll
;                                 for (int r = 0; r < 4; ++r) sc[kt][r] += (MODE == 3) ? bia[kt][r] : ((MODE == 2) ? tp[256 * kt + 16 * r] : tp[16 * kt + r]);
;                         }
;                         const float bshift = far ? bfar : 0.f, boff = bshift * 1.4426950408889634f;
;                         float mx;
;                         { float m = fmaxf(fmaxf(sc[0][0], sc[0][1]), sc[0][2]);
;                           m = fmaxf(fmaxf(m, sc[0][3]), sc[1][0]); m = fmaxf(fmaxf(m, sc[1][1]), sc[1][2]); m = fmaxf(fmaxf(m, sc[1][3]), sc[2][0]);
;                           m = fmaxf(fmaxf(m, sc[2][1]), sc[2][2]); m = fmaxf(fmaxf(m, sc[2][3]), sc[3][0]); m = fmaxf(fmaxf(m, sc[3][1]), sc[3][2]); mx = fmaxf(m, sc[3][3]) + bshift; }
;                         if (MODE == 3 && !colsel) mx = -1e30f;
;                         float p[4][4];
;                         constexpr float L2E = 1.4426950408889634f;
;                         if (MODE == 2 && pass == 1) {
;                             const float negm1 = (mrun[qd] < -1e29f ? 0.f : -mrun[qd] * L2E) + boff + linv[qd];
; #pragma unroll
;                             for (int kt = 0; kt < 4; ++kt)
; #pragma unroll
;                                 for (int r = 0; r < 4; ++r) p[kt][r] = __builtin_amdgcn_exp2f(__builtin_fmaf(sc[kt][r], L2E, negm1));
.LBB0_1050:
	v_mfma_f32_16x16x32_bf16 v[90:93], v[90:93], v[34:37], 0
	v_fma_f32 v175, v157, s24, 0
	v_cmp_ngt_f32_e32 vcc, s30, v157
	v_mfma_f32_16x16x32_bf16 v[92:95], v[94:97], v[38:41], v[90:93]
	s_nop 0
	v_cndmask_b32_e32 v175, 0, v175, vcc
	v_fmamk_f32 v159, v159, 0x3fb8aa3b, v175
	v_fmamk_f32 v160, v160, 0x3fb8aa3b, v175
	v_mfma_f32_16x16x32_bf16 v[96:99], v[98:101], v[34:37], 0
	v_add_u32_e32 v90, 0x207ec, v158
	v_fmamk_f32 v161, v161, 0x3fb8aa3b, v175
	v_fmamk_f32 v162, v162, 0x3fb8aa3b, v175
	v_mfma_f32_16x16x32_bf16 v[98:101], v[102:105], v[38:41], v[96:99]
	v_fmamk_f32 v163, v163, 0x3fb8aa3b, v175
	v_fmamk_f32 v164, v164, 0x3fb8aa3b, v175
	v_fmamk_f32 v165, v165, 0x3fb8aa3b, v175
	s_nop 0
	ds_read2_b32 v[96:97], v90 offset1:1
	v_mfma_f32_16x16x32_bf16 v[102:105], v[106:109], v[34:37], 0
	v_fmamk_f32 v166, v166, 0x3fb8aa3b, v175
	v_exp_f32_e32 v159, v159
	v_exp_f32_e32 v160, v160
	s_waitcnt lgkmcnt(0)
	v_add_f32_e32 v91, v92, v96
	v_add_u32_e32 v92, 0x207f4, v158
	v_add_f32_e32 v90, v93, v97
	ds_read2_b32 v[96:97], v92 offset1:1
	v_mfma_f32_16x16x32_bf16 v[102:105], v[110:113], v[38:41], v[102:105]
	v_exp_f32_e32 v161, v161
	v_exp_f32_e32 v162, v162
	v_exp_f32_e32 v163, v163
	s_waitcnt lgkmcnt(0)
	v_add_f32_e32 v93, v94, v96
	v_add_u32_e32 v94, 0x2082c, v158
	v_add_f32_e32 v92, v95, v97
	ds_read2_b32 v[96:97], v94 offset1:1
	v_mfma_f32_16x16x32_bf16 v[106:109], v[114:117], v[34:37], 0
	v_exp_f32_e32 v164, v164
	v_exp_f32_e32 v165, v165
	v_exp_f32_e32 v166, v166
	s_waitcnt lgkmcnt(0)
	v_add_f32_e32 v95, v98, v96
	v_add_u32_e32 v96, 0x20834, v158
	v_add_f32_e32 v94, v99, v97
	ds_read2_b32 v[96:97], v96 offset1:1
	v_mfma_f32_16x16x32_bf16 v[106:109], v[118:121], v[38:41], v[106:109]
	v_fmamk_f32 v167, v167, 0x3fb8aa3b, v175
	v_fmamk_f32 v168, v168, 0x3fb8aa3b, v175
	v_fmamk_f32 v169, v169, 0x3fb8aa3b, v175
	s_waitcnt lgkmcnt(0)
	v_add_f32_e32 v99, v100, v96
	v_add_u32_e32 v96, 0x2086c, v158
	v_add_f32_e32 v98, v101, v97
	ds_read2_b32 v[96:97], v96 offset1:1
	v_fmamk_f32 v170, v170, 0x3fb8aa3b, v175
	v_fmamk_f32 v171, v171, 0x3fb8aa3b, v175
	v_fmamk_f32 v172, v172, 0x3fb8aa3b, v175
	v_fmamk_f32 v173, v173, 0x3fb8aa3b, v175
	s_waitcnt lgkmcnt(0)
	v_add_f32_e32 v101, v102, v96
	v_add_u32_e32 v96, 0x20874, v158
	v_add_f32_e32 v100, v103, v97
	ds_read2_b32 v[96:97], v96 offset1:1
	v_fmac_f32_e32 v175, 0x3fb8aa3b, v174
	v_exp_f32_e32 v167, v167
	v_exp_f32_e32 v168, v168
	v_exp_f32_e32 v169, v169
	s_waitcnt lgkmcnt(0)
	v_add_f32_e32 v103, v104, v96
	v_add_u32_e32 v96, 0x208ac, v158
	v_add_f32_e32 v102, v105, v97
	ds_read2_b32 v[104:105], v96 offset1:1
	v_exp_f32_e32 v170, v170
	v_exp_f32_e32 v171, v171
	v_exp_f32_e32 v172, v172
	v_exp_f32_e32 v173, v173
	s_waitcnt lgkmcnt(0)
	v_add_f32_e32 v97, v106, v104
	v_add_u32_e32 v104, 0x208b4, v158
	v_add_f32_e32 v96, v107, v105
	ds_read2_b32 v[106:107], v104 offset1:1
	v_exp_f32_e32 v174, v175
	v_cvt_pk_bf16_f32 v180, v159, v160
	v_cvt_pk_bf16_f32 v181, v161, v162
	v_cvt_pk_bf16_f32 v182, v163, v164
	v_cvt_pk_bf16_f32 v183, v165, v166
	s_waitcnt lgkmcnt(0)
	v_add_f32_e32 v105, v108, v106
	v_max_f32_e32 v106, v91, v90
	v_mfma_f32_16x16x32_bf16 v[30:33], v[86:89], v[180:183], v[30:33]
	v_max3_f32 v106, v106, v93, v92
	v_max3_f32 v106, v106, v95, v94
	v_max3_f32 v106, v106, v99, v98
	v_mfma_f32_16x16x32_bf16 v[26:29], v[82:85], v[180:183], v[26:29]
	v_max3_f32 v106, v106, v101, v100
	v_max3_f32 v106, v106, v103, v102
	v_add_f32_e32 v104, v109, v107
	v_mfma_f32_16x16x32_bf16 v[22:25], v[78:81], v[180:183], v[22:25]
	v_max3_f32 v106, v106, v97, v96
	v_max3_f32 v106, v106, v105, v104
	v_add_f32_e32 v107, 0x40c00000, v131
	v_mfma_f32_16x16x32_bf16 v[18:21], v[74:77], v[180:183], v[18:21]
	v_cvt_pk_bf16_f32 v180, v167, v168
	v_cvt_pk_bf16_f32 v181, v169, v170
	v_cvt_pk_bf16_f32 v182, v171, v172
	v_cvt_pk_bf16_f32 v183, v173, v174
	v_cmp_gt_f32_e32 vcc, v106, v107
	s_nop 0
	v_mfma_f32_16x16x32_bf16 v[30:33], v[70:73], v[180:183], v[30:33]
	v_mfma_f32_16x16x32_bf16 v[26:29], v[66:69], v[180:183], v[26:29]
	v_mfma_f32_16x16x32_bf16 v[22:25], v[62:65], v[180:183], v[22:25]
	v_mfma_f32_16x16x32_bf16 v[18:21], v[58:61], v[180:183], v[18:21]
	s_cbranch_vccz .LBB0_1045
	v_add_f32_e32 v106, 0, v106
	ds_bpermute_b32 v107, v144, v106
	s_waitcnt lgkmcnt(0)
	v_max_f32_e32 v107, v107, v107
	v_max_f32_e32 v106, v106, v107
	ds_bpermute_b32 v107, v145, v106
	s_waitcnt lgkmcnt(0)
	v_max3_f32 v107, v131, v106, v107
	v_sub_f32_e32 v106, v131, v107
	v_mul_f32_e32 v106, 0x3fb8aa3b, v106
	v_exp_f32_e32 v106, v106
	v_mov_b32_e32 v131, v107
	v_mul_f32_e32 v136, v136, v106
	v_pk_mul_f32 v[16:17], v[16:17], v[106:107] op_sel_hi:[1,0]
	v_pk_mul_f32 v[14:15], v[14:15], v[106:107] op_sel_hi:[1,0]
	v_pk_mul_f32 v[12:13], v[12:13], v[106:107] op_sel_hi:[1,0]
	v_pk_mul_f32 v[10:11], v[10:11], v[106:107] op_sel_hi:[1,0]
	v_pk_mul_f32 v[8:9], v[8:9], v[106:107] op_sel_hi:[1,0]
	v_pk_mul_f32 v[6:7], v[6:7], v[106:107] op_sel_hi:[1,0]
	v_pk_mul_f32 v[4:5], v[4:5], v[106:107] op_sel_hi:[1,0]
	v_pk_mul_f32 v[2:3], v[2:3], v[106:107] op_sel_hi:[1,0]
	s_branch .LBB0_1045
;     ...
;                             float negm = (mrun[qd] < -1e29f ? 0.f : -mrun[qd] * L2E) + boff; float ps = 0.f;
;                             if (MODE == 3 && !colsel) negm = -__builtin_inff();
; #pragma unroll
;                             for (int kt = 0; kt < 4; ++kt)
; #pragma unroll
;                                 for (int r = 0; r < 4; ++r) { p[kt][r] = (DBG == 2) ? sc[kt][r] + negm : __builtin_amdgcn_exp2f(__builtin_fmaf(sc[kt][r], L2E, negm)); ps += p[kt][r]; }
;                             lrun[qd] += ps;
;                         }
;                         if (MODE == 2 && pass == 1) {
;                             float base[4], im3[4], rot[4];
; #pragma unroll
;                             for (int kt = 0; kt < 4; ++kt) { float im[4];
; #pragma unroll
;                                 for (int r = 0; r < 4; ++r) { float v = p[kt][r]; v += dpp_xor1(v); v += dpp_xor2(v); im[r] = v; }
;                                 base[kt] = 2.0f * (im[0] + im[1] + im[2]) + im[3]; im3[kt] = im[3]; }
; #pragma unroll
;                             for (int kt = 0; kt < 4; ++kt) rot[kt] = __shfl(im3[kt], (lane + 48) & 63);
; #pragma unroll
;                             for (int kt = 0; kt < 4; ++kt) { const float pv3 = q > 0 ? rot[kt] : (kt == 0 ? carry3[qd] : rot[kt > 0 ? kt - 1 : 0]);
;                                 const int jg = (p0 + 16 * kt + 4 * q) >> 2;
;                                 if (hr == 0 && jg < 256) sscore[(tq - t0) * SSTR + jg] = base[kt] + pv3; }
;                             carry3[qd] = rot[3];
;                         }
;                         if (do_pv && DBG != 1) {
; #pragma unroll
;                             for (int st = 0; st < 2; ++st) {
;                                 u32x4 pw; pw.x = pk2(p[2 * st][0], p[2 * st][1]); pw.y = pk2(p[2 * st][2], p[2 * st][3]); pw.z = pk2(p[2 * st + 1][0], p[2 * st + 1][1]); pw.w = pk2(p[2 * st + 1][2], p[2 * st + 1][3]);
;                                 const bf16x8 pf = __builtin_bit_cast(bf16x8, pw);
; #pragma unroll
;                                 for (int dt = 0; dt < 4; ++dt) { bf16x8 av;
;                                     if (MODE != 3) av = avf[st][dt]; else av = avq[st][dt];
;                                     O[qd][dt] = __builtin_amdgcn_mfma_f32_16x16x32_bf16(av, pf, O[qd][dt], 0, 0, 0); } }
.Lw2_1045:
	v_add_f32_e32 v106, 0, v159
	v_add_f32_e32 v106, v160, v106
	v_add_f32_e32 v106, v161, v106
	v_add_f32_e32 v106, v162, v106
	v_add_f32_e32 v106, v163, v106
	v_add_f32_e32 v106, v164, v106
	v_add_f32_e32 v106, v165, v106
	v_add_f32_e32 v106, v166, v106
	v_add_f32_e32 v106, v167, v106
	v_add_f32_e32 v106, v168, v106
	v_add_f32_e32 v106, v169, v106
	v_add_f32_e32 v106, v170, v106
	v_add_f32_e32 v106, v171, v106
	v_add_f32_e32 v106, v172, v106
	v_add_f32_e32 v106, v173, v106
	v_add_f32_e32 v106, v174, v106
	v_add_f32_e32 v137, v137, v106
	v_fma_f32 v106, v131, s24, 0
	v_cmp_ngt_f32_e32 vcc, s30, v131
	s_nop 1
	v_cndmask_b32_e32 v106, 0, v106, vcc
	v_fmamk_f32 v91, v91, 0x3fb8aa3b, v106
	v_exp_f32_e32 v91, v91
	v_fmamk_f32 v90, v90, 0x3fb8aa3b, v106
	v_exp_f32_e32 v90, v90
	v_fmamk_f32 v93, v93, 0x3fb8aa3b, v106
	v_exp_f32_e32 v93, v93
	v_fmamk_f32 v92, v92, 0x3fb8aa3b, v106
	v_fmamk_f32 v95, v95, 0x3fb8aa3b, v106
	v_fmamk_f32 v94, v94, 0x3fb8aa3b, v106
	v_fmamk_f32 v99, v99, 0x3fb8aa3b, v106
	v_fmamk_f32 v98, v98, 0x3fb8aa3b, v106
	v_exp_f32_e32 v92, v92
	v_exp_f32_e32 v95, v95
	v_exp_f32_e32 v94, v94
	v_exp_f32_e32 v99, v99
	v_exp_f32_e32 v98, v98
	v_add_f32_e32 v107, 0, v91
	v_add_f32_e32 v107, v90, v107
	v_add_f32_e32 v107, v93, v107
	v_add_f32_e32 v107, v92, v107
	v_cvt_pk_bf16_f32 v90, v91, v90
	v_cvt_pk_bf16_f32 v91, v93, v92
	v_cvt_pk_bf16_f32 v92, v95, v94
	v_cvt_pk_bf16_f32 v93, v99, v98
	v_fmamk_f32 v101, v101, 0x3fb8aa3b, v106
	v_fmamk_f32 v100, v100, 0x3fb8aa3b, v106
	v_fmamk_f32 v103, v103, 0x3fb8aa3b, v106
	v_fmamk_f32 v102, v102, 0x3fb8aa3b, v106
	v_mfma_f32_16x16x32_bf16 v[14:17], v[86:89], v[90:93], v[14:17]
	v_fmamk_f32 v87, v97, 0x3fb8aa3b, v106
	v_exp_f32_e32 v101, v101
	v_exp_f32_e32 v100, v100
	v_mfma_f32_16x16x32_bf16 v[10:13], v[82:85], v[90:93], v[10:13]
	v_fmamk_f32 v82, v96, 0x3fb8aa3b, v106
	v_fmamk_f32 v83, v105, 0x3fb8aa3b, v106
	v_fmac_f32_e32 v106, 0x3fb8aa3b, v104
	v_exp_f32_e32 v103, v103
	v_exp_f32_e32 v86, v102
	v_exp_f32_e32 v87, v87
	v_exp_f32_e32 v82, v82
	v_mfma_f32_16x16x32_bf16 v[6:9], v[78:81], v[90:93], v[6:9]
	v_exp_f32_e32 v78, v83
	v_exp_f32_e32 v79, v106
	v_add_f32_e32 v107, v95, v107
	v_add_f32_e32 v107, v94, v107
	v_add_f32_e32 v107, v99, v107
	v_add_f32_e32 v107, v98, v107
	v_mfma_f32_16x16x32_bf16 v[2:5], v[74:77], v[90:93], v[2:5]
	v_cvt_pk_bf16_f32 v74, v101, v100
	v_cvt_pk_bf16_f32 v75, v103, v86
	v_cvt_pk_bf16_f32 v76, v87, v82
	v_cvt_pk_bf16_f32 v77, v78, v79
	s_nop 1
	v_mfma_f32_16x16x32_bf16 v[14:17], v[70:73], v[74:77], v[14:17]
	v_add_f32_e32 v70, v101, v107
	v_add_f32_e32 v70, v100, v70
	v_add_f32_e32 v70, v103, v70
	v_mfma_f32_16x16x32_bf16 v[10:13], v[66:69], v[74:77], v[10:13]
	v_add_f32_e32 v66, v86, v70
	v_add_f32_e32 v66, v87, v66
	v_add_f32_e32 v66, v82, v66
	v_mfma_f32_16x16x32_bf16 v[6:9], v[62:65], v[74:77], v[6:9]
	v_add_f32_e32 v62, v78, v66
	v_add_f32_e32 v62, v79, v62
	v_add_f32_e32 v136, v136, v62
	v_mfma_f32_16x16x32_bf16 v[2:5], v[58:61], v[74:77], v[2:5]
.Lw2_1046:
	s_addk_i32 s8, 0x100
	s_cmpk_eq_i32 s8, 0x800
	s_cbranch_scc1 .LBB0_1052
	s_branch .LBB0_1047
;     ...
;             const unsigned kthr = (unsigned)(c.tid >> 3) * (unsigned)kstride + (unsigned)(c.tid & 7) * 8u, vthr = (unsigned)(c.tid >> 3) * (unsigned)vstride + (unsigned)(c.tid & 7) * 8u;
;             int st_k, st_va;
;             { const int row = c.tid >> 3, cj = c.tid & 7, ga = 2 * cj;
;               st_k = row * 128 + (((cj ^ row) & 7) << 4);
;               st_va = row * 128 + (((((ga >> 3) * 4 + (ga & 3)) ^ row) & 7) << 4) + ((ga >> 2) & 1) * 8; }
;             u32x4 kreg[TS], vreg[TS]; int p0n[TS];
;             const int nrounds = (ntiles + TS - 1) / TS;
;             if (nrounds > 0) AT_ISSUE(0);
;             if (pass == 0) {
;                 for (int e = c.tid; e < 4 * NT; e += 512) { const int r = e / NT, dist = DOFF - (e - r * NT); const bool vis = dist >= 0 && (MODE != 0 || dist < 128) && (MODE != 1 || dist < 512);
;                     biasd[e] = vis ? reltab[t5_bucket(dist > 1023 ? 1023 : dist) * 16 + (MODE == 0 ? 8 : 0) + g * 4 + r] : -1e30f; } }
;             for (int rd = 0; rd < nrounds; ++rd) {
;                 int p0s[TS];
; #pragma unroll
;                 for (int i = 0; i < TS; ++i) p0s[i] = p0n[i];
;                 __syncthreads();
; #pragma unroll
;                 for (int i = 0; i < TS; ++i) {
;                     *(LAS u32x4*)(L + AT_K + i * AT_TS + st_k) = kreg[i];
;                     if (do_pv) { const u32x2 lo = {vreg[i].x, vreg[i].y}, hi = {vreg[i].z, vreg[i].w};
;                         *(LAS u32x2*)(L + AT_V + i * AT_TS + st_va) = lo; *(LAS u32x2*)(L + AT_V + i * AT_TS + (st_va ^ 16)) = hi; } }
;                 if (rd + 1 < nrounds) AT_ISSUE(rd + 1);
;                 __syncthreads();
;     ...
;                         for (int kt = 0; kt < 4; ++kt) { sc[kt] = (f32x4){0.f, 0.f, 0.f, 0.f};
; #pragma unroll
;                             for (int ks = 0; ks < 2; ++ks) { const bf16x8 ak = (MODE != 3) ? akf[kt][ks] : akq[kt][ks];
;                                 sc[kt] = __builtin_amdgcn_mfma_f32_16x16x32_bf16(ak, Bq[qd][ks], sc[kt], 0, 0, 0); } }
;                         if (MODE == 3) {
; #pragma unroll
;                             for (int st = 0; st < 2; ++st)
; #pragma unroll
;                                 for (int dt = 0; dt < 4; ++dt) avq[st][dt] = *(const LAS bf16x8*)(L + LV + (16 * dt + n) * 128 + ((((4 * st + q) ^ n) & 7) << 4));
;                             __builtin_amdgcn_sched_barrier(0);
.Lw2_1047:
	s_mov_b32 s9, s7
	s_add_i32 s7, s7, 64
	s_cmpk_eq_i32 s8, 0x700
	s_cselect_b32 s10, 0, 64
	s_add_i32 s42, s7, s10
	s_max_i32 s42, s42, 0
	s_lshl_b64 s[10:11], s[42:43], 13
	s_lshl_b32 s42, s42, 1
	s_waitcnt lgkmcnt(0)
	s_barrier
	s_waitcnt vmcnt(3)
	ds_write_b128 v153, v[204:207]
	s_waitcnt vmcnt(2)
	ds_write_b64 v154, v[200:201] offset:8192
	ds_write_b64 v155, v[202:203] offset:8192
	v_lshl_add_u64 v[200:201], v[138:139], 0, s[10:11]
	v_lshl_add_u64 v[202:203], v[140:141], 0, s[42:43]
	global_load_dwordx4 v[204:207], v[200:201], off
	s_nop 0
	global_load_dwordx4 v[200:203], v[202:203], off
	s_cmp_lt_i32 s9, 0
	s_cselect_b64 s[10:11], -1, 0
	s_cmp_gt_i32 s9, s13
	s_cselect_b64 s[14:15], -1, 0
	s_add_i32 s9, s9, 63
	s_cmp_lt_i32 s9, s12
	s_cselect_b64 s[16:17], -1, 0
	s_or_b64 s[10:11], s[10:11], s[16:17]
	s_or_b64 s[10:11], s[10:11], s[14:15]
	s_and_b64 vcc, exec, s[10:11]
	s_waitcnt lgkmcnt(0)
	s_barrier
	s_cbranch_vccnz .Lw2_1046
	v_add_u32_e32 v58, v143, v147
	ds_read_b128 v[90:93], v58
	v_add_u32_e32 v59, v143, v148
	ds_read_b128 v[94:97], v59
	ds_read_b128 v[98:101], v58 offset:2048
	ds_read_b128 v[102:105], v59 offset:2048
	ds_read_b128 v[106:109], v58 offset:4096
	ds_read_b128 v[110:113], v59 offset:4096
	ds_read_b128 v[114:117], v58 offset:6144
	ds_read_b128 v[118:121], v59 offset:6144
	ds_read_b128 v[86:89], v58 offset:8192
	ds_read_b128 v[82:85], v58 offset:10240
	ds_read_b128 v[78:81], v58 offset:12288
	ds_read_b128 v[74:77], v58 offset:14336
	ds_read_b128 v[70:73], v59 offset:8192
	ds_read_b128 v[66:69], v59 offset:10240
	ds_read_b128 v[62:65], v59 offset:12288
	ds_read_b128 v[58:61], v59 offset:14336
	s_waitcnt lgkmcnt(13)
	v_mfma_f32_16x16x32_bf16 v[164:167], v[98:101], v[42:45], 0
	s_waitcnt lgkmcnt(12)
	v_mfma_f32_16x16x32_bf16 v[164:167], v[102:105], v[46:49], v[164:167]
	v_mfma_f32_16x16x32_bf16 v[158:161], v[90:93], v[42:45], 0
	v_mfma_f32_16x16x32_bf16 v[160:163], v[94:97], v[46:49], v[158:161]
	s_waitcnt lgkmcnt(11)
	v_mfma_f32_16x16x32_bf16 v[168:171], v[106:109], v[42:45], 0
	s_nop 4
	v_add_u32_e32 v158, s8, v152
	v_add_u32_e32 v159, 0x207fc, v158
	ds_read2_b32 v[176:177], v159 offset1:1
	s_waitcnt lgkmcnt(11)
	v_mfma_f32_16x16x32_bf16 v[168:171], v[110:113], v[46:49], v[168:171]
	s_waitcnt lgkmcnt(0)
	v_add_f32_e32 v159, v160, v176
	v_add_f32_e32 v160, v161, v177
	v_add_u32_e32 v161, 0x20804, v158
	ds_read2_b32 v[176:177], v161 offset1:1
	v_mfma_f32_16x16x32_bf16 v[172:175], v[114:117], v[42:45], 0
	s_waitcnt lgkmcnt(0)
	v_add_f32_e32 v161, v162, v176
	v_add_f32_e32 v162, v163, v177
	v_add_u32_e32 v163, 0x2083c, v158
	ds_read2_b32 v[176:177], v163 offset1:1
	v_mfma_f32_16x16x32_bf16 v[172:175], v[118:121], v[46:49], v[172:175]
	s_waitcnt lgkmcnt(0)
	v_add_f32_e32 v163, v164, v176
	v_add_f32_e32 v164, v165, v177
	v_add_u32_e32 v165, 0x20844, v158
	ds_read2_b32 v[176:177], v165 offset1:1
	s_waitcnt lgkmcnt(0)
	v_add_f32_e32 v165, v166, v176
	v_add_f32_e32 v166, v167, v177
	v_add_u32_e32 v167, 0x2087c, v158
	ds_read2_b32 v[176:177], v167 offset1:1
	s_waitcnt lgkmcnt(0)
	v_add_f32_e32 v167, v168, v176
	v_add_f32_e32 v168, v169, v177
	v_add_u32_e32 v169, 0x20884, v158
	ds_read2_b32 v[176:177], v169 offset1:1
	s_waitcnt lgkmcnt(0)
	v_add_f32_e32 v169, v170, v176
	v_add_f32_e32 v170, v171, v177
	v_add_u32_e32 v171, 0x208bc, v158
	ds_read2_b32 v[176:177], v171 offset1:1
	s_waitcnt lgkmcnt(0)
	v_add_f32_e32 v171, v172, v176
	v_add_f32_e32 v172, v173, v177
	v_add_u32_e32 v173, 0x208c4, v158
	ds_read2_b32 v[176:177], v173 offset1:1
	s_waitcnt lgkmcnt(0)
	v_add_f32_e32 v173, v174, v176
	v_add_f32_e32 v174, v175, v177
	v_max_f32_e32 v175, v159, v160
	v_max3_f32 v175, v175, v161, v162
	v_max3_f32 v175, v175, v163, v164
	v_max3_f32 v175, v175, v165, v166
	v_max3_f32 v175, v175, v167, v168
	v_max3_f32 v175, v175, v169, v170
	v_max3_f32 v175, v175, v171, v172
	v_max3_f32 v175, v175, v173, v174
	v_add_f32_e32 v176, 0x40c00000, v157
	v_cmp_gt_f32_e32 vcc, v175, v176
	s_cbranch_vccz .Lw2_1050
	v_add_f32_e32 v175, 0, v175
	ds_bpermute_b32 v176, v144, v175
	s_waitcnt lgkmcnt(0)
	v_max_f32_e32 v176, v176, v176
	v_max_f32_e32 v175, v175, v176
	ds_bpermute_b32 v176, v145, v175
	s_waitcnt lgkmcnt(0)
	v_max3_f32 v175, v157, v175, v176
	v_sub_f32_e32 v157, v157, v175
	v_mul_f32_e32 v157, 0x3fb8aa3b, v157
	v_exp_f32_e32 v176, v157
	v_mov_b32_e32 v157, v175
	v_mul_f32_e32 v137, v137, v176
	v_pk_mul_f32 v[32:33], v[32:33], v[176:177] op_sel_hi:[1,0]
	v_pk_mul_f32 v[30:31], v[30:31], v[176:177] op_sel_hi:[1,0]
	v_pk_mul_f32 v[28:29], v[28:29], v[176:177] op_sel_hi:[1,0]
	v_pk_mul_f32 v[26:27], v[26:27], v[176:177] op_sel_hi:[1,0]
	v_pk_mul_f32 v[24:25], v[24:25], v[176:177] op_sel_hi:[1,0]
	v_pk_mul_f32 v[22:23], v[22:23], v[176:177] op_sel_hi:[1,0]
	v_pk_mul_f32 v[20:21], v[20:21], v[176:177] op_sel_hi:[1,0]
	v_pk_mul_f32 v[18:19], v[18:19], v[176:177] op_sel_hi:[1,0]

;     ...
;                 __syncthreads();
; #pragma unroll
;                 for (int i = 0; i < TS; ++i) {
;                     *(LAS u32x4*)(L + AT_K + i * AT_TS + st_k) = kreg[i];
;                     if (do_pv) { const u32x2 lo = {vreg[i].x, vreg[i].y}, hi = {vreg[i].z, vreg[i].w};
;                         *(LAS u32x2*)(L + AT_V + i * AT_TS + st_va) = lo; *(LAS u32x2*)(L + AT_V + i * AT_TS + (st_va ^ 16)) = hi; } }
;                 if (rd + 1 < nrounds) AT_ISSUE(rd + 1);
;                 __syncthreads();
;     ...
;                         for (int kt = 0; kt < 4; ++kt) { sc[kt] = (f32x4){0.f, 0.f, 0.f, 0.f};
; #pragma unroll
;                             for (int ks = 0; ks < 2; ++ks) { const bf16x8 ak = (MODE != 3) ? akf[kt][ks] : akq[kt][ks];
;                                 sc[kt] = __builtin_amdgcn_mfma_f32_16x16x32_bf16(ak, Bq[qd][ks], sc[kt], 0, 0, 0); } }
;                         if (MODE == 3) {
; #pragma unroll
;                             for (int st = 0; st < 2; ++st)
; #pragma unroll
;                                 for (int dt = 0; dt < 4; ++dt) avq[st][dt] = *(const LAS bf16x8*)(L + LV + (16 * dt + n) * 128 + ((((4 * st + q) ^ n) & 7) << 4));
;                             __builtin_amdgcn_sched_barrier(0);
;                         }
;                         if (!far) {
;                             const LAS float* tp = (MODE == 2) ? biasd + hr * NT + (DOFF - tq + 31 + 16 * p0) + 64 * q : biasd + hr * NT + (DOFF - tq + p0) + 4 * q;
; #pragma unroll
;                             for (int kt = 0; kt < 4; ++kt)
; #pragma unroll
;                                 for (int r = 0; r < 4; ++r) sc[kt][r] += (MODE == 3) ? bia[kt][r] : ((MODE == 2) ? tp[256 * kt + 16 * r] : tp[16 * kt + r]);
;                         }
;                         const float bshift = far ? bfar : 0.f, boff = bshift * 1.4426950408889634f;
;                         float mx;
;                         { float m = fmaxf(fmaxf(sc[0][0], sc[0][1]), sc[0][2]);
;                           m = fmaxf(fmaxf(m, sc[0][3]), sc[1][0]); m = fmaxf(fmaxf(m, sc[1][1]), sc[1][2]); m = fmaxf(fmaxf(m, sc[1][3]), sc[2][0]);
;                           m = fmaxf(fmaxf(m, sc[2][1]), sc[2][2]); m = fmaxf(fmaxf(m, sc[2][3]), sc[3][0]); m = fmaxf(fmaxf(m, sc[3][1]), sc[3][2]); mx = fmaxf(m, sc[3][3]) + bshift; }
;                         if (MODE == 3 && !colsel) mx = -1e30f;
.LBB0_1052:
	s_cmp_lt_i32 s7, 0
	s_cselect_b64 s[8:9], -1, 0
	s_cmp_gt_i32 s7, s13
	s_cselect_b64 s[10:11], -1, 0
	s_or_b32 s13, s7, 63
	s_cmp_lt_i32 s13, s12
	s_cselect_b64 s[12:13], -1, 0
	s_or_b64 s[8:9], s[8:9], s[12:13]
	s_or_b64 s[8:9], s[8:9], s[10:11]
	s_and_b64 vcc, exec, s[8:9]
	s_barrier
	s_waitcnt vmcnt(3)
	ds_write_b128 v153, v[54:57]
	s_waitcnt vmcnt(2)
	ds_write_b64 v154, v[50:51] offset:8192
	ds_write_b64 v155, v[52:53] offset:8192
	s_waitcnt lgkmcnt(0)
	s_barrier
	s_cbranch_vccnz .LBB0_1034
	v_add_u32_e32 v50, v143, v147
	ds_read_b128 v[82:85], v50
	v_add_u32_e32 v51, v143, v148
	ds_read_b128 v[86:89], v51
	ds_read_b128 v[90:93], v50 offset:2048
	ds_read_b128 v[94:97], v51 offset:2048
	ds_read_b128 v[98:101], v50 offset:4096
	ds_read_b128 v[102:105], v51 offset:4096
	ds_read_b128 v[106:109], v50 offset:6144
	ds_read_b128 v[110:113], v51 offset:6144
	ds_read_b128 v[78:81], v50 offset:8192
	ds_read_b128 v[74:77], v50 offset:10240
	ds_read_b128 v[70:73], v50 offset:12288
	ds_read_b128 v[66:69], v50 offset:14336
	ds_read_b128 v[62:65], v51 offset:8192
	ds_read_b128 v[58:61], v51 offset:10240
	ds_read_b128 v[54:57], v51 offset:12288
	ds_read_b128 v[50:53], v51 offset:14336
	s_waitcnt lgkmcnt(13)
	v_mfma_f32_16x16x32_bf16 v[118:121], v[90:93], v[42:45], 0
	s_waitcnt lgkmcnt(11)
	v_mfma_f32_16x16x32_bf16 v[138:141], v[98:101], v[42:45], 0
	v_mfma_f32_16x16x32_bf16 v[114:117], v[82:85], v[42:45], 0
	s_waitcnt lgkmcnt(9)
	v_mfma_f32_16x16x32_bf16 v[42:45], v[106:109], v[42:45], 0
	s_waitcnt lgkmcnt(8)
	v_mfma_f32_16x16x32_bf16 v[158:161], v[110:113], v[46:49], v[42:45]
	v_mfma_f32_16x16x32_bf16 v[114:117], v[86:89], v[46:49], v[114:117]
	s_nop 4
	v_sub_u32_e32 v42, s7, v134
	v_lshl_add_u32 v162, v42, 2, v149
	v_add_u32_e32 v42, 0xffc, v162
	ds_read2_b32 v[42:43], v42 offset1:1
	v_add_u32_e32 v44, 0x1004, v162
	v_mfma_f32_16x16x32_bf16 v[118:121], v[94:97], v[46:49], v[118:121]
	ds_read2_b32 v[44:45], v44 offset1:1
	v_mfma_f32_16x16x32_bf16 v[138:141], v[102:105], v[46:49], v[138:141]
	v_add_u32_e32 v46, 0x103c, v162
	v_add_u32_e32 v48, 0x1044, v162
	ds_read2_b32 v[46:47], v46 offset1:1
	ds_read2_b32 v[48:49], v48 offset1:1
	s_waitcnt lgkmcnt(3)
	v_add_f32_e32 v42, v114, v42
	v_add_u32_e32 v114, 0x107c, v162
	v_add_f32_e32 v43, v115, v43
	ds_read2_b32 v[114:115], v114 offset1:1
	s_waitcnt lgkmcnt(3)
	v_add_f32_e32 v44, v116, v44
	v_add_u32_e32 v116, 0x1084, v162
	v_add_f32_e32 v45, v117, v45
	s_waitcnt lgkmcnt(2)
	v_add_f32_e32 v46, v118, v46
	s_waitcnt lgkmcnt(1)
	v_add_f32_e32 v48, v120, v48
	ds_read2_b32 v[116:117], v116 offset1:1
	v_add_u32_e32 v118, 0x10bc, v162
	v_add_u32_e32 v120, 0x10c4, v162
	v_add_f32_e32 v47, v119, v47
	v_add_f32_e32 v49, v121, v49
	ds_read2_b32 v[118:119], v118 offset1:1
	ds_read2_b32 v[120:121], v120 offset1:1
	s_waitcnt lgkmcnt(3)
	v_add_f32_e32 v114, v138, v114
	v_max_f32_e32 v138, v42, v43
	v_max3_f32 v138, v138, v44, v45
	v_max3_f32 v138, v138, v46, v47
	v_add_f32_e32 v115, v139, v115
	v_max3_f32 v138, v138, v48, v49
	s_waitcnt lgkmcnt(2)
	v_add_f32_e32 v116, v140, v116
	v_add_f32_e32 v117, v141, v117
	v_max3_f32 v138, v138, v114, v115
	s_waitcnt lgkmcnt(1)
	v_add_f32_e32 v118, v158, v118
	v_add_f32_e32 v119, v159, v119
	v_max3_f32 v138, v138, v116, v117
	s_waitcnt lgkmcnt(0)
	v_add_f32_e32 v120, v160, v120
	v_add_f32_e32 v121, v161, v121
	v_max3_f32 v138, v138, v118, v119
	v_max3_f32 v138, v138, v120, v121
	v_add_f32_e32 v139, 0x40c00000, v157
	v_cmp_gt_f32_e32 vcc, v138, v139
	s_cbranch_vccz .LBB0_1055
	v_add_f32_e32 v138, 0, v138
	ds_bpermute_b32 v139, v144, v138
	s_waitcnt lgkmcnt(0)
	v_max_f32_e32 v139, v139, v139
	v_max_f32_e32 v138, v138, v139
	ds_bpermute_b32 v139, v145, v138
	s_waitcnt lgkmcnt(0)
	v_max3_f32 v139, v157, v138, v139
	v_sub_f32_e32 v138, v157, v139
	v_mul_f32_e32 v138, 0x3fb8aa3b, v138
	v_exp_f32_e32 v138, v138
	v_mov_b32_e32 v157, v139
	v_mul_f32_e32 v137, v137, v138
	v_pk_mul_f32 v[32:33], v[32:33], v[138:139] op_sel_hi:[1,0]
	v_pk_mul_f32 v[30:31], v[30:31], v[138:139] op_sel_hi:[1,0]
	v_pk_mul_f32 v[28:29], v[28:29], v[138:139] op_sel_hi:[1,0]
	v_pk_mul_f32 v[26:27], v[26:27], v[138:139] op_sel_hi:[1,0]
	v_pk_mul_f32 v[24:25], v[24:25], v[138:139] op_sel_hi:[1,0]
	v_pk_mul_f32 v[22:23], v[22:23], v[138:139] op_sel_hi:[1,0]
	v_pk_mul_f32 v[20:21], v[20:21], v[138:139] op_sel_hi:[1,0]
	v_pk_mul_f32 v[18:19], v[18:19], v[138:139] op_sel_hi:[1,0]
